# A/B: mid-burst s_setprio 0/1 flip pairs removed from all GEMM K-loops (computing wave keeps priority through the 32-MFMA burst)
# speedup vs baseline: 1.0026x; 1.0004x over previous
; #define PG8_STAGE2(bufoff, gbase, v0, v1) do { \
;         __builtin_amdgcn_global_load_lds((const unsigned*)((const char*)(gbase) + (v0)), (LAS unsigned*)(lds + (bufoff) + ldsw), 16, 0, 0); \
;         __builtin_amdgcn_global_load_lds((const unsigned*)((const char*)(gbase) + (v1)), (LAS unsigned*)(lds + (bufoff) + ldsw + 8192), 16, 0, 0); } while (0)
; #define PG8_STAGE(bufoff, gbase, voff) PG8_STAGE2(bufoff, gbase, (voff)[0], (voff)[1])
; #define PG8_LDA(dst, b, h) do { _Pragma("unroll") for (int m = 0; m < 4; ++m) _Pragma("unroll") for (int k = 0; k < 2; ++k) dst[m][k] = *(const LAS bf16x8*)(lds + PG8_SA(b, h) + aoff + m * 2048 + k * 1024); } while (0)
; #define PG8_BAR __builtin_amdgcn_s_barrier()
; template <class Epi, class Sched, bool ALIGN_EPI, bool SP2, bool GATHER>
; DI void gemm_phase(LAS unsigned char* lds, const Gemm g, const Sched& S, const Epi& E) {
;     ...
;         const bool has_next = S.next(ui + 1, nxt);
;         const char* nA = (has_next && !GATHER) ? (const char*)g.A + (size_t)nxt.pm * tstep : cA; const char* nB = has_next ? (const char*)g.Bt + (size_t)nxt.pn * tstep : cB;
;         if constexpr (GATHER) { if (has_next) { PG8_GATHER(nxt, gN); } else {
; #pragma unroll
;             for (int h = 0; h < 2; ++h) { gN[h][0] = gC[h][0]; gN[h][1] = gC[h][1]; } } }
;         for (int t = 0; t < nt; t += 2) {
;             if constexpr (Epi::MID_T >= 0) { if (t == Epi::MID_T) { E.mid(acc, cur, wr, wc, fr, fq); PG8_SCHED; } }
;             const bool last = (t == nt - 2);
;             const char* a1 = cA + (size_t)(t + 1) * kstep;
;             const char* a2 = last ? nA : cA + (size_t)(t + 2) * kstep; const char* b2 = last ? nB : cB + (size_t)(t + 2) * kstep;
;             const char* a3 = a2 + kstep; const char* b3 = b2 + kstep;
;             unsigned x00 = gC[0][0], x01 = gC[0][1], x10 = gC[1][0], x11 = gC[1][1];
;             if constexpr (GATHER) { if (last) { x00 = gN[0][0]; x01 = gN[0][1]; x10 = gN[1][0]; x11 = gN[1][1]; } }
;             PG8_LDB(B0, 0, 0); PG8_LDB(B1, 0, 1); PG8_SCHED; PG8_LDA(At, 0, 0); PG8_STAGE2(PG8_SA(1, 1), a1 + hstepA, gC[1][0], gC[1][1]);
;             PG8_WAIT_V(8); PG8_WAIT_L(0); PG8_BAR; PG8_MMA(0, 0, At, B0); PG8_MMA(0, 1, At, B1); PG8_BAR; PG8_SCHED;
;             PG8_LDA(At, 0, 1); PG8_STAGE(PG8_SB(0, 0), b2, voffB); PG8_STAGE(PG8_SB(0, 1), b2 + hstep, voffB); PG8_STAGE2(PG8_SA(0, 0), a2, x00, x01);
.LBB0_102:
	s_ashr_i32 s51, s50, 31
	s_lshl_b64 s[14:15], s[50:51], 20
	s_add_u32 s52, s3, s14
	s_addc_u32 s53, s63, s15
	s_and_b64 s[14:15], s[8:9], exec
	s_cselect_b32 s5, s53, s11
	s_cselect_b32 s7, s52, s10
	s_ashr_i32 s49, s48, 31
	s_lshl_b64 s[14:15], s[48:49], 20
	s_add_u32 s54, s64, s14
	s_addc_u32 s55, s65, s15
	s_and_b64 s[14:15], s[8:9], exec
	s_cselect_b32 s16, s55, s13
	s_cselect_b32 s17, s54, s12
	s_add_u32 s10, s10, 0x80080
	s_addc_u32 s11, s11, 0
	s_add_u32 s22, s12, 0x100
	s_addc_u32 s38, s13, 0
	s_mov_b32 s39, -2
	ds_read_b128 v[4:7], v175
	ds_read_b128 v[8:11], v175 offset:1024
	ds_read_b128 v[158:161], v175 offset:2048
	ds_read_b128 v[162:165], v175 offset:3072
	ds_read_b128 v[166:169], v176
	ds_read_b128 v[180:183], v176 offset:1024
	ds_read_b128 v[184:187], v176 offset:2048
	ds_read_b128 v[188:191], v176 offset:3072
	s_add_u32 s12, s10, 0xfff80080
	s_addc_u32 s13, s11, -1
	s_cmp_eq_u32 s39, 28
	s_cselect_b32 s15, s5, s13
	s_cselect_b32 s14, s7, s12
	s_cselect_b32 s13, s16, s38
	s_cselect_b32 s12, s17, s22
	s_add_i32 m0, s67, 0xc000
	ds_read_b128 v[192:195], v177
	ds_read_b128 v[196:199], v177 offset:1024
	ds_read_b128 v[200:203], v177 offset:2048
	ds_read_b128 v[204:207], v177 offset:3072
	ds_read_b128 v[208:211], v177 offset:4096
	ds_read_b128 v[212:215], v177 offset:5120
	ds_read_b128 v[216:219], v177 offset:6144
	ds_read_b128 v[220:223], v177 offset:7168
	global_load_lds_dwordx4 v150, s[10:11]
	s_add_i32 m0, s67, 0xe000
	s_nop 0
	global_load_lds_dwordx4 v152, s[10:11]
	s_waitcnt vmcnt(8)
	s_waitcnt lgkmcnt(0)
	s_barrier
	s_setprio 1
	s_waitcnt lgkmcnt(0)
	v_mfma_f32_16x16x32_bf16 v[136:139], v[4:7], v[192:195], 0
	v_mfma_f32_16x16x32_bf16 v[132:135], v[158:161], v[192:195], 0
	v_mfma_f32_16x16x32_bf16 v[128:131], v[4:7], v[200:203], 0
	v_mfma_f32_16x16x32_bf16 v[124:127], v[158:161], v[200:203], 0
	v_mfma_f32_16x16x32_bf16 v[120:123], v[4:7], v[208:211], 0
	v_mfma_f32_16x16x32_bf16 v[116:119], v[158:161], v[208:211], 0
	v_mfma_f32_16x16x32_bf16 v[112:115], v[4:7], v[216:219], 0
	v_mfma_f32_16x16x32_bf16 v[108:111], v[158:161], v[216:219], 0
	v_mfma_f32_16x16x32_bf16 v[136:139], v[8:11], v[196:199], v[136:139]
	v_mfma_f32_16x16x32_bf16 v[132:135], v[162:165], v[196:199], v[132:135]
	v_mfma_f32_16x16x32_bf16 v[128:131], v[8:11], v[204:207], v[128:131]
	v_mfma_f32_16x16x32_bf16 v[124:127], v[162:165], v[204:207], v[124:127]
	v_mfma_f32_16x16x32_bf16 v[120:123], v[8:11], v[212:215], v[120:123]
	v_mfma_f32_16x16x32_bf16 v[116:119], v[162:165], v[212:215], v[116:119]
	v_mfma_f32_16x16x32_bf16 v[112:115], v[8:11], v[220:223], v[112:115]
	v_mfma_f32_16x16x32_bf16 v[108:111], v[162:165], v[220:223], v[108:111]
	v_mfma_f32_16x16x32_bf16 v[72:75], v[166:169], v[192:195], 0
	v_mfma_f32_16x16x32_bf16 v[68:71], v[184:187], v[192:195], 0
	v_mfma_f32_16x16x32_bf16 v[64:67], v[166:169], v[200:203], 0
	v_mfma_f32_16x16x32_bf16 v[60:63], v[184:187], v[200:203], 0
	v_mfma_f32_16x16x32_bf16 v[56:59], v[166:169], v[208:211], 0
	v_mfma_f32_16x16x32_bf16 v[52:55], v[184:187], v[208:211], 0
	v_mfma_f32_16x16x32_bf16 v[48:51], v[166:169], v[216:219], 0
	v_mfma_f32_16x16x32_bf16 v[44:47], v[184:187], v[216:219], 0
	v_mfma_f32_16x16x32_bf16 v[72:75], v[180:183], v[196:199], v[72:75]
	v_mfma_f32_16x16x32_bf16 v[68:71], v[188:191], v[196:199], v[68:71]
	v_mfma_f32_16x16x32_bf16 v[64:67], v[180:183], v[204:207], v[64:67]
	v_mfma_f32_16x16x32_bf16 v[60:63], v[188:191], v[204:207], v[60:63]
	v_mfma_f32_16x16x32_bf16 v[56:59], v[180:183], v[212:215], v[56:59]
	v_mfma_f32_16x16x32_bf16 v[52:55], v[188:191], v[212:215], v[52:55]
	v_mfma_f32_16x16x32_bf16 v[48:51], v[180:183], v[220:223], v[48:51]
	v_mfma_f32_16x16x32_bf16 v[44:47], v[188:191], v[220:223], v[44:47]
	s_setprio 0
	s_barrier
	s_add_i32 s49, s78, s66
	s_add_u32 s98, s12, 0x80
	s_addc_u32 s99, s13, 0
	s_mov_b32 m0, s49
	ds_read_b128 v[192:195], v177 offset:16384
	ds_read_b128 v[196:199], v177 offset:17408
	ds_read_b128 v[200:203], v177 offset:18432
	ds_read_b128 v[204:207], v177 offset:19456
	ds_read_b128 v[208:211], v177 offset:20480
	ds_read_b128 v[212:215], v177 offset:21504
	ds_read_b128 v[216:219], v177 offset:22528
	ds_read_b128 v[220:223], v177 offset:23552
	global_load_lds_dwordx4 v142, s[12:13]
	s_add_i32 m0, s49, 0x2000
	s_add_u32 s56, s12, 0x80000
	s_addc_u32 s57, s13, 0
	s_add_i32 s49, s79, s66
	global_load_lds_dwordx4 v146, s[12:13]
	s_mov_b32 m0, s49
	s_add_u32 s100, s14, 0x80
	s_addc_u32 s101, s15, 0
	global_load_lds_dwordx4 v142, s[56:57]
	s_add_i32 m0, s49, 0x2000
	s_nop 0
	global_load_lds_dwordx4 v146, s[56:57]
	s_mov_b32 m0, s67
	s_nop 0
	global_load_lds_dwordx4 v140, s[14:15]
	s_mov_b32 m0, s68
	s_nop 0
	global_load_lds_dwordx4 v144, s[14:15]
	s_waitcnt vmcnt(8)
	s_waitcnt lgkmcnt(0)
	s_barrier
; #define PG8_STAGE2(bufoff, gbase, v0, v1) do { \
;         __builtin_amdgcn_global_load_lds((const unsigned*)((const char*)(gbase) + (v0)), (LAS unsigned*)(lds + (bufoff) + ldsw), 16, 0, 0); \
;         __builtin_amdgcn_global_load_lds((const unsigned*)((const char*)(gbase) + (v1)), (LAS unsigned*)(lds + (bufoff) + ldsw + 8192), 16, 0, 0); } while (0)
; #define PG8_STAGE(bufoff, gbase, voff) PG8_STAGE2(bufoff, gbase, (voff)[0], (voff)[1])
; #define PG8_LDA(dst, b, h) do { _Pragma("unroll") for (int m = 0; m < 4; ++m) _Pragma("unroll") for (int k = 0; k < 2; ++k) dst[m][k] = *(const LAS bf16x8*)(lds + PG8_SA(b, h) + aoff + m * 2048 + k * 1024); } while (0)
; #define PG8_LDB(dst, b, h) do { _Pragma("unroll") for (int n = 0; n < 2; ++n) _Pragma("unroll") for (int k = 0; k < 2; ++k) dst[n][k] = *(const LAS bf16x8*)(lds + PG8_SB(b, h) + boff + n * 2048 + k * 1024); } while (0)
; #define PG8_WAIT_V(n) asm volatile("s_waitcnt vmcnt(" #n ")" ::: "memory")
; #define PG8_WAIT_L(n) asm volatile("s_waitcnt lgkmcnt(" #n ")" ::: "memory")
; #define PG8_BAR __builtin_amdgcn_s_barrier()
; #define PG8_SCHED __builtin_amdgcn_sched_barrier(0)
; template <class Epi, class Sched, bool ALIGN_EPI, bool SP2, bool GATHER>
; DI void gemm_phase(LAS unsigned char* lds, const Gemm g, const Sched& S, const Epi& E) {
;     ...
;             PG8_LDB(B0, 0, 0); PG8_LDB(B1, 0, 1); PG8_SCHED; PG8_LDA(At, 0, 0); PG8_STAGE2(PG8_SA(1, 1), a1 + hstepA, gC[1][0], gC[1][1]);
;             PG8_WAIT_V(8); PG8_WAIT_L(0); PG8_BAR; PG8_MMA(0, 0, At, B0); PG8_MMA(0, 1, At, B1); PG8_BAR; PG8_SCHED;
;             PG8_LDA(At, 0, 1); PG8_STAGE(PG8_SB(0, 0), b2, voffB); PG8_STAGE(PG8_SB(0, 1), b2 + hstep, voffB); PG8_STAGE2(PG8_SA(0, 0), a2, x00, x01);
;             PG8_WAIT_V(8); PG8_WAIT_L(0); PG8_BAR; PG8_MMA(1, 0, At, B0); PG8_MMA(1, 1, At, B1); PG8_BAR; PG8_SCHED;
;             PG8_LDB(B0, 1, 0); PG8_LDB(B1, 1, 1); PG8_SCHED; PG8_LDA(At, 1, 0); PG8_STAGE2(PG8_SA(0, 1), a2 + hstepA, x10, x11);
;             PG8_WAIT_V(8); PG8_WAIT_L(0); PG8_BAR; PG8_MMA(0, 0, At, B0); PG8_MMA(0, 1, At, B1); PG8_BAR; PG8_SCHED;
;             PG8_LDA(At, 1, 1); PG8_STAGE(PG8_SB(1, 0), b3, voffB); PG8_STAGE(PG8_SB(1, 1), b3 + hstep, voffB); PG8_STAGE2(PG8_SA(1, 0), a3, x00, x01);
;             PG8_WAIT_V(8); PG8_WAIT_L(0); PG8_BAR; PG8_MMA(1, 0, At, B0); PG8_MMA(1, 1, At, B1); PG8_BAR; PG8_SCHED;
	s_setprio 1
	s_waitcnt lgkmcnt(0)
	v_mfma_f32_16x16x32_bf16 v[104:107], v[4:7], v[192:195], 0
	v_mfma_f32_16x16x32_bf16 v[100:103], v[158:161], v[192:195], 0
	v_mfma_f32_16x16x32_bf16 v[96:99], v[4:7], v[200:203], 0
	v_mfma_f32_16x16x32_bf16 v[92:95], v[158:161], v[200:203], 0
	v_mfma_f32_16x16x32_bf16 v[88:91], v[4:7], v[208:211], 0
	v_mfma_f32_16x16x32_bf16 v[84:87], v[158:161], v[208:211], 0
	v_mfma_f32_16x16x32_bf16 v[4:7], v[4:7], v[216:219], 0
	v_mfma_f32_16x16x32_bf16 v[104:107], v[8:11], v[196:199], v[104:107]
	v_mfma_f32_16x16x32_bf16 v[100:103], v[162:165], v[196:199], v[100:103]
	v_mfma_f32_16x16x32_bf16 v[96:99], v[8:11], v[204:207], v[96:99]
	v_mfma_f32_16x16x32_bf16 v[92:95], v[162:165], v[204:207], v[92:95]
	v_mfma_f32_16x16x32_bf16 v[88:91], v[8:11], v[212:215], v[88:91]
	v_mfma_f32_16x16x32_bf16 v[84:87], v[162:165], v[212:215], v[84:87]
	v_mfma_f32_16x16x32_bf16 v[4:7], v[8:11], v[220:223], v[4:7]
	v_mfma_f32_16x16x32_bf16 v[8:11], v[158:161], v[216:219], 0
	v_mfma_f32_16x16x32_bf16 v[8:11], v[162:165], v[220:223], v[8:11]
	v_mfma_f32_16x16x32_bf16 v[40:43], v[166:169], v[192:195], 0
	v_mfma_f32_16x16x32_bf16 v[36:39], v[184:187], v[192:195], 0
	v_mfma_f32_16x16x32_bf16 v[32:35], v[166:169], v[200:203], 0
	v_mfma_f32_16x16x32_bf16 v[28:31], v[184:187], v[200:203], 0
	v_mfma_f32_16x16x32_bf16 v[24:27], v[166:169], v[208:211], 0
	v_mfma_f32_16x16x32_bf16 v[20:23], v[184:187], v[208:211], 0
	v_mfma_f32_16x16x32_bf16 v[16:19], v[166:169], v[216:219], 0
	v_mfma_f32_16x16x32_bf16 v[12:15], v[184:187], v[216:219], 0
	v_mfma_f32_16x16x32_bf16 v[40:43], v[180:183], v[196:199], v[40:43]
	v_mfma_f32_16x16x32_bf16 v[36:39], v[188:191], v[196:199], v[36:39]
	v_mfma_f32_16x16x32_bf16 v[32:35], v[180:183], v[204:207], v[32:35]
	v_mfma_f32_16x16x32_bf16 v[28:31], v[188:191], v[204:207], v[28:31]
	v_mfma_f32_16x16x32_bf16 v[24:27], v[180:183], v[212:215], v[24:27]
	v_mfma_f32_16x16x32_bf16 v[20:23], v[188:191], v[212:215], v[20:23]
	v_mfma_f32_16x16x32_bf16 v[16:19], v[180:183], v[220:223], v[16:19]
	v_mfma_f32_16x16x32_bf16 v[12:15], v[188:191], v[220:223], v[12:15]
	s_setprio 0
	s_barrier
	s_add_i32 s49, 0, 0x18000
	v_add_u32_e32 v3, s49, v172
	s_add_i32 s51, 0, 0x1c000
	ds_read_b128 v[76:79], v3
	ds_read_b128 v[80:83], v3 offset:1024
	ds_read_b128 v[158:161], v3 offset:2048
	ds_read_b128 v[162:165], v3 offset:3072
	v_add_u32_e32 v3, s51, v172
	ds_read_b128 v[166:169], v3
	ds_read_b128 v[180:183], v3 offset:1024
	ds_read_b128 v[184:187], v3 offset:2048
	ds_read_b128 v[188:191], v3 offset:3072
	s_add_u32 s14, s14, 0x80000
	s_addc_u32 s15, s15, 0
	s_mov_b32 m0, s69
	ds_read_b128 v[192:195], v177 offset:32768
	ds_read_b128 v[196:199], v177 offset:33792
	ds_read_b128 v[200:203], v177 offset:34816
	ds_read_b128 v[204:207], v177 offset:35840
	ds_read_b128 v[208:211], v177 offset:36864
	ds_read_b128 v[212:215], v177 offset:37888
	ds_read_b128 v[216:219], v177 offset:38912
	ds_read_b128 v[220:223], v177 offset:39936
	global_load_lds_dwordx4 v140, s[14:15]
	s_mov_b32 m0, s70
	s_nop 0
	global_load_lds_dwordx4 v144, s[14:15]
	s_waitcnt vmcnt(8)
	s_waitcnt lgkmcnt(0)
	s_barrier
	s_setprio 1
	s_waitcnt lgkmcnt(0)
	v_mfma_f32_16x16x32_bf16 v[136:139], v[76:79], v[192:195], v[136:139]
	v_mfma_f32_16x16x32_bf16 v[132:135], v[158:161], v[192:195], v[132:135]
	v_mfma_f32_16x16x32_bf16 v[128:131], v[76:79], v[200:203], v[128:131]
	v_mfma_f32_16x16x32_bf16 v[124:127], v[158:161], v[200:203], v[124:127]
	v_mfma_f32_16x16x32_bf16 v[120:123], v[76:79], v[208:211], v[120:123]
	v_mfma_f32_16x16x32_bf16 v[116:119], v[158:161], v[208:211], v[116:119]
	v_mfma_f32_16x16x32_bf16 v[112:115], v[76:79], v[216:219], v[112:115]
	v_mfma_f32_16x16x32_bf16 v[108:111], v[158:161], v[216:219], v[108:111]
	v_mfma_f32_16x16x32_bf16 v[136:139], v[80:83], v[196:199], v[136:139]
	v_mfma_f32_16x16x32_bf16 v[132:135], v[162:165], v[196:199], v[132:135]
	v_mfma_f32_16x16x32_bf16 v[128:131], v[80:83], v[204:207], v[128:131]
	v_mfma_f32_16x16x32_bf16 v[124:127], v[162:165], v[204:207], v[124:127]
	v_mfma_f32_16x16x32_bf16 v[120:123], v[80:83], v[212:215], v[120:123]
	v_mfma_f32_16x16x32_bf16 v[116:119], v[162:165], v[212:215], v[116:119]
	v_mfma_f32_16x16x32_bf16 v[112:115], v[80:83], v[220:223], v[112:115]
	v_mfma_f32_16x16x32_bf16 v[108:111], v[162:165], v[220:223], v[108:111]
	v_mfma_f32_16x16x32_bf16 v[72:75], v[166:169], v[192:195], v[72:75]
	v_mfma_f32_16x16x32_bf16 v[68:71], v[184:187], v[192:195], v[68:71]
	v_mfma_f32_16x16x32_bf16 v[64:67], v[166:169], v[200:203], v[64:67]
	v_mfma_f32_16x16x32_bf16 v[60:63], v[184:187], v[200:203], v[60:63]
	v_mfma_f32_16x16x32_bf16 v[56:59], v[166:169], v[208:211], v[56:59]
	v_mfma_f32_16x16x32_bf16 v[52:55], v[184:187], v[208:211], v[52:55]
	v_mfma_f32_16x16x32_bf16 v[48:51], v[166:169], v[216:219], v[48:51]
	v_mfma_f32_16x16x32_bf16 v[44:47], v[184:187], v[216:219], v[44:47]
	v_mfma_f32_16x16x32_bf16 v[72:75], v[180:183], v[196:199], v[72:75]
	v_mfma_f32_16x16x32_bf16 v[68:71], v[188:191], v[196:199], v[68:71]
	v_mfma_f32_16x16x32_bf16 v[64:67], v[180:183], v[204:207], v[64:67]
	v_mfma_f32_16x16x32_bf16 v[60:63], v[188:191], v[204:207], v[60:63]
	v_mfma_f32_16x16x32_bf16 v[56:59], v[180:183], v[212:215], v[56:59]
	v_mfma_f32_16x16x32_bf16 v[52:55], v[188:191], v[212:215], v[52:55]
	v_mfma_f32_16x16x32_bf16 v[48:51], v[180:183], v[220:223], v[48:51]
	v_mfma_f32_16x16x32_bf16 v[44:47], v[188:191], v[220:223], v[44:47]
	s_setprio 0
	s_barrier
; #define PG8_STAGE2(bufoff, gbase, v0, v1) do { \
;         __builtin_amdgcn_global_load_lds((const unsigned*)((const char*)(gbase) + (v0)), (LAS unsigned*)(lds + (bufoff) + ldsw), 16, 0, 0); \
;         __builtin_amdgcn_global_load_lds((const unsigned*)((const char*)(gbase) + (v1)), (LAS unsigned*)(lds + (bufoff) + ldsw + 8192), 16, 0, 0); } while (0)
; #define PG8_STAGE(bufoff, gbase, voff) PG8_STAGE2(bufoff, gbase, (voff)[0], (voff)[1])
; #define PG8_BAR __builtin_amdgcn_s_barrier()
; template <class Epi, class Sched, bool ALIGN_EPI, bool SP2, bool GATHER>
; DI void gemm_phase(LAS unsigned char* lds, const Gemm g, const Sched& S, const Epi& E) {
;     ...
;         for (int t = 0; t < nt; t += 2) {
;             if constexpr (Epi::MID_T >= 0) { if (t == Epi::MID_T) { E.mid(acc, cur, wr, wc, fr, fq); PG8_SCHED; } }
;             const bool last = (t == nt - 2);
;             const char* a1 = cA + (size_t)(t + 1) * kstep;
;             const char* a2 = last ? nA : cA + (size_t)(t + 2) * kstep; const char* b2 = last ? nB : cB + (size_t)(t + 2) * kstep;
;             const char* a3 = a2 + kstep; const char* b3 = b2 + kstep;
;             unsigned x00 = gC[0][0], x01 = gC[0][1], x10 = gC[1][0], x11 = gC[1][1];
;             if constexpr (GATHER) { if (last) { x00 = gN[0][0]; x01 = gN[0][1]; x10 = gN[1][0]; x11 = gN[1][1]; } }
;             PG8_LDB(B0, 0, 0); PG8_LDB(B1, 0, 1); PG8_SCHED; PG8_LDA(At, 0, 0); PG8_STAGE2(PG8_SA(1, 1), a1 + hstepA, gC[1][0], gC[1][1]);
;             PG8_WAIT_V(8); PG8_WAIT_L(0); PG8_BAR; PG8_MMA(0, 0, At, B0); PG8_MMA(0, 1, At, B1); PG8_BAR; PG8_SCHED;
;             PG8_LDA(At, 0, 1); PG8_STAGE(PG8_SB(0, 0), b2, voffB); PG8_STAGE(PG8_SB(0, 1), b2 + hstep, voffB); PG8_STAGE2(PG8_SA(0, 0), a2, x00, x01);
;             PG8_WAIT_V(8); PG8_WAIT_L(0); PG8_BAR; PG8_MMA(1, 0, At, B0); PG8_MMA(1, 1, At, B1); PG8_BAR; PG8_SCHED;
;             PG8_LDB(B0, 1, 0); PG8_LDB(B1, 1, 1); PG8_SCHED; PG8_LDA(At, 1, 0); PG8_STAGE2(PG8_SA(0, 1), a2 + hstepA, x10, x11);
;             PG8_WAIT_V(8); PG8_WAIT_L(0); PG8_BAR; PG8_MMA(0, 0, At, B0); PG8_MMA(0, 1, At, B1); PG8_BAR; PG8_SCHED;
;             PG8_LDA(At, 1, 1); PG8_STAGE(PG8_SB(1, 0), b3, voffB); PG8_STAGE(PG8_SB(1, 1), b3 + hstep, voffB); PG8_STAGE2(PG8_SA(1, 0), a3, x00, x01);
;             PG8_WAIT_V(8); PG8_WAIT_L(0); PG8_BAR; PG8_MMA(1, 0, At, B0); PG8_MMA(1, 1, At, B1); PG8_BAR; PG8_SCHED;
	s_add_i32 s14, s49, s66
	s_mov_b32 m0, s14
	ds_read_b128 v[192:195], v177 offset:49152
	ds_read_b128 v[196:199], v177 offset:50176
	ds_read_b128 v[200:203], v177 offset:51200
	ds_read_b128 v[204:207], v177 offset:52224
	ds_read_b128 v[208:211], v177 offset:53248
	ds_read_b128 v[212:215], v177 offset:54272
	ds_read_b128 v[216:219], v177 offset:55296
	ds_read_b128 v[220:223], v177 offset:56320
	global_load_lds_dwordx4 v142, s[98:99]
	s_add_i32 m0, s14, 0x2000
	s_add_u32 s12, s12, 0x80080
	s_addc_u32 s13, s13, 0
	s_add_i32 s14, s51, s66
	global_load_lds_dwordx4 v146, s[98:99]
	s_mov_b32 m0, s14
	s_nop 0
	global_load_lds_dwordx4 v142, s[12:13]
	s_add_i32 m0, s14, 0x2000
	s_nop 0
	global_load_lds_dwordx4 v146, s[12:13]
	s_mov_b32 m0, s73
	s_nop 0
	global_load_lds_dwordx4 v140, s[100:101]
	s_mov_b32 m0, s74
	s_nop 0
	global_load_lds_dwordx4 v144, s[100:101]
	s_waitcnt vmcnt(8)
	s_waitcnt lgkmcnt(0)
	s_barrier
	s_setprio 1
	s_waitcnt lgkmcnt(0)
	v_mfma_f32_16x16x32_bf16 v[104:107], v[76:79], v[192:195], v[104:107]
	v_mfma_f32_16x16x32_bf16 v[96:99], v[76:79], v[200:203], v[96:99]
	v_mfma_f32_16x16x32_bf16 v[88:91], v[76:79], v[208:211], v[88:91]
	v_mfma_f32_16x16x32_bf16 v[4:7], v[76:79], v[216:219], v[4:7]
	v_mfma_f32_16x16x32_bf16 v[104:107], v[80:83], v[196:199], v[104:107]
	v_mfma_f32_16x16x32_bf16 v[100:103], v[158:161], v[192:195], v[100:103]
	v_mfma_f32_16x16x32_bf16 v[96:99], v[80:83], v[204:207], v[96:99]
	v_mfma_f32_16x16x32_bf16 v[92:95], v[158:161], v[200:203], v[92:95]
	v_mfma_f32_16x16x32_bf16 v[88:91], v[80:83], v[212:215], v[88:91]
	v_mfma_f32_16x16x32_bf16 v[84:87], v[158:161], v[208:211], v[84:87]
	v_mfma_f32_16x16x32_bf16 v[80:83], v[80:83], v[220:223], v[4:7]
	v_mfma_f32_16x16x32_bf16 v[4:7], v[158:161], v[216:219], v[8:11]
	v_mfma_f32_16x16x32_bf16 v[100:103], v[162:165], v[196:199], v[100:103]
	v_mfma_f32_16x16x32_bf16 v[92:95], v[162:165], v[204:207], v[92:95]
	v_mfma_f32_16x16x32_bf16 v[84:87], v[162:165], v[212:215], v[84:87]
	v_mfma_f32_16x16x32_bf16 v[76:79], v[162:165], v[220:223], v[4:7]
	v_mfma_f32_16x16x32_bf16 v[4:7], v[166:169], v[192:195], v[40:43]
	v_mfma_f32_16x16x32_bf16 v[40:43], v[180:183], v[196:199], v[4:7]
	v_mfma_f32_16x16x32_bf16 v[4:7], v[184:187], v[192:195], v[36:39]
	v_mfma_f32_16x16x32_bf16 v[36:39], v[188:191], v[196:199], v[4:7]
	v_mfma_f32_16x16x32_bf16 v[4:7], v[166:169], v[200:203], v[32:35]
	v_mfma_f32_16x16x32_bf16 v[32:35], v[180:183], v[204:207], v[4:7]
	v_mfma_f32_16x16x32_bf16 v[4:7], v[184:187], v[200:203], v[28:31]
	v_mfma_f32_16x16x32_bf16 v[28:31], v[188:191], v[204:207], v[4:7]
	v_mfma_f32_16x16x32_bf16 v[4:7], v[166:169], v[208:211], v[24:27]
	v_mfma_f32_16x16x32_bf16 v[24:27], v[180:183], v[212:215], v[4:7]
	v_mfma_f32_16x16x32_bf16 v[4:7], v[184:187], v[208:211], v[20:23]
	v_mfma_f32_16x16x32_bf16 v[20:23], v[188:191], v[212:215], v[4:7]
	v_mfma_f32_16x16x32_bf16 v[4:7], v[166:169], v[216:219], v[16:19]
	v_mfma_f32_16x16x32_bf16 v[16:19], v[180:183], v[220:223], v[4:7]
	v_mfma_f32_16x16x32_bf16 v[4:7], v[184:187], v[216:219], v[12:15]
	v_mfma_f32_16x16x32_bf16 v[12:15], v[188:191], v[220:223], v[4:7]
	s_setprio 0
	s_barrier
	s_add_i32 s39, s39, 2
	s_add_u32 s10, s10, 0x100
	s_addc_u32 s11, s11, 0
	s_add_u32 s22, s22, 0x100
	s_addc_u32 s38, s38, 0
	s_cmp_gt_u32 s39, 29
	s_cbranch_scc1 .Lpeel_exit_p1
.LBB0_103:
	ds_read_b128 v[4:7], v175
	ds_read_b128 v[8:11], v175 offset:1024
	ds_read_b128 v[158:161], v175 offset:2048
	ds_read_b128 v[162:165], v175 offset:3072
	ds_read_b128 v[166:169], v176
	ds_read_b128 v[180:183], v176 offset:1024
	ds_read_b128 v[184:187], v176 offset:2048
	ds_read_b128 v[188:191], v176 offset:3072
	s_add_u32 s12, s10, 0xfff80080
	s_addc_u32 s13, s11, -1
	s_cmp_eq_u32 s39, 28
	s_cselect_b32 s15, s5, s13
	s_cselect_b32 s14, s7, s12
	s_cselect_b32 s13, s16, s38
	s_cselect_b32 s12, s17, s22
	s_add_i32 m0, s67, 0xc000
	ds_read_b128 v[192:195], v177
	ds_read_b128 v[196:199], v177 offset:1024
	ds_read_b128 v[200:203], v177 offset:2048
	ds_read_b128 v[204:207], v177 offset:3072
	ds_read_b128 v[208:211], v177 offset:4096
	ds_read_b128 v[212:215], v177 offset:5120
	ds_read_b128 v[216:219], v177 offset:6144
	ds_read_b128 v[220:223], v177 offset:7168
	global_load_lds_dwordx4 v150, s[10:11]
	s_add_i32 m0, s67, 0xe000
	s_nop 0
	global_load_lds_dwordx4 v152, s[10:11]
	s_waitcnt vmcnt(8)
	s_waitcnt lgkmcnt(0)
	s_barrier
	s_setprio 1
	s_waitcnt lgkmcnt(0)
	v_mfma_f32_16x16x32_bf16 v[136:139], v[4:7], v[192:195], v[136:139]
	v_mfma_f32_16x16x32_bf16 v[132:135], v[158:161], v[192:195], v[132:135]
	v_mfma_f32_16x16x32_bf16 v[128:131], v[4:7], v[200:203], v[128:131]
	v_mfma_f32_16x16x32_bf16 v[124:127], v[158:161], v[200:203], v[124:127]
	v_mfma_f32_16x16x32_bf16 v[120:123], v[4:7], v[208:211], v[120:123]
	v_mfma_f32_16x16x32_bf16 v[116:119], v[158:161], v[208:211], v[116:119]
	v_mfma_f32_16x16x32_bf16 v[112:115], v[4:7], v[216:219], v[112:115]
	v_mfma_f32_16x16x32_bf16 v[108:111], v[158:161], v[216:219], v[108:111]
	v_mfma_f32_16x16x32_bf16 v[136:139], v[8:11], v[196:199], v[136:139]
	v_mfma_f32_16x16x32_bf16 v[132:135], v[162:165], v[196:199], v[132:135]
	v_mfma_f32_16x16x32_bf16 v[128:131], v[8:11], v[204:207], v[128:131]
	v_mfma_f32_16x16x32_bf16 v[124:127], v[162:165], v[204:207], v[124:127]
	v_mfma_f32_16x16x32_bf16 v[120:123], v[8:11], v[212:215], v[120:123]
	v_mfma_f32_16x16x32_bf16 v[116:119], v[162:165], v[212:215], v[116:119]
	v_mfma_f32_16x16x32_bf16 v[112:115], v[8:11], v[220:223], v[112:115]
	v_mfma_f32_16x16x32_bf16 v[108:111], v[162:165], v[220:223], v[108:111]
	v_mfma_f32_16x16x32_bf16 v[72:75], v[166:169], v[192:195], v[72:75]
	v_mfma_f32_16x16x32_bf16 v[68:71], v[184:187], v[192:195], v[68:71]
	v_mfma_f32_16x16x32_bf16 v[64:67], v[166:169], v[200:203], v[64:67]
	v_mfma_f32_16x16x32_bf16 v[60:63], v[184:187], v[200:203], v[60:63]
	v_mfma_f32_16x16x32_bf16 v[56:59], v[166:169], v[208:211], v[56:59]
	v_mfma_f32_16x16x32_bf16 v[52:55], v[184:187], v[208:211], v[52:55]
	v_mfma_f32_16x16x32_bf16 v[48:51], v[166:169], v[216:219], v[48:51]
	v_mfma_f32_16x16x32_bf16 v[44:47], v[184:187], v[216:219], v[44:47]
	v_mfma_f32_16x16x32_bf16 v[72:75], v[180:183], v[196:199], v[72:75]
	v_mfma_f32_16x16x32_bf16 v[68:71], v[188:191], v[196:199], v[68:71]
	v_mfma_f32_16x16x32_bf16 v[64:67], v[180:183], v[204:207], v[64:67]
	v_mfma_f32_16x16x32_bf16 v[60:63], v[188:191], v[204:207], v[60:63]
	v_mfma_f32_16x16x32_bf16 v[56:59], v[180:183], v[212:215], v[56:59]
	v_mfma_f32_16x16x32_bf16 v[52:55], v[188:191], v[212:215], v[52:55]
	v_mfma_f32_16x16x32_bf16 v[48:51], v[180:183], v[220:223], v[48:51]
	v_mfma_f32_16x16x32_bf16 v[44:47], v[188:191], v[220:223], v[44:47]
	s_setprio 0
	s_barrier
; #define PG8_STAGE2(bufoff, gbase, v0, v1) do { \
;         __builtin_amdgcn_global_load_lds((const unsigned*)((const char*)(gbase) + (v0)), (LAS unsigned*)(lds + (bufoff) + ldsw), 16, 0, 0); \
;         __builtin_amdgcn_global_load_lds((const unsigned*)((const char*)(gbase) + (v1)), (LAS unsigned*)(lds + (bufoff) + ldsw + 8192), 16, 0, 0); } while (0)
; #define PG8_STAGE(bufoff, gbase, voff) PG8_STAGE2(bufoff, gbase, (voff)[0], (voff)[1])
; #define PG8_LDA(dst, b, h) do { _Pragma("unroll") for (int m = 0; m < 4; ++m) _Pragma("unroll") for (int k = 0; k < 2; ++k) dst[m][k] = *(const LAS bf16x8*)(lds + PG8_SA(b, h) + aoff + m * 2048 + k * 1024); } while (0)
; #define PG8_LDB(dst, b, h) do { _Pragma("unroll") for (int n = 0; n < 2; ++n) _Pragma("unroll") for (int k = 0; k < 2; ++k) dst[n][k] = *(const LAS bf16x8*)(lds + PG8_SB(b, h) + boff + n * 2048 + k * 1024); } while (0)
; #define PG8_WAIT_V(n) asm volatile("s_waitcnt vmcnt(" #n ")" ::: "memory")
; #define PG8_WAIT_L(n) asm volatile("s_waitcnt lgkmcnt(" #n ")" ::: "memory")
; #define PG8_BAR __builtin_amdgcn_s_barrier()
; #define PG8_SCHED __builtin_amdgcn_sched_barrier(0)
; template <class Epi, class Sched, bool ALIGN_EPI, bool SP2, bool GATHER>
; DI void gemm_phase(LAS unsigned char* lds, const Gemm g, const Sched& S, const Epi& E) {
;     ...
;             PG8_LDB(B0, 0, 0); PG8_LDB(B1, 0, 1); PG8_SCHED; PG8_LDA(At, 0, 0); PG8_STAGE2(PG8_SA(1, 1), a1 + hstepA, gC[1][0], gC[1][1]);
;             PG8_WAIT_V(8); PG8_WAIT_L(0); PG8_BAR; PG8_MMA(0, 0, At, B0); PG8_MMA(0, 1, At, B1); PG8_BAR; PG8_SCHED;
;             PG8_LDA(At, 0, 1); PG8_STAGE(PG8_SB(0, 0), b2, voffB); PG8_STAGE(PG8_SB(0, 1), b2 + hstep, voffB); PG8_STAGE2(PG8_SA(0, 0), a2, x00, x01);
;             PG8_WAIT_V(8); PG8_WAIT_L(0); PG8_BAR; PG8_MMA(1, 0, At, B0); PG8_MMA(1, 1, At, B1); PG8_BAR; PG8_SCHED;
;             PG8_LDB(B0, 1, 0); PG8_LDB(B1, 1, 1); PG8_SCHED; PG8_LDA(At, 1, 0); PG8_STAGE2(PG8_SA(0, 1), a2 + hstepA, x10, x11);
;             PG8_WAIT_V(8); PG8_WAIT_L(0); PG8_BAR; PG8_MMA(0, 0, At, B0); PG8_MMA(0, 1, At, B1); PG8_BAR; PG8_SCHED;
;             PG8_LDA(At, 1, 1); PG8_STAGE(PG8_SB(1, 0), b3, voffB); PG8_STAGE(PG8_SB(1, 1), b3 + hstep, voffB); PG8_STAGE2(PG8_SA(1, 0), a3, x00, x01);
;             PG8_WAIT_V(8); PG8_WAIT_L(0); PG8_BAR; PG8_MMA(1, 0, At, B0); PG8_MMA(1, 1, At, B1); PG8_BAR; PG8_SCHED;
	s_add_i32 s49, s78, s66
	s_add_u32 s98, s12, 0x80
	s_addc_u32 s99, s13, 0
	s_mov_b32 m0, s49
	ds_read_b128 v[192:195], v177 offset:16384
	ds_read_b128 v[196:199], v177 offset:17408
	ds_read_b128 v[200:203], v177 offset:18432
	ds_read_b128 v[204:207], v177 offset:19456
	ds_read_b128 v[208:211], v177 offset:20480
	ds_read_b128 v[212:215], v177 offset:21504
	ds_read_b128 v[216:219], v177 offset:22528
	ds_read_b128 v[220:223], v177 offset:23552
	global_load_lds_dwordx4 v142, s[12:13]
	s_add_i32 m0, s49, 0x2000
	s_add_u32 s56, s12, 0x80000
	s_addc_u32 s57, s13, 0
	s_add_i32 s49, s79, s66
	global_load_lds_dwordx4 v146, s[12:13]
	s_mov_b32 m0, s49
	s_add_u32 s100, s14, 0x80
	s_addc_u32 s101, s15, 0
	global_load_lds_dwordx4 v142, s[56:57]
	s_add_i32 m0, s49, 0x2000
	s_nop 0
	global_load_lds_dwordx4 v146, s[56:57]
	s_mov_b32 m0, s67
	s_nop 0
	global_load_lds_dwordx4 v140, s[14:15]
	s_mov_b32 m0, s68
	s_nop 0
	global_load_lds_dwordx4 v144, s[14:15]
	s_waitcnt vmcnt(8)
	s_waitcnt lgkmcnt(0)
	s_barrier
	s_setprio 1
	s_waitcnt lgkmcnt(0)
	v_mfma_f32_16x16x32_bf16 v[104:107], v[4:7], v[192:195], v[104:107]
	v_mfma_f32_16x16x32_bf16 v[100:103], v[158:161], v[192:195], v[100:103]
	v_mfma_f32_16x16x32_bf16 v[96:99], v[4:7], v[200:203], v[96:99]
	v_mfma_f32_16x16x32_bf16 v[92:95], v[158:161], v[200:203], v[92:95]
	v_mfma_f32_16x16x32_bf16 v[88:91], v[4:7], v[208:211], v[88:91]
	v_mfma_f32_16x16x32_bf16 v[84:87], v[158:161], v[208:211], v[84:87]
	v_mfma_f32_16x16x32_bf16 v[4:7], v[4:7], v[216:219], v[80:83]
	v_mfma_f32_16x16x32_bf16 v[104:107], v[8:11], v[196:199], v[104:107]
	v_mfma_f32_16x16x32_bf16 v[100:103], v[162:165], v[196:199], v[100:103]
	v_mfma_f32_16x16x32_bf16 v[96:99], v[8:11], v[204:207], v[96:99]
	v_mfma_f32_16x16x32_bf16 v[92:95], v[162:165], v[204:207], v[92:95]
	v_mfma_f32_16x16x32_bf16 v[88:91], v[8:11], v[212:215], v[88:91]
	v_mfma_f32_16x16x32_bf16 v[84:87], v[162:165], v[212:215], v[84:87]
	v_mfma_f32_16x16x32_bf16 v[4:7], v[8:11], v[220:223], v[4:7]
	v_mfma_f32_16x16x32_bf16 v[8:11], v[158:161], v[216:219], v[76:79]
	v_mfma_f32_16x16x32_bf16 v[8:11], v[162:165], v[220:223], v[8:11]
	v_mfma_f32_16x16x32_bf16 v[40:43], v[166:169], v[192:195], v[40:43]
	v_mfma_f32_16x16x32_bf16 v[36:39], v[184:187], v[192:195], v[36:39]
	v_mfma_f32_16x16x32_bf16 v[32:35], v[166:169], v[200:203], v[32:35]
	v_mfma_f32_16x16x32_bf16 v[28:31], v[184:187], v[200:203], v[28:31]
	v_mfma_f32_16x16x32_bf16 v[24:27], v[166:169], v[208:211], v[24:27]
	v_mfma_f32_16x16x32_bf16 v[20:23], v[184:187], v[208:211], v[20:23]
	v_mfma_f32_16x16x32_bf16 v[16:19], v[166:169], v[216:219], v[16:19]
	v_mfma_f32_16x16x32_bf16 v[12:15], v[184:187], v[216:219], v[12:15]
	v_mfma_f32_16x16x32_bf16 v[40:43], v[180:183], v[196:199], v[40:43]
	v_mfma_f32_16x16x32_bf16 v[36:39], v[188:191], v[196:199], v[36:39]
	v_mfma_f32_16x16x32_bf16 v[32:35], v[180:183], v[204:207], v[32:35]
	v_mfma_f32_16x16x32_bf16 v[28:31], v[188:191], v[204:207], v[28:31]
	v_mfma_f32_16x16x32_bf16 v[24:27], v[180:183], v[212:215], v[24:27]
	v_mfma_f32_16x16x32_bf16 v[20:23], v[188:191], v[212:215], v[20:23]
	v_mfma_f32_16x16x32_bf16 v[16:19], v[180:183], v[220:223], v[16:19]
	v_mfma_f32_16x16x32_bf16 v[12:15], v[188:191], v[220:223], v[12:15]
	s_setprio 0
	s_barrier
	s_add_i32 s49, 0, 0x18000
	v_add_u32_e32 v3, s49, v172
	s_add_i32 s51, 0, 0x1c000
	ds_read_b128 v[76:79], v3
	ds_read_b128 v[80:83], v3 offset:1024
	ds_read_b128 v[158:161], v3 offset:2048
	ds_read_b128 v[162:165], v3 offset:3072
	v_add_u32_e32 v3, s51, v172
	ds_read_b128 v[166:169], v3
	ds_read_b128 v[180:183], v3 offset:1024
	ds_read_b128 v[184:187], v3 offset:2048
	ds_read_b128 v[188:191], v3 offset:3072
	s_add_u32 s14, s14, 0x80000
	s_addc_u32 s15, s15, 0
	s_mov_b32 m0, s69
	ds_read_b128 v[192:195], v177 offset:32768
	ds_read_b128 v[196:199], v177 offset:33792
	ds_read_b128 v[200:203], v177 offset:34816
	ds_read_b128 v[204:207], v177 offset:35840
	ds_read_b128 v[208:211], v177 offset:36864
	ds_read_b128 v[212:215], v177 offset:37888
	ds_read_b128 v[216:219], v177 offset:38912
	ds_read_b128 v[220:223], v177 offset:39936
	global_load_lds_dwordx4 v140, s[14:15]
	s_mov_b32 m0, s70
	s_nop 0
	global_load_lds_dwordx4 v144, s[14:15]
	s_waitcnt vmcnt(8)
	s_waitcnt lgkmcnt(0)
	s_barrier
; #define PG8_STAGE2(bufoff, gbase, v0, v1) do { \
;         __builtin_amdgcn_global_load_lds((const unsigned*)((const char*)(gbase) + (v0)), (LAS unsigned*)(lds + (bufoff) + ldsw), 16, 0, 0); \
;         __builtin_amdgcn_global_load_lds((const unsigned*)((const char*)(gbase) + (v1)), (LAS unsigned*)(lds + (bufoff) + ldsw + 8192), 16, 0, 0); } while (0)
; #define PG8_STAGE(bufoff, gbase, voff) PG8_STAGE2(bufoff, gbase, (voff)[0], (voff)[1])
; #define PG8_BAR __builtin_amdgcn_s_barrier()
; template <class Epi, class Sched, bool ALIGN_EPI, bool SP2, bool GATHER>
; DI void gemm_phase(LAS unsigned char* lds, const Gemm g, const Sched& S, const Epi& E) {
;     ...
;         for (int t = 0; t < nt; t += 2) {
;             if constexpr (Epi::MID_T >= 0) { if (t == Epi::MID_T) { E.mid(acc, cur, wr, wc, fr, fq); PG8_SCHED; } }
;             const bool last = (t == nt - 2);
;             const char* a1 = cA + (size_t)(t + 1) * kstep;
;             const char* a2 = last ? nA : cA + (size_t)(t + 2) * kstep; const char* b2 = last ? nB : cB + (size_t)(t + 2) * kstep;
;             const char* a3 = a2 + kstep; const char* b3 = b2 + kstep;
;             unsigned x00 = gC[0][0], x01 = gC[0][1], x10 = gC[1][0], x11 = gC[1][1];
;             if constexpr (GATHER) { if (last) { x00 = gN[0][0]; x01 = gN[0][1]; x10 = gN[1][0]; x11 = gN[1][1]; } }
;             PG8_LDB(B0, 0, 0); PG8_LDB(B1, 0, 1); PG8_SCHED; PG8_LDA(At, 0, 0); PG8_STAGE2(PG8_SA(1, 1), a1 + hstepA, gC[1][0], gC[1][1]);
;             PG8_WAIT_V(8); PG8_WAIT_L(0); PG8_BAR; PG8_MMA(0, 0, At, B0); PG8_MMA(0, 1, At, B1); PG8_BAR; PG8_SCHED;
;             PG8_LDA(At, 0, 1); PG8_STAGE(PG8_SB(0, 0), b2, voffB); PG8_STAGE(PG8_SB(0, 1), b2 + hstep, voffB); PG8_STAGE2(PG8_SA(0, 0), a2, x00, x01);
;             PG8_WAIT_V(8); PG8_WAIT_L(0); PG8_BAR; PG8_MMA(1, 0, At, B0); PG8_MMA(1, 1, At, B1); PG8_BAR; PG8_SCHED;
;             PG8_LDB(B0, 1, 0); PG8_LDB(B1, 1, 1); PG8_SCHED; PG8_LDA(At, 1, 0); PG8_STAGE2(PG8_SA(0, 1), a2 + hstepA, x10, x11);
;             PG8_WAIT_V(8); PG8_WAIT_L(0); PG8_BAR; PG8_MMA(0, 0, At, B0); PG8_MMA(0, 1, At, B1); PG8_BAR; PG8_SCHED;
;             PG8_LDA(At, 1, 1); PG8_STAGE(PG8_SB(1, 0), b3, voffB); PG8_STAGE(PG8_SB(1, 1), b3 + hstep, voffB); PG8_STAGE2(PG8_SA(1, 0), a3, x00, x01);
;             PG8_WAIT_V(8); PG8_WAIT_L(0); PG8_BAR; PG8_MMA(1, 0, At, B0); PG8_MMA(1, 1, At, B1); PG8_BAR; PG8_SCHED;
	s_setprio 1
	s_waitcnt lgkmcnt(0)
	v_mfma_f32_16x16x32_bf16 v[136:139], v[76:79], v[192:195], v[136:139]
	v_mfma_f32_16x16x32_bf16 v[132:135], v[158:161], v[192:195], v[132:135]
	v_mfma_f32_16x16x32_bf16 v[128:131], v[76:79], v[200:203], v[128:131]
	v_mfma_f32_16x16x32_bf16 v[124:127], v[158:161], v[200:203], v[124:127]
	v_mfma_f32_16x16x32_bf16 v[120:123], v[76:79], v[208:211], v[120:123]
	v_mfma_f32_16x16x32_bf16 v[116:119], v[158:161], v[208:211], v[116:119]
	v_mfma_f32_16x16x32_bf16 v[112:115], v[76:79], v[216:219], v[112:115]
	v_mfma_f32_16x16x32_bf16 v[108:111], v[158:161], v[216:219], v[108:111]
	v_mfma_f32_16x16x32_bf16 v[136:139], v[80:83], v[196:199], v[136:139]
	v_mfma_f32_16x16x32_bf16 v[132:135], v[162:165], v[196:199], v[132:135]
	v_mfma_f32_16x16x32_bf16 v[128:131], v[80:83], v[204:207], v[128:131]
	v_mfma_f32_16x16x32_bf16 v[124:127], v[162:165], v[204:207], v[124:127]
	v_mfma_f32_16x16x32_bf16 v[120:123], v[80:83], v[212:215], v[120:123]
	v_mfma_f32_16x16x32_bf16 v[116:119], v[162:165], v[212:215], v[116:119]
	v_mfma_f32_16x16x32_bf16 v[112:115], v[80:83], v[220:223], v[112:115]
	v_mfma_f32_16x16x32_bf16 v[108:111], v[162:165], v[220:223], v[108:111]
	v_mfma_f32_16x16x32_bf16 v[72:75], v[166:169], v[192:195], v[72:75]
	v_mfma_f32_16x16x32_bf16 v[68:71], v[184:187], v[192:195], v[68:71]
	v_mfma_f32_16x16x32_bf16 v[64:67], v[166:169], v[200:203], v[64:67]
	v_mfma_f32_16x16x32_bf16 v[60:63], v[184:187], v[200:203], v[60:63]
	v_mfma_f32_16x16x32_bf16 v[56:59], v[166:169], v[208:211], v[56:59]
	v_mfma_f32_16x16x32_bf16 v[52:55], v[184:187], v[208:211], v[52:55]
	v_mfma_f32_16x16x32_bf16 v[48:51], v[166:169], v[216:219], v[48:51]
	v_mfma_f32_16x16x32_bf16 v[44:47], v[184:187], v[216:219], v[44:47]
	v_mfma_f32_16x16x32_bf16 v[72:75], v[180:183], v[196:199], v[72:75]
	v_mfma_f32_16x16x32_bf16 v[68:71], v[188:191], v[196:199], v[68:71]
	v_mfma_f32_16x16x32_bf16 v[64:67], v[180:183], v[204:207], v[64:67]
	v_mfma_f32_16x16x32_bf16 v[60:63], v[188:191], v[204:207], v[60:63]
	v_mfma_f32_16x16x32_bf16 v[56:59], v[180:183], v[212:215], v[56:59]
	v_mfma_f32_16x16x32_bf16 v[52:55], v[188:191], v[212:215], v[52:55]
	v_mfma_f32_16x16x32_bf16 v[48:51], v[180:183], v[220:223], v[48:51]
	v_mfma_f32_16x16x32_bf16 v[44:47], v[188:191], v[220:223], v[44:47]
	s_setprio 0
	s_barrier
	s_add_i32 s14, s49, s66
	s_mov_b32 m0, s14
	ds_read_b128 v[192:195], v177 offset:49152
	ds_read_b128 v[196:199], v177 offset:50176
	ds_read_b128 v[200:203], v177 offset:51200
	ds_read_b128 v[204:207], v177 offset:52224
	ds_read_b128 v[208:211], v177 offset:53248
	ds_read_b128 v[212:215], v177 offset:54272
	ds_read_b128 v[216:219], v177 offset:55296
	ds_read_b128 v[220:223], v177 offset:56320
	global_load_lds_dwordx4 v142, s[98:99]
	s_add_i32 m0, s14, 0x2000
	s_add_u32 s12, s12, 0x80080
	s_addc_u32 s13, s13, 0
	s_add_i32 s14, s51, s66
	global_load_lds_dwordx4 v146, s[98:99]
	s_mov_b32 m0, s14
	s_nop 0
	global_load_lds_dwordx4 v142, s[12:13]
	s_add_i32 m0, s14, 0x2000
	s_nop 0
	global_load_lds_dwordx4 v146, s[12:13]
	s_mov_b32 m0, s73
	s_nop 0
	global_load_lds_dwordx4 v140, s[100:101]
	s_mov_b32 m0, s74
	s_nop 0
	global_load_lds_dwordx4 v144, s[100:101]
	s_waitcnt vmcnt(8)
	s_waitcnt lgkmcnt(0)
	s_barrier
	s_setprio 1
	s_waitcnt lgkmcnt(0)
	v_mfma_f32_16x16x32_bf16 v[104:107], v[76:79], v[192:195], v[104:107]
	v_mfma_f32_16x16x32_bf16 v[96:99], v[76:79], v[200:203], v[96:99]
	v_mfma_f32_16x16x32_bf16 v[88:91], v[76:79], v[208:211], v[88:91]
	v_mfma_f32_16x16x32_bf16 v[4:7], v[76:79], v[216:219], v[4:7]
	v_mfma_f32_16x16x32_bf16 v[104:107], v[80:83], v[196:199], v[104:107]
	v_mfma_f32_16x16x32_bf16 v[100:103], v[158:161], v[192:195], v[100:103]
	v_mfma_f32_16x16x32_bf16 v[96:99], v[80:83], v[204:207], v[96:99]
	v_mfma_f32_16x16x32_bf16 v[92:95], v[158:161], v[200:203], v[92:95]
	v_mfma_f32_16x16x32_bf16 v[88:91], v[80:83], v[212:215], v[88:91]
	v_mfma_f32_16x16x32_bf16 v[84:87], v[158:161], v[208:211], v[84:87]
	v_mfma_f32_16x16x32_bf16 v[80:83], v[80:83], v[220:223], v[4:7]
	v_mfma_f32_16x16x32_bf16 v[4:7], v[158:161], v[216:219], v[8:11]
	v_mfma_f32_16x16x32_bf16 v[100:103], v[162:165], v[196:199], v[100:103]
	v_mfma_f32_16x16x32_bf16 v[92:95], v[162:165], v[204:207], v[92:95]
	v_mfma_f32_16x16x32_bf16 v[84:87], v[162:165], v[212:215], v[84:87]
	v_mfma_f32_16x16x32_bf16 v[76:79], v[162:165], v[220:223], v[4:7]
	v_mfma_f32_16x16x32_bf16 v[4:7], v[166:169], v[192:195], v[40:43]
	v_mfma_f32_16x16x32_bf16 v[40:43], v[180:183], v[196:199], v[4:7]
	v_mfma_f32_16x16x32_bf16 v[4:7], v[184:187], v[192:195], v[36:39]
	v_mfma_f32_16x16x32_bf16 v[36:39], v[188:191], v[196:199], v[4:7]
	v_mfma_f32_16x16x32_bf16 v[4:7], v[166:169], v[200:203], v[32:35]
	v_mfma_f32_16x16x32_bf16 v[32:35], v[180:183], v[204:207], v[4:7]
	v_mfma_f32_16x16x32_bf16 v[4:7], v[184:187], v[200:203], v[28:31]
	v_mfma_f32_16x16x32_bf16 v[28:31], v[188:191], v[204:207], v[4:7]
	v_mfma_f32_16x16x32_bf16 v[4:7], v[166:169], v[208:211], v[24:27]
	v_mfma_f32_16x16x32_bf16 v[24:27], v[180:183], v[212:215], v[4:7]
	v_mfma_f32_16x16x32_bf16 v[4:7], v[184:187], v[208:211], v[20:23]
	v_mfma_f32_16x16x32_bf16 v[20:23], v[188:191], v[212:215], v[4:7]
	v_mfma_f32_16x16x32_bf16 v[4:7], v[166:169], v[216:219], v[16:19]
	v_mfma_f32_16x16x32_bf16 v[16:19], v[180:183], v[220:223], v[4:7]
	v_mfma_f32_16x16x32_bf16 v[4:7], v[184:187], v[216:219], v[12:15]
	v_mfma_f32_16x16x32_bf16 v[12:15], v[188:191], v[220:223], v[4:7]
	s_setprio 0
	s_barrier
	s_add_i32 s39, s39, 2
	s_add_u32 s10, s10, 0x100
	s_addc_u32 s11, s11, 0
	s_add_u32 s22, s22, 0x100
	s_addc_u32 s38, s38, 0
	s_cmp_gt_u32 s39, 29
	s_cbranch_scc0 .LBB0_103

; #define PG8_STAGE2(bufoff, gbase, v0, v1) do { \
;         __builtin_amdgcn_global_load_lds((const unsigned*)((const char*)(gbase) + (v0)), (LAS unsigned*)(lds + (bufoff) + ldsw), 16, 0, 0); \
;         __builtin_amdgcn_global_load_lds((const unsigned*)((const char*)(gbase) + (v1)), (LAS unsigned*)(lds + (bufoff) + ldsw + 8192), 16, 0, 0); } while (0)
; #define PG8_STAGE(bufoff, gbase, voff) PG8_STAGE2(bufoff, gbase, (voff)[0], (voff)[1])
; #define PG8_BAR __builtin_amdgcn_s_barrier()
; template <class Epi, class Sched, bool ALIGN_EPI, bool SP2, bool GATHER>
; DI void gemm_phase(LAS unsigned char* lds, const Gemm g, const Sched& S, const Epi& E) {
;     ...
;         for (int t = 0; t < nt; t += 2) {
;             if constexpr (Epi::MID_T >= 0) { if (t == Epi::MID_T) { E.mid(acc, cur, wr, wc, fr, fq); PG8_SCHED; } }
;             const bool last = (t == nt - 2);
;             const char* a1 = cA + (size_t)(t + 1) * kstep;
;             const char* a2 = last ? nA : cA + (size_t)(t + 2) * kstep; const char* b2 = last ? nB : cB + (size_t)(t + 2) * kstep;
;             const char* a3 = a2 + kstep; const char* b3 = b2 + kstep;
;             unsigned x00 = gC[0][0], x01 = gC[0][1], x10 = gC[1][0], x11 = gC[1][1];
;             if constexpr (GATHER) { if (last) { x00 = gN[0][0]; x01 = gN[0][1]; x10 = gN[1][0]; x11 = gN[1][1]; } }
;             PG8_LDB(B0, 0, 0); PG8_LDB(B1, 0, 1); PG8_SCHED; PG8_LDA(At, 0, 0); PG8_STAGE2(PG8_SA(1, 1), a1 + hstepA, gC[1][0], gC[1][1]);
;             PG8_WAIT_V(8); PG8_WAIT_L(0); PG8_BAR; PG8_MMA(0, 0, At, B0); PG8_MMA(0, 1, At, B1); PG8_BAR; PG8_SCHED;
;             PG8_LDA(At, 0, 1); PG8_STAGE(PG8_SB(0, 0), b2, voffB); PG8_STAGE(PG8_SB(0, 1), b2 + hstep, voffB); PG8_STAGE2(PG8_SA(0, 0), a2, x00, x01);
;             PG8_WAIT_V(8); PG8_WAIT_L(0); PG8_BAR; PG8_MMA(1, 0, At, B0); PG8_MMA(1, 1, At, B1); PG8_BAR; PG8_SCHED;
;             PG8_LDB(B0, 1, 0); PG8_LDB(B1, 1, 1); PG8_SCHED; PG8_LDA(At, 1, 0); PG8_STAGE2(PG8_SA(0, 1), a2 + hstepA, x10, x11);
;             PG8_WAIT_V(8); PG8_WAIT_L(0); PG8_BAR; PG8_MMA(0, 0, At, B0); PG8_MMA(0, 1, At, B1); PG8_BAR; PG8_SCHED;
;             PG8_LDA(At, 1, 1); PG8_STAGE(PG8_SB(1, 0), b3, voffB); PG8_STAGE(PG8_SB(1, 1), b3 + hstep, voffB); PG8_STAGE2(PG8_SA(1, 0), a3, x00, x01);
;             PG8_WAIT_V(8); PG8_WAIT_L(0); PG8_BAR; PG8_MMA(1, 0, At, B0); PG8_MMA(1, 1, At, B1); PG8_BAR; PG8_SCHED;
.LBB0_601:
	v_add_u32_e32 v3, s74, v180
	ds_read_b128 v[132:135], v3
	ds_read_b128 v[136:139], v3 offset:1024
	ds_read_b128 v[140:143], v3 offset:2048
	ds_read_b128 v[144:147], v3 offset:3072
	v_add_u32_e32 v3, s75, v180
	s_add_u32 s52, s48, s50
	ds_read_b128 v[148:151], v3
	ds_read_b128 v[152:155], v3 offset:1024
	ds_read_b128 v[184:187], v3 offset:2048
	ds_read_b128 v[188:191], v3 offset:3072
	s_addc_u32 s53, s49, s51
	s_add_u32 s52, s52, 0x100
	s_addc_u32 s53, s53, 0
	s_add_u32 s62, s82, s50
	s_addc_u32 s85, s83, s51
	s_cmpk_eq_i32 s50, 0x1300
	s_cselect_b32 s55, s5, s53
	s_cselect_b32 s54, s4, s52
	s_cselect_b32 s53, s47, s85
	s_cselect_b32 s52, s46, s62
	v_lshl_add_u64 v[176:177], v[172:173], 0, s[50:51]
	s_add_i32 m0, s64, 0xc000
	ds_read_b128 v[192:195], v182
	ds_read_b128 v[196:199], v182 offset:1024
	ds_read_b128 v[200:203], v182 offset:2048
	ds_read_b128 v[204:207], v182 offset:3072
	ds_read_b128 v[208:211], v182 offset:4096
	ds_read_b128 v[212:215], v182 offset:5120
	ds_read_b128 v[216:219], v182 offset:6144
	ds_read_b128 v[220:223], v182 offset:7168
	global_load_lds_dwordx4 v[176:177], off
	v_lshl_add_u64 v[176:177], v[174:175], 0, s[50:51]
	s_add_i32 m0, s64, 0xe000
	s_nop 0
	global_load_lds_dwordx4 v[176:177], off
	s_waitcnt vmcnt(8)
	s_waitcnt lgkmcnt(0)
	s_barrier
	s_setprio 1
	s_waitcnt lgkmcnt(0)
	v_mfma_f32_16x16x32_bf16 v[128:131], v[132:135], v[192:195], v[128:131]
	v_mfma_f32_16x16x32_bf16 v[124:127], v[140:143], v[192:195], v[124:127]
	v_mfma_f32_16x16x32_bf16 v[112:115], v[132:135], v[200:203], v[112:115]
	v_mfma_f32_16x16x32_bf16 v[108:111], v[140:143], v[200:203], v[108:111]
	v_mfma_f32_16x16x32_bf16 v[96:99], v[132:135], v[208:211], v[96:99]
	v_mfma_f32_16x16x32_bf16 v[92:95], v[140:143], v[208:211], v[92:95]
	v_mfma_f32_16x16x32_bf16 v[80:83], v[132:135], v[216:219], v[80:83]
	v_mfma_f32_16x16x32_bf16 v[76:79], v[140:143], v[216:219], v[76:79]
	v_mfma_f32_16x16x32_bf16 v[128:131], v[136:139], v[196:199], v[128:131]
	v_mfma_f32_16x16x32_bf16 v[124:127], v[144:147], v[196:199], v[124:127]
	v_mfma_f32_16x16x32_bf16 v[112:115], v[136:139], v[204:207], v[112:115]
	v_mfma_f32_16x16x32_bf16 v[108:111], v[144:147], v[204:207], v[108:111]
	v_mfma_f32_16x16x32_bf16 v[96:99], v[136:139], v[212:215], v[96:99]
	v_mfma_f32_16x16x32_bf16 v[92:95], v[144:147], v[212:215], v[92:95]
	v_mfma_f32_16x16x32_bf16 v[80:83], v[136:139], v[220:223], v[80:83]
	v_mfma_f32_16x16x32_bf16 v[76:79], v[144:147], v[220:223], v[76:79]
	v_mfma_f32_16x16x32_bf16 v[120:123], v[148:151], v[192:195], v[120:123]
	v_mfma_f32_16x16x32_bf16 v[116:119], v[184:187], v[192:195], v[116:119]
	v_mfma_f32_16x16x32_bf16 v[104:107], v[148:151], v[200:203], v[104:107]
	v_mfma_f32_16x16x32_bf16 v[100:103], v[184:187], v[200:203], v[100:103]
	v_mfma_f32_16x16x32_bf16 v[88:91], v[148:151], v[208:211], v[88:91]
	v_mfma_f32_16x16x32_bf16 v[84:87], v[184:187], v[208:211], v[84:87]
	v_mfma_f32_16x16x32_bf16 v[72:75], v[148:151], v[216:219], v[72:75]
	v_mfma_f32_16x16x32_bf16 v[68:71], v[184:187], v[216:219], v[68:71]
	v_mfma_f32_16x16x32_bf16 v[120:123], v[152:155], v[196:199], v[120:123]
	v_mfma_f32_16x16x32_bf16 v[116:119], v[188:191], v[196:199], v[116:119]
	v_mfma_f32_16x16x32_bf16 v[104:107], v[152:155], v[204:207], v[104:107]
	v_mfma_f32_16x16x32_bf16 v[100:103], v[188:191], v[204:207], v[100:103]
	v_mfma_f32_16x16x32_bf16 v[88:91], v[152:155], v[212:215], v[88:91]
	v_mfma_f32_16x16x32_bf16 v[84:87], v[188:191], v[212:215], v[84:87]
	v_mfma_f32_16x16x32_bf16 v[72:75], v[152:155], v[220:223], v[72:75]
	v_mfma_f32_16x16x32_bf16 v[68:71], v[188:191], v[220:223], v[68:71]
	s_setprio 0
	s_barrier
	s_add_i32 s62, s74, s63
	v_lshl_add_u64 v[176:177], s[52:53], 0, v[158:159]
	s_mov_b32 m0, s62
	ds_read_b128 v[192:195], v182 offset:16384
	ds_read_b128 v[196:199], v182 offset:17408
	ds_read_b128 v[200:203], v182 offset:18432
	ds_read_b128 v[204:207], v182 offset:19456
	ds_read_b128 v[208:211], v182 offset:20480
	ds_read_b128 v[212:215], v182 offset:21504
	ds_read_b128 v[216:219], v182 offset:22528
	ds_read_b128 v[220:223], v182 offset:23552
	global_load_lds_dwordx4 v[176:177], off
	s_add_i32 m0, s62, 0x2000
	s_add_u32 s86, s52, 0xa0000
	v_lshl_add_u64 v[224:225], s[52:53], 0, v[162:163]
	s_addc_u32 s87, s53, 0
	s_add_i32 s62, s75, s63
	global_load_lds_dwordx4 v[224:225], off
	v_lshl_add_u64 v[226:227], s[86:87], 0, v[158:159]
	s_mov_b32 m0, s62
	v_lshl_add_u64 v[228:229], s[54:55], 0, v[160:161]
	global_load_lds_dwordx4 v[226:227], off
	v_lshl_add_u64 v[226:227], s[86:87], 0, v[162:163]
	s_add_i32 m0, s62, 0x2000
	s_nop 0
	global_load_lds_dwordx4 v[226:227], off
	v_lshl_add_u64 v[226:227], s[54:55], 0, v[156:157]
	s_mov_b32 m0, s64
	s_nop 0
	global_load_lds_dwordx4 v[226:227], off
	s_mov_b32 m0, s65
	s_nop 0
	global_load_lds_dwordx4 v[228:229], off
	s_waitcnt vmcnt(8)
	s_waitcnt lgkmcnt(0)
	s_barrier
; #define PG8_STAGE2(bufoff, gbase, v0, v1) do { \
;         __builtin_amdgcn_global_load_lds((const unsigned*)((const char*)(gbase) + (v0)), (LAS unsigned*)(lds + (bufoff) + ldsw), 16, 0, 0); \
;         __builtin_amdgcn_global_load_lds((const unsigned*)((const char*)(gbase) + (v1)), (LAS unsigned*)(lds + (bufoff) + ldsw + 8192), 16, 0, 0); } while (0)
; #define PG8_STAGE(bufoff, gbase, voff) PG8_STAGE2(bufoff, gbase, (voff)[0], (voff)[1])
; #define PG8_LDA(dst, b, h) do { _Pragma("unroll") for (int m = 0; m < 4; ++m) _Pragma("unroll") for (int k = 0; k < 2; ++k) dst[m][k] = *(const LAS bf16x8*)(lds + PG8_SA(b, h) + aoff + m * 2048 + k * 1024); } while (0)
; #define PG8_LDB(dst, b, h) do { _Pragma("unroll") for (int n = 0; n < 2; ++n) _Pragma("unroll") for (int k = 0; k < 2; ++k) dst[n][k] = *(const LAS bf16x8*)(lds + PG8_SB(b, h) + boff + n * 2048 + k * 1024); } while (0)
; #define PG8_WAIT_V(n) asm volatile("s_waitcnt vmcnt(" #n ")" ::: "memory")
; #define PG8_WAIT_L(n) asm volatile("s_waitcnt lgkmcnt(" #n ")" ::: "memory")
; #define PG8_BAR __builtin_amdgcn_s_barrier()
; #define PG8_SCHED __builtin_amdgcn_sched_barrier(0)
; template <class Epi, class Sched, bool ALIGN_EPI, bool SP2, bool GATHER>
; DI void gemm_phase(LAS unsigned char* lds, const Gemm g, const Sched& S, const Epi& E) {
;     ...
;             PG8_LDB(B0, 0, 0); PG8_LDB(B1, 0, 1); PG8_SCHED; PG8_LDA(At, 0, 0); PG8_STAGE2(PG8_SA(1, 1), a1 + hstepA, gC[1][0], gC[1][1]);
;             PG8_WAIT_V(8); PG8_WAIT_L(0); PG8_BAR; PG8_MMA(0, 0, At, B0); PG8_MMA(0, 1, At, B1); PG8_BAR; PG8_SCHED;
;             PG8_LDA(At, 0, 1); PG8_STAGE(PG8_SB(0, 0), b2, voffB); PG8_STAGE(PG8_SB(0, 1), b2 + hstep, voffB); PG8_STAGE2(PG8_SA(0, 0), a2, x00, x01);
;             PG8_WAIT_V(8); PG8_WAIT_L(0); PG8_BAR; PG8_MMA(1, 0, At, B0); PG8_MMA(1, 1, At, B1); PG8_BAR; PG8_SCHED;
;             PG8_LDB(B0, 1, 0); PG8_LDB(B1, 1, 1); PG8_SCHED; PG8_LDA(At, 1, 0); PG8_STAGE2(PG8_SA(0, 1), a2 + hstepA, x10, x11);
;             PG8_WAIT_V(8); PG8_WAIT_L(0); PG8_BAR; PG8_MMA(0, 0, At, B0); PG8_MMA(0, 1, At, B1); PG8_BAR; PG8_SCHED;
;             PG8_LDA(At, 1, 1); PG8_STAGE(PG8_SB(1, 0), b3, voffB); PG8_STAGE(PG8_SB(1, 1), b3 + hstep, voffB); PG8_STAGE2(PG8_SA(1, 0), a3, x00, x01);
;             PG8_WAIT_V(8); PG8_WAIT_L(0); PG8_BAR; PG8_MMA(1, 0, At, B0); PG8_MMA(1, 1, At, B1); PG8_BAR; PG8_SCHED;
	s_setprio 1
	s_waitcnt lgkmcnt(0)
	v_mfma_f32_16x16x32_bf16 v[64:67], v[132:135], v[192:195], v[64:67]
	v_mfma_f32_16x16x32_bf16 v[60:63], v[140:143], v[192:195], v[60:63]
	v_mfma_f32_16x16x32_bf16 v[48:51], v[132:135], v[200:203], v[48:51]
	v_mfma_f32_16x16x32_bf16 v[44:47], v[140:143], v[200:203], v[44:47]
	v_mfma_f32_16x16x32_bf16 v[32:35], v[132:135], v[208:211], v[32:35]
	v_mfma_f32_16x16x32_bf16 v[28:31], v[140:143], v[208:211], v[28:31]
	v_mfma_f32_16x16x32_bf16 v[16:19], v[132:135], v[216:219], v[16:19]
	v_mfma_f32_16x16x32_bf16 v[12:15], v[140:143], v[216:219], v[12:15]
	v_mfma_f32_16x16x32_bf16 v[64:67], v[136:139], v[196:199], v[64:67]
	v_mfma_f32_16x16x32_bf16 v[60:63], v[144:147], v[196:199], v[60:63]
	v_mfma_f32_16x16x32_bf16 v[48:51], v[136:139], v[204:207], v[48:51]
	v_mfma_f32_16x16x32_bf16 v[44:47], v[144:147], v[204:207], v[44:47]
	v_mfma_f32_16x16x32_bf16 v[32:35], v[136:139], v[212:215], v[32:35]
	v_mfma_f32_16x16x32_bf16 v[28:31], v[144:147], v[212:215], v[28:31]
	v_mfma_f32_16x16x32_bf16 v[16:19], v[136:139], v[220:223], v[16:19]
	v_mfma_f32_16x16x32_bf16 v[12:15], v[144:147], v[220:223], v[12:15]
	v_mfma_f32_16x16x32_bf16 v[56:59], v[148:151], v[192:195], v[56:59]
	v_mfma_f32_16x16x32_bf16 v[52:55], v[184:187], v[192:195], v[52:55]
	v_mfma_f32_16x16x32_bf16 v[40:43], v[148:151], v[200:203], v[40:43]
	v_mfma_f32_16x16x32_bf16 v[36:39], v[184:187], v[200:203], v[36:39]
	v_mfma_f32_16x16x32_bf16 v[24:27], v[148:151], v[208:211], v[24:27]
	v_mfma_f32_16x16x32_bf16 v[20:23], v[184:187], v[208:211], v[20:23]
	v_mfma_f32_16x16x32_bf16 v[8:11], v[148:151], v[216:219], v[8:11]
	v_mfma_f32_16x16x32_bf16 v[4:7], v[184:187], v[216:219], v[4:7]
	v_mfma_f32_16x16x32_bf16 v[56:59], v[152:155], v[196:199], v[56:59]
	v_mfma_f32_16x16x32_bf16 v[52:55], v[188:191], v[196:199], v[52:55]
	v_mfma_f32_16x16x32_bf16 v[40:43], v[152:155], v[204:207], v[40:43]
	v_mfma_f32_16x16x32_bf16 v[36:39], v[188:191], v[204:207], v[36:39]
	v_mfma_f32_16x16x32_bf16 v[24:27], v[152:155], v[212:215], v[24:27]
	v_mfma_f32_16x16x32_bf16 v[20:23], v[188:191], v[212:215], v[20:23]
	v_mfma_f32_16x16x32_bf16 v[8:11], v[152:155], v[220:223], v[8:11]
	v_mfma_f32_16x16x32_bf16 v[4:7], v[188:191], v[220:223], v[4:7]
	s_setprio 0
	s_barrier
	s_add_i32 s62, 0, 0x18000
	v_add_u32_e32 v3, s62, v180
	s_add_i32 s85, 0, 0x1c000
	ds_read_b128 v[132:135], v3
	ds_read_b128 v[136:139], v3 offset:1024
	ds_read_b128 v[140:143], v3 offset:2048
	ds_read_b128 v[144:147], v3 offset:3072
	v_add_u32_e32 v3, s85, v180
	ds_read_b128 v[148:151], v3
	ds_read_b128 v[152:155], v3 offset:1024
	ds_read_b128 v[184:187], v3 offset:2048
	ds_read_b128 v[188:191], v3 offset:3072
	s_add_u32 s54, s54, 0xa0000
	s_addc_u32 s55, s55, 0
	s_mov_b32 m0, s66
	v_lshl_add_u64 v[230:231], s[54:55], 0, v[156:157]
	ds_read_b128 v[192:195], v182 offset:32768
	ds_read_b128 v[196:199], v182 offset:33792
	ds_read_b128 v[200:203], v182 offset:34816
	ds_read_b128 v[204:207], v182 offset:35840
	ds_read_b128 v[208:211], v182 offset:36864
	ds_read_b128 v[212:215], v182 offset:37888
	ds_read_b128 v[216:219], v182 offset:38912
	ds_read_b128 v[220:223], v182 offset:39936
	global_load_lds_dwordx4 v[230:231], off
	v_lshl_add_u64 v[230:231], s[54:55], 0, v[160:161]
	s_mov_b32 m0, s67
	s_nop 0
	global_load_lds_dwordx4 v[230:231], off
	s_waitcnt vmcnt(8)
	s_waitcnt lgkmcnt(0)
	s_barrier
	s_setprio 1
	s_waitcnt lgkmcnt(0)
	v_mfma_f32_16x16x32_bf16 v[128:131], v[132:135], v[192:195], v[128:131]
	v_mfma_f32_16x16x32_bf16 v[124:127], v[140:143], v[192:195], v[124:127]
	v_mfma_f32_16x16x32_bf16 v[112:115], v[132:135], v[200:203], v[112:115]
	v_mfma_f32_16x16x32_bf16 v[108:111], v[140:143], v[200:203], v[108:111]
	v_mfma_f32_16x16x32_bf16 v[96:99], v[132:135], v[208:211], v[96:99]
	v_mfma_f32_16x16x32_bf16 v[92:95], v[140:143], v[208:211], v[92:95]
	v_mfma_f32_16x16x32_bf16 v[80:83], v[132:135], v[216:219], v[80:83]
	v_mfma_f32_16x16x32_bf16 v[76:79], v[140:143], v[216:219], v[76:79]
	v_mfma_f32_16x16x32_bf16 v[128:131], v[136:139], v[196:199], v[128:131]
	v_mfma_f32_16x16x32_bf16 v[124:127], v[144:147], v[196:199], v[124:127]
	v_mfma_f32_16x16x32_bf16 v[112:115], v[136:139], v[204:207], v[112:115]
	v_mfma_f32_16x16x32_bf16 v[108:111], v[144:147], v[204:207], v[108:111]
	v_mfma_f32_16x16x32_bf16 v[96:99], v[136:139], v[212:215], v[96:99]
	v_mfma_f32_16x16x32_bf16 v[92:95], v[144:147], v[212:215], v[92:95]
	v_mfma_f32_16x16x32_bf16 v[80:83], v[136:139], v[220:223], v[80:83]
	v_mfma_f32_16x16x32_bf16 v[76:79], v[144:147], v[220:223], v[76:79]
	v_mfma_f32_16x16x32_bf16 v[120:123], v[148:151], v[192:195], v[120:123]
	v_mfma_f32_16x16x32_bf16 v[116:119], v[184:187], v[192:195], v[116:119]
	v_mfma_f32_16x16x32_bf16 v[104:107], v[148:151], v[200:203], v[104:107]
	v_mfma_f32_16x16x32_bf16 v[100:103], v[184:187], v[200:203], v[100:103]
	v_mfma_f32_16x16x32_bf16 v[88:91], v[148:151], v[208:211], v[88:91]
	v_mfma_f32_16x16x32_bf16 v[84:87], v[184:187], v[208:211], v[84:87]
	v_mfma_f32_16x16x32_bf16 v[72:75], v[148:151], v[216:219], v[72:75]
	v_mfma_f32_16x16x32_bf16 v[68:71], v[184:187], v[216:219], v[68:71]
	v_mfma_f32_16x16x32_bf16 v[120:123], v[152:155], v[196:199], v[120:123]
	v_mfma_f32_16x16x32_bf16 v[116:119], v[188:191], v[196:199], v[116:119]
	v_mfma_f32_16x16x32_bf16 v[104:107], v[152:155], v[204:207], v[104:107]
	v_mfma_f32_16x16x32_bf16 v[100:103], v[188:191], v[204:207], v[100:103]
	v_mfma_f32_16x16x32_bf16 v[88:91], v[152:155], v[212:215], v[88:91]
	v_mfma_f32_16x16x32_bf16 v[84:87], v[188:191], v[212:215], v[84:87]
	v_mfma_f32_16x16x32_bf16 v[72:75], v[152:155], v[220:223], v[72:75]
	v_mfma_f32_16x16x32_bf16 v[68:71], v[188:191], v[220:223], v[68:71]
	s_setprio 0
	s_barrier
; #define PG8_STAGE2(bufoff, gbase, v0, v1) do { \
;         __builtin_amdgcn_global_load_lds((const unsigned*)((const char*)(gbase) + (v0)), (LAS unsigned*)(lds + (bufoff) + ldsw), 16, 0, 0); \
;         __builtin_amdgcn_global_load_lds((const unsigned*)((const char*)(gbase) + (v1)), (LAS unsigned*)(lds + (bufoff) + ldsw + 8192), 16, 0, 0); } while (0)
; #define PG8_STAGE(bufoff, gbase, voff) PG8_STAGE2(bufoff, gbase, (voff)[0], (voff)[1])
; #define PG8_BAR __builtin_amdgcn_s_barrier()
; template <class Epi, class Sched, bool ALIGN_EPI, bool SP2, bool GATHER>
; DI void gemm_phase(LAS unsigned char* lds, const Gemm g, const Sched& S, const Epi& E) {
;     ...
;         for (int t = 0; t < nt; t += 2) {
;             if constexpr (Epi::MID_T >= 0) { if (t == Epi::MID_T) { E.mid(acc, cur, wr, wc, fr, fq); PG8_SCHED; } }
;             const bool last = (t == nt - 2);
;             const char* a1 = cA + (size_t)(t + 1) * kstep;
;             const char* a2 = last ? nA : cA + (size_t)(t + 2) * kstep; const char* b2 = last ? nB : cB + (size_t)(t + 2) * kstep;
;             const char* a3 = a2 + kstep; const char* b3 = b2 + kstep;
;             unsigned x00 = gC[0][0], x01 = gC[0][1], x10 = gC[1][0], x11 = gC[1][1];
;             if constexpr (GATHER) { if (last) { x00 = gN[0][0]; x01 = gN[0][1]; x10 = gN[1][0]; x11 = gN[1][1]; } }
;             PG8_LDB(B0, 0, 0); PG8_LDB(B1, 0, 1); PG8_SCHED; PG8_LDA(At, 0, 0); PG8_STAGE2(PG8_SA(1, 1), a1 + hstepA, gC[1][0], gC[1][1]);
;             PG8_WAIT_V(8); PG8_WAIT_L(0); PG8_BAR; PG8_MMA(0, 0, At, B0); PG8_MMA(0, 1, At, B1); PG8_BAR; PG8_SCHED;
;             PG8_LDA(At, 0, 1); PG8_STAGE(PG8_SB(0, 0), b2, voffB); PG8_STAGE(PG8_SB(0, 1), b2 + hstep, voffB); PG8_STAGE2(PG8_SA(0, 0), a2, x00, x01);
;             PG8_WAIT_V(8); PG8_WAIT_L(0); PG8_BAR; PG8_MMA(1, 0, At, B0); PG8_MMA(1, 1, At, B1); PG8_BAR; PG8_SCHED;
;             PG8_LDB(B0, 1, 0); PG8_LDB(B1, 1, 1); PG8_SCHED; PG8_LDA(At, 1, 0); PG8_STAGE2(PG8_SA(0, 1), a2 + hstepA, x10, x11);
;             PG8_WAIT_V(8); PG8_WAIT_L(0); PG8_BAR; PG8_MMA(0, 0, At, B0); PG8_MMA(0, 1, At, B1); PG8_BAR; PG8_SCHED;
;             PG8_LDA(At, 1, 1); PG8_STAGE(PG8_SB(1, 0), b3, voffB); PG8_STAGE(PG8_SB(1, 1), b3 + hstep, voffB); PG8_STAGE2(PG8_SA(1, 0), a3, x00, x01);
;             PG8_WAIT_V(8); PG8_WAIT_L(0); PG8_BAR; PG8_MMA(1, 0, At, B0); PG8_MMA(1, 1, At, B1); PG8_BAR; PG8_SCHED;
	s_add_i32 s54, s62, s63
	v_lshl_add_u64 v[176:177], v[176:177], 0, s[18:19]
	s_mov_b32 m0, s54
	ds_read_b128 v[192:195], v182 offset:49152
	ds_read_b128 v[196:199], v182 offset:50176
	ds_read_b128 v[200:203], v182 offset:51200
	ds_read_b128 v[204:207], v182 offset:52224
	ds_read_b128 v[208:211], v182 offset:53248
	ds_read_b128 v[212:215], v182 offset:54272
	ds_read_b128 v[216:219], v182 offset:55296
	ds_read_b128 v[220:223], v182 offset:56320
	global_load_lds_dwordx4 v[176:177], off
	s_add_i32 m0, s54, 0x2000
	s_add_u32 s52, s52, 0xa0080
	v_lshl_add_u64 v[176:177], v[224:225], 0, s[18:19]
	s_addc_u32 s53, s53, 0
	s_add_i32 s54, s85, s63
	global_load_lds_dwordx4 v[176:177], off
	v_lshl_add_u64 v[176:177], s[52:53], 0, v[158:159]
	s_mov_b32 m0, s54
	s_nop 0
	global_load_lds_dwordx4 v[176:177], off
	v_lshl_add_u64 v[176:177], s[52:53], 0, v[162:163]
	s_add_i32 m0, s54, 0x2000
	s_nop 0
	global_load_lds_dwordx4 v[176:177], off
	v_lshl_add_u64 v[176:177], v[226:227], 0, s[18:19]
	s_mov_b32 m0, s71
	s_nop 0
	global_load_lds_dwordx4 v[176:177], off
	v_lshl_add_u64 v[176:177], v[228:229], 0, s[18:19]
	s_mov_b32 m0, s72
	s_nop 0
	global_load_lds_dwordx4 v[176:177], off
	s_waitcnt vmcnt(8)
	s_waitcnt lgkmcnt(0)
	s_barrier
	s_setprio 1
	s_waitcnt lgkmcnt(0)
	v_mfma_f32_16x16x32_bf16 v[64:67], v[132:135], v[192:195], v[64:67]
	v_mfma_f32_16x16x32_bf16 v[60:63], v[140:143], v[192:195], v[60:63]
	v_mfma_f32_16x16x32_bf16 v[48:51], v[132:135], v[200:203], v[48:51]
	v_mfma_f32_16x16x32_bf16 v[44:47], v[140:143], v[200:203], v[44:47]
	v_mfma_f32_16x16x32_bf16 v[32:35], v[132:135], v[208:211], v[32:35]
	v_mfma_f32_16x16x32_bf16 v[28:31], v[140:143], v[208:211], v[28:31]
	v_mfma_f32_16x16x32_bf16 v[16:19], v[132:135], v[216:219], v[16:19]
	v_mfma_f32_16x16x32_bf16 v[12:15], v[140:143], v[216:219], v[12:15]
	v_mfma_f32_16x16x32_bf16 v[64:67], v[136:139], v[196:199], v[64:67]
	v_mfma_f32_16x16x32_bf16 v[60:63], v[144:147], v[196:199], v[60:63]
	v_mfma_f32_16x16x32_bf16 v[48:51], v[136:139], v[204:207], v[48:51]
	v_mfma_f32_16x16x32_bf16 v[44:47], v[144:147], v[204:207], v[44:47]
	v_mfma_f32_16x16x32_bf16 v[32:35], v[136:139], v[212:215], v[32:35]
	v_mfma_f32_16x16x32_bf16 v[28:31], v[144:147], v[212:215], v[28:31]
	v_mfma_f32_16x16x32_bf16 v[16:19], v[136:139], v[220:223], v[16:19]
	v_mfma_f32_16x16x32_bf16 v[12:15], v[144:147], v[220:223], v[12:15]
	v_mfma_f32_16x16x32_bf16 v[56:59], v[148:151], v[192:195], v[56:59]
	v_mfma_f32_16x16x32_bf16 v[52:55], v[184:187], v[192:195], v[52:55]
	v_mfma_f32_16x16x32_bf16 v[40:43], v[148:151], v[200:203], v[40:43]
	v_mfma_f32_16x16x32_bf16 v[36:39], v[184:187], v[200:203], v[36:39]
	v_mfma_f32_16x16x32_bf16 v[24:27], v[148:151], v[208:211], v[24:27]
	v_mfma_f32_16x16x32_bf16 v[20:23], v[184:187], v[208:211], v[20:23]
	v_mfma_f32_16x16x32_bf16 v[8:11], v[148:151], v[216:219], v[8:11]
	v_mfma_f32_16x16x32_bf16 v[4:7], v[184:187], v[216:219], v[4:7]
	v_mfma_f32_16x16x32_bf16 v[56:59], v[152:155], v[196:199], v[56:59]
	v_mfma_f32_16x16x32_bf16 v[52:55], v[188:191], v[196:199], v[52:55]
	v_mfma_f32_16x16x32_bf16 v[40:43], v[152:155], v[204:207], v[40:43]
	v_mfma_f32_16x16x32_bf16 v[36:39], v[188:191], v[204:207], v[36:39]
	v_mfma_f32_16x16x32_bf16 v[24:27], v[152:155], v[212:215], v[24:27]
	v_mfma_f32_16x16x32_bf16 v[20:23], v[188:191], v[212:215], v[20:23]
	v_mfma_f32_16x16x32_bf16 v[8:11], v[152:155], v[220:223], v[8:11]
	v_mfma_f32_16x16x32_bf16 v[4:7], v[188:191], v[220:223], v[4:7]
	s_setprio 0
	s_barrier
	s_add_i32 s84, s84, 2
	s_add_u32 s50, s50, 0x100
	s_addc_u32 s51, s51, 0
	s_cmp_gt_u32 s84, 37
	s_cbranch_scc1 .LBB0_604

; #define PG8_BAR __builtin_amdgcn_s_barrier()
; template <class Epi, class Sched, bool ALIGN_EPI, bool SP2, bool GATHER>
; DI void gemm_phase(LAS unsigned char* lds, const Gemm g, const Sched& S, const Epi& E) {
;     ...
;     for (;;) {
;         const bool has_next = S.next(ui + 1, nxt);
;         const char* nA = (has_next && !GATHER) ? (const char*)g.A + (size_t)nxt.pm * tstep : cA; const char* nB = has_next ? (const char*)g.Bt + (size_t)nxt.pn * tstep : cB;
;         if constexpr (GATHER) { if (has_next) { PG8_GATHER(nxt, gN); } else {
; #pragma unroll
;             for (int h = 0; h < 2; ++h) { gN[h][0] = gC[h][0]; gN[h][1] = gC[h][1]; } } }
;         for (int t = 0; t < nt; t += 2) {
;             if constexpr (Epi::MID_T >= 0) { if (t == Epi::MID_T) { E.mid(acc, cur, wr, wc, fr, fq); PG8_SCHED; } }
;             const bool last = (t == nt - 2);
;             const char* a1 = cA + (size_t)(t + 1) * kstep;
;             const char* a2 = last ? nA : cA + (size_t)(t + 2) * kstep; const char* b2 = last ? nB : cB + (size_t)(t + 2) * kstep;
;             const char* a3 = a2 + kstep; const char* b3 = b2 + kstep;
;             unsigned x00 = gC[0][0], x01 = gC[0][1], x10 = gC[1][0], x11 = gC[1][1];
;             if constexpr (GATHER) { if (last) { x00 = gN[0][0]; x01 = gN[0][1]; x10 = gN[1][0]; x11 = gN[1][1]; } }
;             PG8_LDB(B0, 0, 0); PG8_LDB(B1, 0, 1); PG8_SCHED; PG8_LDA(At, 0, 0); PG8_STAGE2(PG8_SA(1, 1), a1 + hstepA, gC[1][0], gC[1][1]);
;             PG8_WAIT_V(8); PG8_WAIT_L(0); PG8_BAR; PG8_MMA(0, 0, At, B0); PG8_MMA(0, 1, At, B1); PG8_BAR; PG8_SCHED;
;             PG8_LDA(At, 0, 1); PG8_STAGE(PG8_SB(0, 0), b2, voffB); PG8_STAGE(PG8_SB(0, 1), b2 + hstep, voffB); PG8_STAGE2(PG8_SA(0, 0), a2, x00, x01);
;             PG8_WAIT_V(8); PG8_WAIT_L(0); PG8_BAR; PG8_MMA(1, 0, At, B0); PG8_MMA(1, 1, At, B1); PG8_BAR; PG8_SCHED;
;             PG8_LDB(B0, 1, 0); PG8_LDB(B1, 1, 1); PG8_SCHED; PG8_LDA(At, 1, 0); PG8_STAGE2(PG8_SA(0, 1), a2 + hstepA, x10, x11);
;             PG8_WAIT_V(8); PG8_WAIT_L(0); PG8_BAR; PG8_MMA(0, 0, At, B0); PG8_MMA(0, 1, At, B1); PG8_BAR; PG8_SCHED;
;             PG8_LDA(At, 1, 1); PG8_STAGE(PG8_SB(1, 0), b3, voffB); PG8_STAGE(PG8_SB(1, 1), b3 + hstep, voffB); PG8_STAGE2(PG8_SA(1, 0), a3, x00, x01);
;             PG8_WAIT_V(8); PG8_WAIT_L(0); PG8_BAR; PG8_MMA(1, 0, At, B0); PG8_MMA(1, 1, At, B1); PG8_BAR; PG8_SCHED;
.LBB0_673:
	s_ashr_i32 s27, s26, 31
	s_lshl_b64 s[28:29], s[26:27], 20
	s_add_u32 s28, s38, s28
	s_addc_u32 s29, s39, s29
	s_and_b64 s[30:31], s[4:5], exec
	s_cselect_b32 s27, s29, s37
	s_cselect_b32 s57, s28, s36
	s_ashr_i32 s25, s24, 31
	s_lshl_b64 s[30:31], s[24:25], 20
	s_add_u32 s30, s44, s30
	s_addc_u32 s31, s45, s31
	s_and_b64 s[42:43], s[4:5], exec
	s_cselect_b32 s25, s31, s41
	s_cselect_b32 s63, s30, s40
	s_add_u32 s36, s36, 0x80080
	s_addc_u32 s37, s37, 0
	s_add_u32 s64, s40, 0x100
	s_addc_u32 s65, s41, 0
	s_mov_b32 s66, -2
	ds_read_b128 v[146:149], v154
	ds_read_b128 v[158:161], v154 offset:1024
	ds_read_b128 v[162:165], v154 offset:2048
	ds_read_b128 v[166:169], v154 offset:3072
	ds_read_b128 v[170:173], v155
	ds_read_b128 v[174:177], v155 offset:1024
	ds_read_b128 v[178:181], v155 offset:2048
	ds_read_b128 v[182:185], v155 offset:3072
	s_add_u32 s40, s36, 0xfff80080
	s_addc_u32 s41, s37, -1
	s_cmp_eq_u32 s66, 28
	s_cselect_b32 s43, s27, s41
	s_cselect_b32 s42, s57, s40
	s_cselect_b32 s41, s25, s65
	s_cselect_b32 s40, s63, s64
	v_lshl_add_u64 v[150:151], s[36:37], 0, v[138:139]
	s_add_i32 m0, s35, 0xc000
	ds_read_b128 v[186:189], v156
	ds_read_b128 v[190:193], v156 offset:1024
	ds_read_b128 v[194:197], v156 offset:2048
	ds_read_b128 v[198:201], v156 offset:3072
	ds_read_b128 v[202:205], v156 offset:4096
	ds_read_b128 v[206:209], v156 offset:5120
	ds_read_b128 v[210:213], v156 offset:6144
	ds_read_b128 v[214:217], v156 offset:7168
	global_load_lds_dwordx4 v[150:151], off
	v_lshl_add_u64 v[150:151], s[36:37], 0, v[140:141]
	s_add_i32 m0, s35, 0xe000
	s_nop 0
	global_load_lds_dwordx4 v[150:151], off
	s_waitcnt vmcnt(8)
	s_waitcnt lgkmcnt(0)
	s_barrier
	s_setprio 1
	s_waitcnt lgkmcnt(0)
	v_mfma_f32_16x16x32_bf16 v[126:129], v[146:149], v[186:189], 0
	v_mfma_f32_16x16x32_bf16 v[122:125], v[162:165], v[186:189], 0
	v_mfma_f32_16x16x32_bf16 v[110:113], v[146:149], v[194:197], 0
	v_mfma_f32_16x16x32_bf16 v[106:109], v[162:165], v[194:197], 0
	v_mfma_f32_16x16x32_bf16 v[94:97], v[146:149], v[202:205], 0
	v_mfma_f32_16x16x32_bf16 v[90:93], v[162:165], v[202:205], 0
	v_mfma_f32_16x16x32_bf16 v[78:81], v[146:149], v[210:213], 0
	v_mfma_f32_16x16x32_bf16 v[74:77], v[162:165], v[210:213], 0
	v_mfma_f32_16x16x32_bf16 v[126:129], v[158:161], v[190:193], v[126:129]
	v_mfma_f32_16x16x32_bf16 v[122:125], v[166:169], v[190:193], v[122:125]
	v_mfma_f32_16x16x32_bf16 v[110:113], v[158:161], v[198:201], v[110:113]
	v_mfma_f32_16x16x32_bf16 v[106:109], v[166:169], v[198:201], v[106:109]
	v_mfma_f32_16x16x32_bf16 v[94:97], v[158:161], v[206:209], v[94:97]
	v_mfma_f32_16x16x32_bf16 v[90:93], v[166:169], v[206:209], v[90:93]
	v_mfma_f32_16x16x32_bf16 v[78:81], v[158:161], v[214:217], v[78:81]
	v_mfma_f32_16x16x32_bf16 v[74:77], v[166:169], v[214:217], v[74:77]
	v_mfma_f32_16x16x32_bf16 v[118:121], v[170:173], v[186:189], 0
	v_mfma_f32_16x16x32_bf16 v[114:117], v[178:181], v[186:189], 0
	v_mfma_f32_16x16x32_bf16 v[102:105], v[170:173], v[194:197], 0
	v_mfma_f32_16x16x32_bf16 v[98:101], v[178:181], v[194:197], 0
	v_mfma_f32_16x16x32_bf16 v[86:89], v[170:173], v[202:205], 0
	v_mfma_f32_16x16x32_bf16 v[82:85], v[178:181], v[202:205], 0
	v_mfma_f32_16x16x32_bf16 v[70:73], v[170:173], v[210:213], 0
	v_mfma_f32_16x16x32_bf16 v[66:69], v[178:181], v[210:213], 0
	v_mfma_f32_16x16x32_bf16 v[118:121], v[174:177], v[190:193], v[118:121]
	v_mfma_f32_16x16x32_bf16 v[114:117], v[182:185], v[190:193], v[114:117]
	v_mfma_f32_16x16x32_bf16 v[102:105], v[174:177], v[198:201], v[102:105]
	v_mfma_f32_16x16x32_bf16 v[98:101], v[182:185], v[198:201], v[98:101]
	v_mfma_f32_16x16x32_bf16 v[86:89], v[174:177], v[206:209], v[86:89]
	v_mfma_f32_16x16x32_bf16 v[82:85], v[182:185], v[206:209], v[82:85]
	v_mfma_f32_16x16x32_bf16 v[70:73], v[174:177], v[214:217], v[70:73]
	v_mfma_f32_16x16x32_bf16 v[66:69], v[182:185], v[214:217], v[66:69]
	s_setprio 0
	s_barrier
	s_add_i32 s62, s54, s46
	v_lshl_add_u64 v[150:151], s[40:41], 0, v[132:133]
	s_mov_b32 m0, s62
	ds_read_b128 v[186:189], v156 offset:16384
	ds_read_b128 v[190:193], v156 offset:17408
	ds_read_b128 v[194:197], v156 offset:18432
	ds_read_b128 v[198:201], v156 offset:19456
	ds_read_b128 v[202:205], v156 offset:20480
	ds_read_b128 v[206:209], v156 offset:21504
	ds_read_b128 v[210:213], v156 offset:22528
	ds_read_b128 v[214:217], v156 offset:23552
	global_load_lds_dwordx4 v[150:151], off
	s_add_i32 m0, s62, 0x2000
	s_add_u32 s68, s40, 0x80000
	v_lshl_add_u64 v[218:219], s[40:41], 0, v[136:137]
	s_addc_u32 s69, s41, 0
	s_add_i32 s62, s55, s46
	global_load_lds_dwordx4 v[218:219], off
	v_lshl_add_u64 v[220:221], s[68:69], 0, v[132:133]
	s_mov_b32 m0, s62
	v_lshl_add_u64 v[222:223], s[42:43], 0, v[134:135]
	global_load_lds_dwordx4 v[220:221], off
	v_lshl_add_u64 v[220:221], s[68:69], 0, v[136:137]
	s_add_i32 m0, s62, 0x2000
	s_nop 0
	global_load_lds_dwordx4 v[220:221], off
	v_lshl_add_u64 v[220:221], s[42:43], 0, v[130:131]
	s_mov_b32 m0, s35
	s_nop 0
	global_load_lds_dwordx4 v[220:221], off
	s_mov_b32 m0, s47
	s_nop 0
	global_load_lds_dwordx4 v[222:223], off
	s_waitcnt vmcnt(8)
	s_waitcnt lgkmcnt(0)
	s_barrier
; #define PG8_STAGE2(bufoff, gbase, v0, v1) do { \
;         __builtin_amdgcn_global_load_lds((const unsigned*)((const char*)(gbase) + (v0)), (LAS unsigned*)(lds + (bufoff) + ldsw), 16, 0, 0); \
;         __builtin_amdgcn_global_load_lds((const unsigned*)((const char*)(gbase) + (v1)), (LAS unsigned*)(lds + (bufoff) + ldsw + 8192), 16, 0, 0); } while (0)
; #define PG8_STAGE(bufoff, gbase, voff) PG8_STAGE2(bufoff, gbase, (voff)[0], (voff)[1])
; #define PG8_LDA(dst, b, h) do { _Pragma("unroll") for (int m = 0; m < 4; ++m) _Pragma("unroll") for (int k = 0; k < 2; ++k) dst[m][k] = *(const LAS bf16x8*)(lds + PG8_SA(b, h) + aoff + m * 2048 + k * 1024); } while (0)
; #define PG8_LDB(dst, b, h) do { _Pragma("unroll") for (int n = 0; n < 2; ++n) _Pragma("unroll") for (int k = 0; k < 2; ++k) dst[n][k] = *(const LAS bf16x8*)(lds + PG8_SB(b, h) + boff + n * 2048 + k * 1024); } while (0)
; #define PG8_WAIT_V(n) asm volatile("s_waitcnt vmcnt(" #n ")" ::: "memory")
; #define PG8_WAIT_L(n) asm volatile("s_waitcnt lgkmcnt(" #n ")" ::: "memory")
; #define PG8_BAR __builtin_amdgcn_s_barrier()
; #define PG8_SCHED __builtin_amdgcn_sched_barrier(0)
; template <class Epi, class Sched, bool ALIGN_EPI, bool SP2, bool GATHER>
; DI void gemm_phase(LAS unsigned char* lds, const Gemm g, const Sched& S, const Epi& E) {
;     ...
;             PG8_LDB(B0, 0, 0); PG8_LDB(B1, 0, 1); PG8_SCHED; PG8_LDA(At, 0, 0); PG8_STAGE2(PG8_SA(1, 1), a1 + hstepA, gC[1][0], gC[1][1]);
;             PG8_WAIT_V(8); PG8_WAIT_L(0); PG8_BAR; PG8_MMA(0, 0, At, B0); PG8_MMA(0, 1, At, B1); PG8_BAR; PG8_SCHED;
;             PG8_LDA(At, 0, 1); PG8_STAGE(PG8_SB(0, 0), b2, voffB); PG8_STAGE(PG8_SB(0, 1), b2 + hstep, voffB); PG8_STAGE2(PG8_SA(0, 0), a2, x00, x01);
;             PG8_WAIT_V(8); PG8_WAIT_L(0); PG8_BAR; PG8_MMA(1, 0, At, B0); PG8_MMA(1, 1, At, B1); PG8_BAR; PG8_SCHED;
;             PG8_LDB(B0, 1, 0); PG8_LDB(B1, 1, 1); PG8_SCHED; PG8_LDA(At, 1, 0); PG8_STAGE2(PG8_SA(0, 1), a2 + hstepA, x10, x11);
;             PG8_WAIT_V(8); PG8_WAIT_L(0); PG8_BAR; PG8_MMA(0, 0, At, B0); PG8_MMA(0, 1, At, B1); PG8_BAR; PG8_SCHED;
;             PG8_LDA(At, 1, 1); PG8_STAGE(PG8_SB(1, 0), b3, voffB); PG8_STAGE(PG8_SB(1, 1), b3 + hstep, voffB); PG8_STAGE2(PG8_SA(1, 0), a3, x00, x01);
;             PG8_WAIT_V(8); PG8_WAIT_L(0); PG8_BAR; PG8_MMA(1, 0, At, B0); PG8_MMA(1, 1, At, B1); PG8_BAR; PG8_SCHED;
	s_setprio 1
	s_waitcnt lgkmcnt(0)
	v_mfma_f32_16x16x32_bf16 v[62:65], v[146:149], v[186:189], 0
	v_mfma_f32_16x16x32_bf16 v[58:61], v[162:165], v[186:189], 0
	v_mfma_f32_16x16x32_bf16 v[46:49], v[146:149], v[194:197], 0
	v_mfma_f32_16x16x32_bf16 v[42:45], v[162:165], v[194:197], 0
	v_mfma_f32_16x16x32_bf16 v[22:25], v[146:149], v[202:205], 0
	v_mfma_f32_16x16x32_bf16 v[18:21], v[162:165], v[202:205], 0
	v_mfma_f32_16x16x32_bf16 v[6:9], v[146:149], v[210:213], 0
	v_mfma_f32_16x16x32_bf16 v[2:5], v[162:165], v[210:213], 0
	v_mfma_f32_16x16x32_bf16 v[62:65], v[158:161], v[190:193], v[62:65]
	v_mfma_f32_16x16x32_bf16 v[58:61], v[166:169], v[190:193], v[58:61]
	v_mfma_f32_16x16x32_bf16 v[46:49], v[158:161], v[198:201], v[46:49]
	v_mfma_f32_16x16x32_bf16 v[42:45], v[166:169], v[198:201], v[42:45]
	v_mfma_f32_16x16x32_bf16 v[22:25], v[158:161], v[206:209], v[22:25]
	v_mfma_f32_16x16x32_bf16 v[18:21], v[166:169], v[206:209], v[18:21]
	v_mfma_f32_16x16x32_bf16 v[6:9], v[158:161], v[214:217], v[6:9]
	v_mfma_f32_16x16x32_bf16 v[2:5], v[166:169], v[214:217], v[2:5]
	v_mfma_f32_16x16x32_bf16 v[54:57], v[170:173], v[186:189], 0
	v_mfma_f32_16x16x32_bf16 v[50:53], v[178:181], v[186:189], 0
	v_mfma_f32_16x16x32_bf16 v[30:33], v[170:173], v[194:197], 0
	v_mfma_f32_16x16x32_bf16 v[26:29], v[178:181], v[194:197], 0
	v_mfma_f32_16x16x32_bf16 v[34:37], v[170:173], v[202:205], 0
	v_mfma_f32_16x16x32_bf16 v[38:41], v[178:181], v[202:205], 0
	v_mfma_f32_16x16x32_bf16 v[10:13], v[170:173], v[210:213], 0
	v_mfma_f32_16x16x32_bf16 v[14:17], v[178:181], v[210:213], 0
	v_mfma_f32_16x16x32_bf16 v[54:57], v[174:177], v[190:193], v[54:57]
	v_mfma_f32_16x16x32_bf16 v[50:53], v[182:185], v[190:193], v[50:53]
	v_mfma_f32_16x16x32_bf16 v[30:33], v[174:177], v[198:201], v[30:33]
	v_mfma_f32_16x16x32_bf16 v[26:29], v[182:185], v[198:201], v[26:29]
	v_mfma_f32_16x16x32_bf16 v[34:37], v[174:177], v[206:209], v[34:37]
	v_mfma_f32_16x16x32_bf16 v[38:41], v[182:185], v[206:209], v[38:41]
	v_mfma_f32_16x16x32_bf16 v[10:13], v[174:177], v[214:217], v[10:13]
	v_mfma_f32_16x16x32_bf16 v[14:17], v[182:185], v[214:217], v[14:17]
	s_setprio 0
	s_barrier
	s_add_i32 s62, 0, 0x18000
	v_add_u32_e32 v157, s62, v152
	s_add_i32 s67, 0, 0x1c000
	ds_read_b128 v[146:149], v157
	ds_read_b128 v[158:161], v157 offset:1024
	ds_read_b128 v[162:165], v157 offset:2048
	ds_read_b128 v[166:169], v157 offset:3072
	v_add_u32_e32 v157, s67, v152
	ds_read_b128 v[170:173], v157
	ds_read_b128 v[174:177], v157 offset:1024
	ds_read_b128 v[178:181], v157 offset:2048
	ds_read_b128 v[182:185], v157 offset:3072
	s_add_u32 s42, s42, 0x80000
	s_addc_u32 s43, s43, 0
	s_mov_b32 m0, s48
	v_lshl_add_u64 v[224:225], s[42:43], 0, v[130:131]
	ds_read_b128 v[186:189], v156 offset:32768
	ds_read_b128 v[190:193], v156 offset:33792
	ds_read_b128 v[194:197], v156 offset:34816
	ds_read_b128 v[198:201], v156 offset:35840
	ds_read_b128 v[202:205], v156 offset:36864
	ds_read_b128 v[206:209], v156 offset:37888
	ds_read_b128 v[210:213], v156 offset:38912
	ds_read_b128 v[214:217], v156 offset:39936
	global_load_lds_dwordx4 v[224:225], off
	v_lshl_add_u64 v[224:225], s[42:43], 0, v[134:135]
	s_mov_b32 m0, s49
	s_nop 0
	global_load_lds_dwordx4 v[224:225], off
	s_waitcnt vmcnt(8)
	s_waitcnt lgkmcnt(0)
	s_barrier
	s_setprio 1
	s_waitcnt lgkmcnt(0)
	v_mfma_f32_16x16x32_bf16 v[126:129], v[146:149], v[186:189], v[126:129]
	v_mfma_f32_16x16x32_bf16 v[122:125], v[162:165], v[186:189], v[122:125]
	v_mfma_f32_16x16x32_bf16 v[110:113], v[146:149], v[194:197], v[110:113]
	v_mfma_f32_16x16x32_bf16 v[106:109], v[162:165], v[194:197], v[106:109]
	v_mfma_f32_16x16x32_bf16 v[94:97], v[146:149], v[202:205], v[94:97]
	v_mfma_f32_16x16x32_bf16 v[90:93], v[162:165], v[202:205], v[90:93]
	v_mfma_f32_16x16x32_bf16 v[78:81], v[146:149], v[210:213], v[78:81]
	v_mfma_f32_16x16x32_bf16 v[74:77], v[162:165], v[210:213], v[74:77]
	v_mfma_f32_16x16x32_bf16 v[126:129], v[158:161], v[190:193], v[126:129]
	v_mfma_f32_16x16x32_bf16 v[122:125], v[166:169], v[190:193], v[122:125]
	v_mfma_f32_16x16x32_bf16 v[110:113], v[158:161], v[198:201], v[110:113]
	v_mfma_f32_16x16x32_bf16 v[106:109], v[166:169], v[198:201], v[106:109]
	v_mfma_f32_16x16x32_bf16 v[94:97], v[158:161], v[206:209], v[94:97]
	v_mfma_f32_16x16x32_bf16 v[90:93], v[166:169], v[206:209], v[90:93]
	v_mfma_f32_16x16x32_bf16 v[78:81], v[158:161], v[214:217], v[78:81]
	v_mfma_f32_16x16x32_bf16 v[74:77], v[166:169], v[214:217], v[74:77]
	v_mfma_f32_16x16x32_bf16 v[118:121], v[170:173], v[186:189], v[118:121]
	v_mfma_f32_16x16x32_bf16 v[114:117], v[178:181], v[186:189], v[114:117]
	v_mfma_f32_16x16x32_bf16 v[102:105], v[170:173], v[194:197], v[102:105]
	v_mfma_f32_16x16x32_bf16 v[98:101], v[178:181], v[194:197], v[98:101]
	v_mfma_f32_16x16x32_bf16 v[86:89], v[170:173], v[202:205], v[86:89]
	v_mfma_f32_16x16x32_bf16 v[82:85], v[178:181], v[202:205], v[82:85]
	v_mfma_f32_16x16x32_bf16 v[70:73], v[170:173], v[210:213], v[70:73]
	v_mfma_f32_16x16x32_bf16 v[66:69], v[178:181], v[210:213], v[66:69]
	v_mfma_f32_16x16x32_bf16 v[118:121], v[174:177], v[190:193], v[118:121]
	v_mfma_f32_16x16x32_bf16 v[114:117], v[182:185], v[190:193], v[114:117]
	v_mfma_f32_16x16x32_bf16 v[102:105], v[174:177], v[198:201], v[102:105]
	v_mfma_f32_16x16x32_bf16 v[98:101], v[182:185], v[198:201], v[98:101]
	v_mfma_f32_16x16x32_bf16 v[86:89], v[174:177], v[206:209], v[86:89]
	v_mfma_f32_16x16x32_bf16 v[82:85], v[182:185], v[206:209], v[82:85]
	v_mfma_f32_16x16x32_bf16 v[70:73], v[174:177], v[214:217], v[70:73]
	v_mfma_f32_16x16x32_bf16 v[66:69], v[182:185], v[214:217], v[66:69]
	s_setprio 0
	s_barrier
; #define PG8_STAGE2(bufoff, gbase, v0, v1) do { \
;         __builtin_amdgcn_global_load_lds((const unsigned*)((const char*)(gbase) + (v0)), (LAS unsigned*)(lds + (bufoff) + ldsw), 16, 0, 0); \
;         __builtin_amdgcn_global_load_lds((const unsigned*)((const char*)(gbase) + (v1)), (LAS unsigned*)(lds + (bufoff) + ldsw + 8192), 16, 0, 0); } while (0)
; #define PG8_STAGE(bufoff, gbase, voff) PG8_STAGE2(bufoff, gbase, (voff)[0], (voff)[1])
; #define PG8_BAR __builtin_amdgcn_s_barrier()
; template <class Epi, class Sched, bool ALIGN_EPI, bool SP2, bool GATHER>
; DI void gemm_phase(LAS unsigned char* lds, const Gemm g, const Sched& S, const Epi& E) {
;     ...
;         for (int t = 0; t < nt; t += 2) {
;             if constexpr (Epi::MID_T >= 0) { if (t == Epi::MID_T) { E.mid(acc, cur, wr, wc, fr, fq); PG8_SCHED; } }
;             const bool last = (t == nt - 2);
;             const char* a1 = cA + (size_t)(t + 1) * kstep;
;             const char* a2 = last ? nA : cA + (size_t)(t + 2) * kstep; const char* b2 = last ? nB : cB + (size_t)(t + 2) * kstep;
;             const char* a3 = a2 + kstep; const char* b3 = b2 + kstep;
;             unsigned x00 = gC[0][0], x01 = gC[0][1], x10 = gC[1][0], x11 = gC[1][1];
;             if constexpr (GATHER) { if (last) { x00 = gN[0][0]; x01 = gN[0][1]; x10 = gN[1][0]; x11 = gN[1][1]; } }
;             PG8_LDB(B0, 0, 0); PG8_LDB(B1, 0, 1); PG8_SCHED; PG8_LDA(At, 0, 0); PG8_STAGE2(PG8_SA(1, 1), a1 + hstepA, gC[1][0], gC[1][1]);
;             PG8_WAIT_V(8); PG8_WAIT_L(0); PG8_BAR; PG8_MMA(0, 0, At, B0); PG8_MMA(0, 1, At, B1); PG8_BAR; PG8_SCHED;
;             PG8_LDA(At, 0, 1); PG8_STAGE(PG8_SB(0, 0), b2, voffB); PG8_STAGE(PG8_SB(0, 1), b2 + hstep, voffB); PG8_STAGE2(PG8_SA(0, 0), a2, x00, x01);
;             PG8_WAIT_V(8); PG8_WAIT_L(0); PG8_BAR; PG8_MMA(1, 0, At, B0); PG8_MMA(1, 1, At, B1); PG8_BAR; PG8_SCHED;
;             PG8_LDB(B0, 1, 0); PG8_LDB(B1, 1, 1); PG8_SCHED; PG8_LDA(At, 1, 0); PG8_STAGE2(PG8_SA(0, 1), a2 + hstepA, x10, x11);
;             PG8_WAIT_V(8); PG8_WAIT_L(0); PG8_BAR; PG8_MMA(0, 0, At, B0); PG8_MMA(0, 1, At, B1); PG8_BAR; PG8_SCHED;
;             PG8_LDA(At, 1, 1); PG8_STAGE(PG8_SB(1, 0), b3, voffB); PG8_STAGE(PG8_SB(1, 1), b3 + hstep, voffB); PG8_STAGE2(PG8_SA(1, 0), a3, x00, x01);
;             PG8_WAIT_V(8); PG8_WAIT_L(0); PG8_BAR; PG8_MMA(1, 0, At, B0); PG8_MMA(1, 1, At, B1); PG8_BAR; PG8_SCHED;
	s_add_i32 s42, s62, s46
	v_lshl_add_u64 v[150:151], v[150:151], 0, s[12:13]
	s_mov_b32 m0, s42
	ds_read_b128 v[186:189], v156 offset:49152
	ds_read_b128 v[190:193], v156 offset:50176
	ds_read_b128 v[194:197], v156 offset:51200
	ds_read_b128 v[198:201], v156 offset:52224
	ds_read_b128 v[202:205], v156 offset:53248
	ds_read_b128 v[206:209], v156 offset:54272
	ds_read_b128 v[210:213], v156 offset:55296
	ds_read_b128 v[214:217], v156 offset:56320
	global_load_lds_dwordx4 v[150:151], off
	s_add_i32 m0, s42, 0x2000
	s_add_u32 s40, s40, 0x80080
	v_lshl_add_u64 v[150:151], v[218:219], 0, s[12:13]
	s_addc_u32 s41, s41, 0
	s_add_i32 s42, s67, s46
	global_load_lds_dwordx4 v[150:151], off
	v_lshl_add_u64 v[150:151], s[40:41], 0, v[132:133]
	s_mov_b32 m0, s42
	s_nop 0
	global_load_lds_dwordx4 v[150:151], off
	v_lshl_add_u64 v[150:151], s[40:41], 0, v[136:137]
	s_add_i32 m0, s42, 0x2000
	s_nop 0
	global_load_lds_dwordx4 v[150:151], off
	v_lshl_add_u64 v[150:151], v[220:221], 0, s[12:13]
	s_mov_b32 m0, s51
	s_nop 0
	global_load_lds_dwordx4 v[150:151], off
	v_lshl_add_u64 v[150:151], v[222:223], 0, s[12:13]
	s_mov_b32 m0, s52
	s_nop 0
	global_load_lds_dwordx4 v[150:151], off
	s_waitcnt vmcnt(8)
	s_waitcnt lgkmcnt(0)
	s_barrier
	s_setprio 1
	s_waitcnt lgkmcnt(0)
	v_mfma_f32_16x16x32_bf16 v[62:65], v[146:149], v[186:189], v[62:65]
	v_mfma_f32_16x16x32_bf16 v[58:61], v[162:165], v[186:189], v[58:61]
	v_mfma_f32_16x16x32_bf16 v[46:49], v[146:149], v[194:197], v[46:49]
	v_mfma_f32_16x16x32_bf16 v[42:45], v[162:165], v[194:197], v[42:45]
	v_mfma_f32_16x16x32_bf16 v[22:25], v[146:149], v[202:205], v[22:25]
	v_mfma_f32_16x16x32_bf16 v[18:21], v[162:165], v[202:205], v[18:21]
	v_mfma_f32_16x16x32_bf16 v[6:9], v[146:149], v[210:213], v[6:9]
	v_mfma_f32_16x16x32_bf16 v[2:5], v[162:165], v[210:213], v[2:5]
	v_mfma_f32_16x16x32_bf16 v[62:65], v[158:161], v[190:193], v[62:65]
	v_mfma_f32_16x16x32_bf16 v[58:61], v[166:169], v[190:193], v[58:61]
	v_mfma_f32_16x16x32_bf16 v[46:49], v[158:161], v[198:201], v[46:49]
	v_mfma_f32_16x16x32_bf16 v[42:45], v[166:169], v[198:201], v[42:45]
	v_mfma_f32_16x16x32_bf16 v[22:25], v[158:161], v[206:209], v[22:25]
	v_mfma_f32_16x16x32_bf16 v[18:21], v[166:169], v[206:209], v[18:21]
	v_mfma_f32_16x16x32_bf16 v[6:9], v[158:161], v[214:217], v[6:9]
	v_mfma_f32_16x16x32_bf16 v[2:5], v[166:169], v[214:217], v[2:5]
	v_mfma_f32_16x16x32_bf16 v[54:57], v[170:173], v[186:189], v[54:57]
	v_mfma_f32_16x16x32_bf16 v[50:53], v[178:181], v[186:189], v[50:53]
	v_mfma_f32_16x16x32_bf16 v[30:33], v[170:173], v[194:197], v[30:33]
	v_mfma_f32_16x16x32_bf16 v[26:29], v[178:181], v[194:197], v[26:29]
	v_mfma_f32_16x16x32_bf16 v[34:37], v[170:173], v[202:205], v[34:37]
	v_mfma_f32_16x16x32_bf16 v[38:41], v[178:181], v[202:205], v[38:41]
	v_mfma_f32_16x16x32_bf16 v[10:13], v[170:173], v[210:213], v[10:13]
	v_mfma_f32_16x16x32_bf16 v[14:17], v[178:181], v[210:213], v[14:17]
	v_mfma_f32_16x16x32_bf16 v[54:57], v[174:177], v[190:193], v[54:57]
	v_mfma_f32_16x16x32_bf16 v[50:53], v[182:185], v[190:193], v[50:53]
	v_mfma_f32_16x16x32_bf16 v[30:33], v[174:177], v[198:201], v[30:33]
	v_mfma_f32_16x16x32_bf16 v[26:29], v[182:185], v[198:201], v[26:29]
	v_mfma_f32_16x16x32_bf16 v[34:37], v[174:177], v[206:209], v[34:37]
	v_mfma_f32_16x16x32_bf16 v[38:41], v[182:185], v[206:209], v[38:41]
	v_mfma_f32_16x16x32_bf16 v[10:13], v[174:177], v[214:217], v[10:13]
	v_mfma_f32_16x16x32_bf16 v[14:17], v[182:185], v[214:217], v[14:17]
	s_setprio 0
	s_barrier
	s_add_i32 s66, s66, 2
	s_add_u32 s36, s36, 0x100
	s_addc_u32 s37, s37, 0
	s_add_u32 s64, s64, 0x100
	s_addc_u32 s65, s65, 0
	s_cmp_gt_u32 s66, 29
	s_cbranch_scc1 .Lpeel_exit_p6
.LBB0_674:
	ds_read_b128 v[146:149], v154
	ds_read_b128 v[158:161], v154 offset:1024
	ds_read_b128 v[162:165], v154 offset:2048
	ds_read_b128 v[166:169], v154 offset:3072
	ds_read_b128 v[170:173], v155
	ds_read_b128 v[174:177], v155 offset:1024
	ds_read_b128 v[178:181], v155 offset:2048
	ds_read_b128 v[182:185], v155 offset:3072
	s_add_u32 s40, s36, 0xfff80080
	s_addc_u32 s41, s37, -1
	s_cmp_eq_u32 s66, 28
	s_cselect_b32 s43, s27, s41
	s_cselect_b32 s42, s57, s40
	s_cselect_b32 s41, s25, s65
	s_cselect_b32 s40, s63, s64
	v_lshl_add_u64 v[150:151], s[36:37], 0, v[138:139]
	s_add_i32 m0, s35, 0xc000
	ds_read_b128 v[186:189], v156
	ds_read_b128 v[190:193], v156 offset:1024
	ds_read_b128 v[194:197], v156 offset:2048
	ds_read_b128 v[198:201], v156 offset:3072
	ds_read_b128 v[202:205], v156 offset:4096
	ds_read_b128 v[206:209], v156 offset:5120
	ds_read_b128 v[210:213], v156 offset:6144
	ds_read_b128 v[214:217], v156 offset:7168
	global_load_lds_dwordx4 v[150:151], off
	v_lshl_add_u64 v[150:151], s[36:37], 0, v[140:141]
	s_add_i32 m0, s35, 0xe000
	s_nop 0
	global_load_lds_dwordx4 v[150:151], off
	s_waitcnt vmcnt(8)
	s_waitcnt lgkmcnt(0)
	s_barrier
; #define PG8_STAGE2(bufoff, gbase, v0, v1) do { \
;         __builtin_amdgcn_global_load_lds((const unsigned*)((const char*)(gbase) + (v0)), (LAS unsigned*)(lds + (bufoff) + ldsw), 16, 0, 0); \
;         __builtin_amdgcn_global_load_lds((const unsigned*)((const char*)(gbase) + (v1)), (LAS unsigned*)(lds + (bufoff) + ldsw + 8192), 16, 0, 0); } while (0)
; #define PG8_STAGE(bufoff, gbase, voff) PG8_STAGE2(bufoff, gbase, (voff)[0], (voff)[1])
; #define PG8_LDA(dst, b, h) do { _Pragma("unroll") for (int m = 0; m < 4; ++m) _Pragma("unroll") for (int k = 0; k < 2; ++k) dst[m][k] = *(const LAS bf16x8*)(lds + PG8_SA(b, h) + aoff + m * 2048 + k * 1024); } while (0)
; #define PG8_LDB(dst, b, h) do { _Pragma("unroll") for (int n = 0; n < 2; ++n) _Pragma("unroll") for (int k = 0; k < 2; ++k) dst[n][k] = *(const LAS bf16x8*)(lds + PG8_SB(b, h) + boff + n * 2048 + k * 1024); } while (0)
; #define PG8_WAIT_V(n) asm volatile("s_waitcnt vmcnt(" #n ")" ::: "memory")
; #define PG8_WAIT_L(n) asm volatile("s_waitcnt lgkmcnt(" #n ")" ::: "memory")
; #define PG8_BAR __builtin_amdgcn_s_barrier()
; #define PG8_SCHED __builtin_amdgcn_sched_barrier(0)
; template <class Epi, class Sched, bool ALIGN_EPI, bool SP2, bool GATHER>
; DI void gemm_phase(LAS unsigned char* lds, const Gemm g, const Sched& S, const Epi& E) {
;     ...
;             PG8_LDB(B0, 0, 0); PG8_LDB(B1, 0, 1); PG8_SCHED; PG8_LDA(At, 0, 0); PG8_STAGE2(PG8_SA(1, 1), a1 + hstepA, gC[1][0], gC[1][1]);
;             PG8_WAIT_V(8); PG8_WAIT_L(0); PG8_BAR; PG8_MMA(0, 0, At, B0); PG8_MMA(0, 1, At, B1); PG8_BAR; PG8_SCHED;
;             PG8_LDA(At, 0, 1); PG8_STAGE(PG8_SB(0, 0), b2, voffB); PG8_STAGE(PG8_SB(0, 1), b2 + hstep, voffB); PG8_STAGE2(PG8_SA(0, 0), a2, x00, x01);
;             PG8_WAIT_V(8); PG8_WAIT_L(0); PG8_BAR; PG8_MMA(1, 0, At, B0); PG8_MMA(1, 1, At, B1); PG8_BAR; PG8_SCHED;
;             PG8_LDB(B0, 1, 0); PG8_LDB(B1, 1, 1); PG8_SCHED; PG8_LDA(At, 1, 0); PG8_STAGE2(PG8_SA(0, 1), a2 + hstepA, x10, x11);
;             PG8_WAIT_V(8); PG8_WAIT_L(0); PG8_BAR; PG8_MMA(0, 0, At, B0); PG8_MMA(0, 1, At, B1); PG8_BAR; PG8_SCHED;
;             PG8_LDA(At, 1, 1); PG8_STAGE(PG8_SB(1, 0), b3, voffB); PG8_STAGE(PG8_SB(1, 1), b3 + hstep, voffB); PG8_STAGE2(PG8_SA(1, 0), a3, x00, x01);
;             PG8_WAIT_V(8); PG8_WAIT_L(0); PG8_BAR; PG8_MMA(1, 0, At, B0); PG8_MMA(1, 1, At, B1); PG8_BAR; PG8_SCHED;
	s_setprio 1
	s_waitcnt lgkmcnt(0)
	v_mfma_f32_16x16x32_bf16 v[126:129], v[146:149], v[186:189], v[126:129]
	v_mfma_f32_16x16x32_bf16 v[122:125], v[162:165], v[186:189], v[122:125]
	v_mfma_f32_16x16x32_bf16 v[110:113], v[146:149], v[194:197], v[110:113]
	v_mfma_f32_16x16x32_bf16 v[106:109], v[162:165], v[194:197], v[106:109]
	v_mfma_f32_16x16x32_bf16 v[94:97], v[146:149], v[202:205], v[94:97]
	v_mfma_f32_16x16x32_bf16 v[90:93], v[162:165], v[202:205], v[90:93]
	v_mfma_f32_16x16x32_bf16 v[78:81], v[146:149], v[210:213], v[78:81]
	v_mfma_f32_16x16x32_bf16 v[74:77], v[162:165], v[210:213], v[74:77]
	v_mfma_f32_16x16x32_bf16 v[126:129], v[158:161], v[190:193], v[126:129]
	v_mfma_f32_16x16x32_bf16 v[122:125], v[166:169], v[190:193], v[122:125]
	v_mfma_f32_16x16x32_bf16 v[110:113], v[158:161], v[198:201], v[110:113]
	v_mfma_f32_16x16x32_bf16 v[106:109], v[166:169], v[198:201], v[106:109]
	v_mfma_f32_16x16x32_bf16 v[94:97], v[158:161], v[206:209], v[94:97]
	v_mfma_f32_16x16x32_bf16 v[90:93], v[166:169], v[206:209], v[90:93]
	v_mfma_f32_16x16x32_bf16 v[78:81], v[158:161], v[214:217], v[78:81]
	v_mfma_f32_16x16x32_bf16 v[74:77], v[166:169], v[214:217], v[74:77]
	v_mfma_f32_16x16x32_bf16 v[118:121], v[170:173], v[186:189], v[118:121]
	v_mfma_f32_16x16x32_bf16 v[114:117], v[178:181], v[186:189], v[114:117]
	v_mfma_f32_16x16x32_bf16 v[102:105], v[170:173], v[194:197], v[102:105]
	v_mfma_f32_16x16x32_bf16 v[98:101], v[178:181], v[194:197], v[98:101]
	v_mfma_f32_16x16x32_bf16 v[86:89], v[170:173], v[202:205], v[86:89]
	v_mfma_f32_16x16x32_bf16 v[82:85], v[178:181], v[202:205], v[82:85]
	v_mfma_f32_16x16x32_bf16 v[70:73], v[170:173], v[210:213], v[70:73]
	v_mfma_f32_16x16x32_bf16 v[66:69], v[178:181], v[210:213], v[66:69]
	v_mfma_f32_16x16x32_bf16 v[118:121], v[174:177], v[190:193], v[118:121]
	v_mfma_f32_16x16x32_bf16 v[114:117], v[182:185], v[190:193], v[114:117]
	v_mfma_f32_16x16x32_bf16 v[102:105], v[174:177], v[198:201], v[102:105]
	v_mfma_f32_16x16x32_bf16 v[98:101], v[182:185], v[198:201], v[98:101]
	v_mfma_f32_16x16x32_bf16 v[86:89], v[174:177], v[206:209], v[86:89]
	v_mfma_f32_16x16x32_bf16 v[82:85], v[182:185], v[206:209], v[82:85]
	v_mfma_f32_16x16x32_bf16 v[70:73], v[174:177], v[214:217], v[70:73]
	v_mfma_f32_16x16x32_bf16 v[66:69], v[182:185], v[214:217], v[66:69]
	s_setprio 0
	s_barrier
	s_add_i32 s62, s54, s46
	v_lshl_add_u64 v[150:151], s[40:41], 0, v[132:133]
	s_mov_b32 m0, s62
	ds_read_b128 v[186:189], v156 offset:16384
	ds_read_b128 v[190:193], v156 offset:17408
	ds_read_b128 v[194:197], v156 offset:18432
	ds_read_b128 v[198:201], v156 offset:19456
	ds_read_b128 v[202:205], v156 offset:20480
	ds_read_b128 v[206:209], v156 offset:21504
	ds_read_b128 v[210:213], v156 offset:22528
	ds_read_b128 v[214:217], v156 offset:23552
	global_load_lds_dwordx4 v[150:151], off
	s_add_i32 m0, s62, 0x2000
	s_add_u32 s68, s40, 0x80000
	v_lshl_add_u64 v[218:219], s[40:41], 0, v[136:137]
	s_addc_u32 s69, s41, 0
	s_add_i32 s62, s55, s46
	global_load_lds_dwordx4 v[218:219], off
	v_lshl_add_u64 v[220:221], s[68:69], 0, v[132:133]
	s_mov_b32 m0, s62
	v_lshl_add_u64 v[222:223], s[42:43], 0, v[134:135]
	global_load_lds_dwordx4 v[220:221], off
	v_lshl_add_u64 v[220:221], s[68:69], 0, v[136:137]
	s_add_i32 m0, s62, 0x2000
	s_nop 0
	global_load_lds_dwordx4 v[220:221], off
	v_lshl_add_u64 v[220:221], s[42:43], 0, v[130:131]
	s_mov_b32 m0, s35
	s_nop 0
	global_load_lds_dwordx4 v[220:221], off
	s_mov_b32 m0, s47
	s_nop 0
	global_load_lds_dwordx4 v[222:223], off
	s_waitcnt vmcnt(8)
	s_waitcnt lgkmcnt(0)
	s_barrier
	s_setprio 1
	s_waitcnt lgkmcnt(0)
	v_mfma_f32_16x16x32_bf16 v[62:65], v[146:149], v[186:189], v[62:65]
	v_mfma_f32_16x16x32_bf16 v[58:61], v[162:165], v[186:189], v[58:61]
	v_mfma_f32_16x16x32_bf16 v[46:49], v[146:149], v[194:197], v[46:49]
	v_mfma_f32_16x16x32_bf16 v[42:45], v[162:165], v[194:197], v[42:45]
	v_mfma_f32_16x16x32_bf16 v[22:25], v[146:149], v[202:205], v[22:25]
	v_mfma_f32_16x16x32_bf16 v[18:21], v[162:165], v[202:205], v[18:21]
	v_mfma_f32_16x16x32_bf16 v[6:9], v[146:149], v[210:213], v[6:9]
	v_mfma_f32_16x16x32_bf16 v[2:5], v[162:165], v[210:213], v[2:5]
	v_mfma_f32_16x16x32_bf16 v[62:65], v[158:161], v[190:193], v[62:65]
	v_mfma_f32_16x16x32_bf16 v[58:61], v[166:169], v[190:193], v[58:61]
	v_mfma_f32_16x16x32_bf16 v[46:49], v[158:161], v[198:201], v[46:49]
	v_mfma_f32_16x16x32_bf16 v[42:45], v[166:169], v[198:201], v[42:45]
	v_mfma_f32_16x16x32_bf16 v[22:25], v[158:161], v[206:209], v[22:25]
	v_mfma_f32_16x16x32_bf16 v[18:21], v[166:169], v[206:209], v[18:21]
	v_mfma_f32_16x16x32_bf16 v[6:9], v[158:161], v[214:217], v[6:9]
	v_mfma_f32_16x16x32_bf16 v[2:5], v[166:169], v[214:217], v[2:5]
	v_mfma_f32_16x16x32_bf16 v[54:57], v[170:173], v[186:189], v[54:57]
	v_mfma_f32_16x16x32_bf16 v[50:53], v[178:181], v[186:189], v[50:53]
	v_mfma_f32_16x16x32_bf16 v[30:33], v[170:173], v[194:197], v[30:33]
	v_mfma_f32_16x16x32_bf16 v[26:29], v[178:181], v[194:197], v[26:29]
	v_mfma_f32_16x16x32_bf16 v[34:37], v[170:173], v[202:205], v[34:37]
	v_mfma_f32_16x16x32_bf16 v[38:41], v[178:181], v[202:205], v[38:41]
	v_mfma_f32_16x16x32_bf16 v[10:13], v[170:173], v[210:213], v[10:13]
	v_mfma_f32_16x16x32_bf16 v[14:17], v[178:181], v[210:213], v[14:17]
	v_mfma_f32_16x16x32_bf16 v[54:57], v[174:177], v[190:193], v[54:57]
	v_mfma_f32_16x16x32_bf16 v[50:53], v[182:185], v[190:193], v[50:53]
	v_mfma_f32_16x16x32_bf16 v[30:33], v[174:177], v[198:201], v[30:33]
	v_mfma_f32_16x16x32_bf16 v[26:29], v[182:185], v[198:201], v[26:29]
	v_mfma_f32_16x16x32_bf16 v[34:37], v[174:177], v[206:209], v[34:37]
	v_mfma_f32_16x16x32_bf16 v[38:41], v[182:185], v[206:209], v[38:41]
	v_mfma_f32_16x16x32_bf16 v[10:13], v[174:177], v[214:217], v[10:13]
	v_mfma_f32_16x16x32_bf16 v[14:17], v[182:185], v[214:217], v[14:17]
	s_setprio 0
	s_barrier
; #define PG8_STAGE2(bufoff, gbase, v0, v1) do { \
;         __builtin_amdgcn_global_load_lds((const unsigned*)((const char*)(gbase) + (v0)), (LAS unsigned*)(lds + (bufoff) + ldsw), 16, 0, 0); \
;         __builtin_amdgcn_global_load_lds((const unsigned*)((const char*)(gbase) + (v1)), (LAS unsigned*)(lds + (bufoff) + ldsw + 8192), 16, 0, 0); } while (0)
; #define PG8_STAGE(bufoff, gbase, voff) PG8_STAGE2(bufoff, gbase, (voff)[0], (voff)[1])
; #define PG8_LDA(dst, b, h) do { _Pragma("unroll") for (int m = 0; m < 4; ++m) _Pragma("unroll") for (int k = 0; k < 2; ++k) dst[m][k] = *(const LAS bf16x8*)(lds + PG8_SA(b, h) + aoff + m * 2048 + k * 1024); } while (0)
; #define PG8_LDB(dst, b, h) do { _Pragma("unroll") for (int n = 0; n < 2; ++n) _Pragma("unroll") for (int k = 0; k < 2; ++k) dst[n][k] = *(const LAS bf16x8*)(lds + PG8_SB(b, h) + boff + n * 2048 + k * 1024); } while (0)
; #define PG8_WAIT_V(n) asm volatile("s_waitcnt vmcnt(" #n ")" ::: "memory")
; #define PG8_WAIT_L(n) asm volatile("s_waitcnt lgkmcnt(" #n ")" ::: "memory")
; #define PG8_BAR __builtin_amdgcn_s_barrier()
; #define PG8_SCHED __builtin_amdgcn_sched_barrier(0)
; template <class Epi, class Sched, bool ALIGN_EPI, bool SP2, bool GATHER>
; DI void gemm_phase(LAS unsigned char* lds, const Gemm g, const Sched& S, const Epi& E) {
;     ...
;             PG8_LDB(B0, 0, 0); PG8_LDB(B1, 0, 1); PG8_SCHED; PG8_LDA(At, 0, 0); PG8_STAGE2(PG8_SA(1, 1), a1 + hstepA, gC[1][0], gC[1][1]);
;             PG8_WAIT_V(8); PG8_WAIT_L(0); PG8_BAR; PG8_MMA(0, 0, At, B0); PG8_MMA(0, 1, At, B1); PG8_BAR; PG8_SCHED;
;             PG8_LDA(At, 0, 1); PG8_STAGE(PG8_SB(0, 0), b2, voffB); PG8_STAGE(PG8_SB(0, 1), b2 + hstep, voffB); PG8_STAGE2(PG8_SA(0, 0), a2, x00, x01);
;             PG8_WAIT_V(8); PG8_WAIT_L(0); PG8_BAR; PG8_MMA(1, 0, At, B0); PG8_MMA(1, 1, At, B1); PG8_BAR; PG8_SCHED;
;             PG8_LDB(B0, 1, 0); PG8_LDB(B1, 1, 1); PG8_SCHED; PG8_LDA(At, 1, 0); PG8_STAGE2(PG8_SA(0, 1), a2 + hstepA, x10, x11);
;             PG8_WAIT_V(8); PG8_WAIT_L(0); PG8_BAR; PG8_MMA(0, 0, At, B0); PG8_MMA(0, 1, At, B1); PG8_BAR; PG8_SCHED;
;             PG8_LDA(At, 1, 1); PG8_STAGE(PG8_SB(1, 0), b3, voffB); PG8_STAGE(PG8_SB(1, 1), b3 + hstep, voffB); PG8_STAGE2(PG8_SA(1, 0), a3, x00, x01);
;             PG8_WAIT_V(8); PG8_WAIT_L(0); PG8_BAR; PG8_MMA(1, 0, At, B0); PG8_MMA(1, 1, At, B1); PG8_BAR; PG8_SCHED;
	s_add_i32 s62, 0, 0x18000
	v_add_u32_e32 v157, s62, v152
	s_add_i32 s67, 0, 0x1c000
	ds_read_b128 v[146:149], v157
	ds_read_b128 v[158:161], v157 offset:1024
	ds_read_b128 v[162:165], v157 offset:2048
	ds_read_b128 v[166:169], v157 offset:3072
	v_add_u32_e32 v157, s67, v152
	ds_read_b128 v[170:173], v157
	ds_read_b128 v[174:177], v157 offset:1024
	ds_read_b128 v[178:181], v157 offset:2048
	ds_read_b128 v[182:185], v157 offset:3072
	s_add_u32 s42, s42, 0x80000
	s_addc_u32 s43, s43, 0
	s_mov_b32 m0, s48
	v_lshl_add_u64 v[224:225], s[42:43], 0, v[130:131]
	ds_read_b128 v[186:189], v156 offset:32768
	ds_read_b128 v[190:193], v156 offset:33792
	ds_read_b128 v[194:197], v156 offset:34816
	ds_read_b128 v[198:201], v156 offset:35840
	ds_read_b128 v[202:205], v156 offset:36864
	ds_read_b128 v[206:209], v156 offset:37888
	ds_read_b128 v[210:213], v156 offset:38912
	ds_read_b128 v[214:217], v156 offset:39936
	global_load_lds_dwordx4 v[224:225], off
	v_lshl_add_u64 v[224:225], s[42:43], 0, v[134:135]
	s_mov_b32 m0, s49
	s_nop 0
	global_load_lds_dwordx4 v[224:225], off
	s_waitcnt vmcnt(8)
	s_waitcnt lgkmcnt(0)
	s_barrier
	s_setprio 1
	s_waitcnt lgkmcnt(0)
	v_mfma_f32_16x16x32_bf16 v[126:129], v[146:149], v[186:189], v[126:129]
	v_mfma_f32_16x16x32_bf16 v[122:125], v[162:165], v[186:189], v[122:125]
	v_mfma_f32_16x16x32_bf16 v[110:113], v[146:149], v[194:197], v[110:113]
	v_mfma_f32_16x16x32_bf16 v[106:109], v[162:165], v[194:197], v[106:109]
	v_mfma_f32_16x16x32_bf16 v[94:97], v[146:149], v[202:205], v[94:97]
	v_mfma_f32_16x16x32_bf16 v[90:93], v[162:165], v[202:205], v[90:93]
	v_mfma_f32_16x16x32_bf16 v[78:81], v[146:149], v[210:213], v[78:81]
	v_mfma_f32_16x16x32_bf16 v[74:77], v[162:165], v[210:213], v[74:77]
	v_mfma_f32_16x16x32_bf16 v[126:129], v[158:161], v[190:193], v[126:129]
	v_mfma_f32_16x16x32_bf16 v[122:125], v[166:169], v[190:193], v[122:125]
	v_mfma_f32_16x16x32_bf16 v[110:113], v[158:161], v[198:201], v[110:113]
	v_mfma_f32_16x16x32_bf16 v[106:109], v[166:169], v[198:201], v[106:109]
	v_mfma_f32_16x16x32_bf16 v[94:97], v[158:161], v[206:209], v[94:97]
	v_mfma_f32_16x16x32_bf16 v[90:93], v[166:169], v[206:209], v[90:93]
	v_mfma_f32_16x16x32_bf16 v[78:81], v[158:161], v[214:217], v[78:81]
	v_mfma_f32_16x16x32_bf16 v[74:77], v[166:169], v[214:217], v[74:77]
	v_mfma_f32_16x16x32_bf16 v[118:121], v[170:173], v[186:189], v[118:121]
	v_mfma_f32_16x16x32_bf16 v[114:117], v[178:181], v[186:189], v[114:117]
	v_mfma_f32_16x16x32_bf16 v[102:105], v[170:173], v[194:197], v[102:105]
	v_mfma_f32_16x16x32_bf16 v[98:101], v[178:181], v[194:197], v[98:101]
	v_mfma_f32_16x16x32_bf16 v[86:89], v[170:173], v[202:205], v[86:89]
	v_mfma_f32_16x16x32_bf16 v[82:85], v[178:181], v[202:205], v[82:85]
	v_mfma_f32_16x16x32_bf16 v[70:73], v[170:173], v[210:213], v[70:73]
	v_mfma_f32_16x16x32_bf16 v[66:69], v[178:181], v[210:213], v[66:69]
	v_mfma_f32_16x16x32_bf16 v[118:121], v[174:177], v[190:193], v[118:121]
	v_mfma_f32_16x16x32_bf16 v[114:117], v[182:185], v[190:193], v[114:117]
	v_mfma_f32_16x16x32_bf16 v[102:105], v[174:177], v[198:201], v[102:105]
	v_mfma_f32_16x16x32_bf16 v[98:101], v[182:185], v[198:201], v[98:101]
	v_mfma_f32_16x16x32_bf16 v[86:89], v[174:177], v[206:209], v[86:89]
	v_mfma_f32_16x16x32_bf16 v[82:85], v[182:185], v[206:209], v[82:85]
	v_mfma_f32_16x16x32_bf16 v[70:73], v[174:177], v[214:217], v[70:73]
	v_mfma_f32_16x16x32_bf16 v[66:69], v[182:185], v[214:217], v[66:69]
	s_setprio 0
	s_barrier
; #define PG8_STAGE2(bufoff, gbase, v0, v1) do { \
;         __builtin_amdgcn_global_load_lds((const unsigned*)((const char*)(gbase) + (v0)), (LAS unsigned*)(lds + (bufoff) + ldsw), 16, 0, 0); \
;         __builtin_amdgcn_global_load_lds((const unsigned*)((const char*)(gbase) + (v1)), (LAS unsigned*)(lds + (bufoff) + ldsw + 8192), 16, 0, 0); } while (0)
; #define PG8_STAGE(bufoff, gbase, voff) PG8_STAGE2(bufoff, gbase, (voff)[0], (voff)[1])
; #define PG8_BAR __builtin_amdgcn_s_barrier()
; template <class Epi, class Sched, bool ALIGN_EPI, bool SP2, bool GATHER>
; DI void gemm_phase(LAS unsigned char* lds, const Gemm g, const Sched& S, const Epi& E) {
;     ...
;         for (int t = 0; t < nt; t += 2) {
;             if constexpr (Epi::MID_T >= 0) { if (t == Epi::MID_T) { E.mid(acc, cur, wr, wc, fr, fq); PG8_SCHED; } }
;             const bool last = (t == nt - 2);
;             const char* a1 = cA + (size_t)(t + 1) * kstep;
;             const char* a2 = last ? nA : cA + (size_t)(t + 2) * kstep; const char* b2 = last ? nB : cB + (size_t)(t + 2) * kstep;
;             const char* a3 = a2 + kstep; const char* b3 = b2 + kstep;
;             unsigned x00 = gC[0][0], x01 = gC[0][1], x10 = gC[1][0], x11 = gC[1][1];
;             if constexpr (GATHER) { if (last) { x00 = gN[0][0]; x01 = gN[0][1]; x10 = gN[1][0]; x11 = gN[1][1]; } }
;             PG8_LDB(B0, 0, 0); PG8_LDB(B1, 0, 1); PG8_SCHED; PG8_LDA(At, 0, 0); PG8_STAGE2(PG8_SA(1, 1), a1 + hstepA, gC[1][0], gC[1][1]);
;             PG8_WAIT_V(8); PG8_WAIT_L(0); PG8_BAR; PG8_MMA(0, 0, At, B0); PG8_MMA(0, 1, At, B1); PG8_BAR; PG8_SCHED;
;             PG8_LDA(At, 0, 1); PG8_STAGE(PG8_SB(0, 0), b2, voffB); PG8_STAGE(PG8_SB(0, 1), b2 + hstep, voffB); PG8_STAGE2(PG8_SA(0, 0), a2, x00, x01);
;             PG8_WAIT_V(8); PG8_WAIT_L(0); PG8_BAR; PG8_MMA(1, 0, At, B0); PG8_MMA(1, 1, At, B1); PG8_BAR; PG8_SCHED;
;             PG8_LDB(B0, 1, 0); PG8_LDB(B1, 1, 1); PG8_SCHED; PG8_LDA(At, 1, 0); PG8_STAGE2(PG8_SA(0, 1), a2 + hstepA, x10, x11);
;             PG8_WAIT_V(8); PG8_WAIT_L(0); PG8_BAR; PG8_MMA(0, 0, At, B0); PG8_MMA(0, 1, At, B1); PG8_BAR; PG8_SCHED;
;             PG8_LDA(At, 1, 1); PG8_STAGE(PG8_SB(1, 0), b3, voffB); PG8_STAGE(PG8_SB(1, 1), b3 + hstep, voffB); PG8_STAGE2(PG8_SA(1, 0), a3, x00, x01);
;             PG8_WAIT_V(8); PG8_WAIT_L(0); PG8_BAR; PG8_MMA(1, 0, At, B0); PG8_MMA(1, 1, At, B1); PG8_BAR; PG8_SCHED;
	s_add_i32 s42, s62, s46
	v_lshl_add_u64 v[150:151], v[150:151], 0, s[12:13]
	s_mov_b32 m0, s42
	ds_read_b128 v[186:189], v156 offset:49152
	ds_read_b128 v[190:193], v156 offset:50176
	ds_read_b128 v[194:197], v156 offset:51200
	ds_read_b128 v[198:201], v156 offset:52224
	ds_read_b128 v[202:205], v156 offset:53248
	ds_read_b128 v[206:209], v156 offset:54272
	ds_read_b128 v[210:213], v156 offset:55296
	ds_read_b128 v[214:217], v156 offset:56320
	global_load_lds_dwordx4 v[150:151], off
	s_add_i32 m0, s42, 0x2000
	s_add_u32 s40, s40, 0x80080
	v_lshl_add_u64 v[150:151], v[218:219], 0, s[12:13]
	s_addc_u32 s41, s41, 0
	s_add_i32 s42, s67, s46
	global_load_lds_dwordx4 v[150:151], off
	v_lshl_add_u64 v[150:151], s[40:41], 0, v[132:133]
	s_mov_b32 m0, s42
	s_nop 0
	global_load_lds_dwordx4 v[150:151], off
	v_lshl_add_u64 v[150:151], s[40:41], 0, v[136:137]
	s_add_i32 m0, s42, 0x2000
	s_nop 0
	global_load_lds_dwordx4 v[150:151], off
	v_lshl_add_u64 v[150:151], v[220:221], 0, s[12:13]
	s_mov_b32 m0, s51
	s_nop 0
	global_load_lds_dwordx4 v[150:151], off
	v_lshl_add_u64 v[150:151], v[222:223], 0, s[12:13]
	s_mov_b32 m0, s52
	s_nop 0
	global_load_lds_dwordx4 v[150:151], off
	s_waitcnt vmcnt(8)
	s_waitcnt lgkmcnt(0)
	s_barrier
	s_setprio 1
	s_waitcnt lgkmcnt(0)
	v_mfma_f32_16x16x32_bf16 v[62:65], v[146:149], v[186:189], v[62:65]
	v_mfma_f32_16x16x32_bf16 v[58:61], v[162:165], v[186:189], v[58:61]
	v_mfma_f32_16x16x32_bf16 v[46:49], v[146:149], v[194:197], v[46:49]
	v_mfma_f32_16x16x32_bf16 v[42:45], v[162:165], v[194:197], v[42:45]
	v_mfma_f32_16x16x32_bf16 v[22:25], v[146:149], v[202:205], v[22:25]
	v_mfma_f32_16x16x32_bf16 v[18:21], v[162:165], v[202:205], v[18:21]
	v_mfma_f32_16x16x32_bf16 v[6:9], v[146:149], v[210:213], v[6:9]
	v_mfma_f32_16x16x32_bf16 v[2:5], v[162:165], v[210:213], v[2:5]
	v_mfma_f32_16x16x32_bf16 v[62:65], v[158:161], v[190:193], v[62:65]
	v_mfma_f32_16x16x32_bf16 v[58:61], v[166:169], v[190:193], v[58:61]
	v_mfma_f32_16x16x32_bf16 v[46:49], v[158:161], v[198:201], v[46:49]
	v_mfma_f32_16x16x32_bf16 v[42:45], v[166:169], v[198:201], v[42:45]
	v_mfma_f32_16x16x32_bf16 v[22:25], v[158:161], v[206:209], v[22:25]
	v_mfma_f32_16x16x32_bf16 v[18:21], v[166:169], v[206:209], v[18:21]
	v_mfma_f32_16x16x32_bf16 v[6:9], v[158:161], v[214:217], v[6:9]
	v_mfma_f32_16x16x32_bf16 v[2:5], v[166:169], v[214:217], v[2:5]
	v_mfma_f32_16x16x32_bf16 v[54:57], v[170:173], v[186:189], v[54:57]
	v_mfma_f32_16x16x32_bf16 v[50:53], v[178:181], v[186:189], v[50:53]
	v_mfma_f32_16x16x32_bf16 v[30:33], v[170:173], v[194:197], v[30:33]
	v_mfma_f32_16x16x32_bf16 v[26:29], v[178:181], v[194:197], v[26:29]
	v_mfma_f32_16x16x32_bf16 v[34:37], v[170:173], v[202:205], v[34:37]
	v_mfma_f32_16x16x32_bf16 v[38:41], v[178:181], v[202:205], v[38:41]
	v_mfma_f32_16x16x32_bf16 v[10:13], v[170:173], v[210:213], v[10:13]
	v_mfma_f32_16x16x32_bf16 v[14:17], v[178:181], v[210:213], v[14:17]
	v_mfma_f32_16x16x32_bf16 v[54:57], v[174:177], v[190:193], v[54:57]
	v_mfma_f32_16x16x32_bf16 v[50:53], v[182:185], v[190:193], v[50:53]
	v_mfma_f32_16x16x32_bf16 v[30:33], v[174:177], v[198:201], v[30:33]
	v_mfma_f32_16x16x32_bf16 v[26:29], v[182:185], v[198:201], v[26:29]
	v_mfma_f32_16x16x32_bf16 v[34:37], v[174:177], v[206:209], v[34:37]
	v_mfma_f32_16x16x32_bf16 v[38:41], v[182:185], v[206:209], v[38:41]
	v_mfma_f32_16x16x32_bf16 v[10:13], v[174:177], v[214:217], v[10:13]
	v_mfma_f32_16x16x32_bf16 v[14:17], v[182:185], v[214:217], v[14:17]
	s_setprio 0
	s_barrier
	s_add_i32 s66, s66, 2
	s_add_u32 s36, s36, 0x100
	s_addc_u32 s37, s37, 0
	s_add_u32 s64, s64, 0x100
	s_addc_u32 s65, s65, 0
	s_cmp_gt_u32 s66, 29
	s_cbranch_scc0 .LBB0_674

; #define PG8_STAGE2(bufoff, gbase, v0, v1) do { \
;         __builtin_amdgcn_global_load_lds((const unsigned*)((const char*)(gbase) + (v0)), (LAS unsigned*)(lds + (bufoff) + ldsw), 16, 0, 0); \
;         __builtin_amdgcn_global_load_lds((const unsigned*)((const char*)(gbase) + (v1)), (LAS unsigned*)(lds + (bufoff) + ldsw + 8192), 16, 0, 0); } while (0)
; #define PG8_STAGE(bufoff, gbase, voff) PG8_STAGE2(bufoff, gbase, (voff)[0], (voff)[1])
; #define PG8_BAR __builtin_amdgcn_s_barrier()
; template <class Epi, class Sched, bool ALIGN_EPI, bool SP2, bool GATHER>
; DI void gemm_phase(LAS unsigned char* lds, const Gemm g, const Sched& S, const Epi& E) {
;     ...
;         for (int t = 0; t < nt; t += 2) {
;             if constexpr (Epi::MID_T >= 0) { if (t == Epi::MID_T) { E.mid(acc, cur, wr, wc, fr, fq); PG8_SCHED; } }
;             const bool last = (t == nt - 2);
;             const char* a1 = cA + (size_t)(t + 1) * kstep;
;             const char* a2 = last ? nA : cA + (size_t)(t + 2) * kstep; const char* b2 = last ? nB : cB + (size_t)(t + 2) * kstep;
;             const char* a3 = a2 + kstep; const char* b3 = b2 + kstep;
;             unsigned x00 = gC[0][0], x01 = gC[0][1], x10 = gC[1][0], x11 = gC[1][1];
;             if constexpr (GATHER) { if (last) { x00 = gN[0][0]; x01 = gN[0][1]; x10 = gN[1][0]; x11 = gN[1][1]; } }
;             PG8_LDB(B0, 0, 0); PG8_LDB(B1, 0, 1); PG8_SCHED; PG8_LDA(At, 0, 0); PG8_STAGE2(PG8_SA(1, 1), a1 + hstepA, gC[1][0], gC[1][1]);
;             PG8_WAIT_V(8); PG8_WAIT_L(0); PG8_BAR; PG8_MMA(0, 0, At, B0); PG8_MMA(0, 1, At, B1); PG8_BAR; PG8_SCHED;
;             PG8_LDA(At, 0, 1); PG8_STAGE(PG8_SB(0, 0), b2, voffB); PG8_STAGE(PG8_SB(0, 1), b2 + hstep, voffB); PG8_STAGE2(PG8_SA(0, 0), a2, x00, x01);
;             PG8_WAIT_V(8); PG8_WAIT_L(0); PG8_BAR; PG8_MMA(1, 0, At, B0); PG8_MMA(1, 1, At, B1); PG8_BAR; PG8_SCHED;
;             PG8_LDB(B0, 1, 0); PG8_LDB(B1, 1, 1); PG8_SCHED; PG8_LDA(At, 1, 0); PG8_STAGE2(PG8_SA(0, 1), a2 + hstepA, x10, x11);
;             PG8_WAIT_V(8); PG8_WAIT_L(0); PG8_BAR; PG8_MMA(0, 0, At, B0); PG8_MMA(0, 1, At, B1); PG8_BAR; PG8_SCHED;
;             PG8_LDA(At, 1, 1); PG8_STAGE(PG8_SB(1, 0), b3, voffB); PG8_STAGE(PG8_SB(1, 1), b3 + hstep, voffB); PG8_STAGE2(PG8_SA(1, 0), a3, x00, x01);
;             PG8_WAIT_V(8); PG8_WAIT_L(0); PG8_BAR; PG8_MMA(1, 0, At, B0); PG8_MMA(1, 1, At, B1); PG8_BAR; PG8_SCHED;
.LBB0_905:
	v_add_u32_e32 v151, s53, v155
	ds_read_b128 v[160:163], v151
	ds_read_b128 v[164:167], v151 offset:1024
	ds_read_b128 v[168:171], v151 offset:2048
	ds_read_b128 v[172:175], v151 offset:3072
	v_add_u32_e32 v151, s54, v155
	ds_read_b128 v[176:179], v151
	ds_read_b128 v[180:183], v151 offset:1024
	ds_read_b128 v[184:187], v151 offset:2048
	ds_read_b128 v[188:191], v151 offset:3072
	s_add_u32 s42, s36, 0x80
	s_addc_u32 s43, s37, 0
	s_and_b64 s[40:41], s[40:41], exec
	s_cselect_b32 s43, s5, s43
	s_cselect_b32 s42, s4, s42
	s_cselect_b32 s41, s29, s66
	s_cselect_b32 s40, s64, s65
	v_lshl_add_u64 v[224:225], s[36:37], 0, v[140:141]
	s_add_i32 m0, s35, 0xc000
	ds_read_b128 v[192:195], v157
	ds_read_b128 v[196:199], v157 offset:1024
	ds_read_b128 v[200:203], v157 offset:2048
	ds_read_b128 v[204:207], v157 offset:3072
	ds_read_b128 v[208:211], v157 offset:4096
	ds_read_b128 v[212:215], v157 offset:5120
	ds_read_b128 v[216:219], v157 offset:6144
	ds_read_b128 v[220:223], v157 offset:7168
	global_load_lds_dwordx4 v[224:225], off
	v_lshl_add_u64 v[224:225], s[36:37], 0, v[144:145]
	s_add_i32 m0, s35, 0xe000
	s_nop 0
	global_load_lds_dwordx4 v[224:225], off
	s_waitcnt vmcnt(8)
	s_waitcnt lgkmcnt(0)
	s_barrier
	s_setprio 1
	s_waitcnt lgkmcnt(0)
	v_mfma_f32_16x16x32_bf16 v[122:125], v[160:163], v[192:195], v[122:125]
	v_mfma_f32_16x16x32_bf16 v[126:129], v[168:171], v[192:195], v[126:129]
	v_mfma_f32_16x16x32_bf16 v[106:109], v[160:163], v[200:203], v[106:109]
	v_mfma_f32_16x16x32_bf16 v[110:113], v[168:171], v[200:203], v[110:113]
	v_mfma_f32_16x16x32_bf16 v[90:93], v[160:163], v[208:211], v[90:93]
	v_mfma_f32_16x16x32_bf16 v[94:97], v[168:171], v[208:211], v[94:97]
	v_mfma_f32_16x16x32_bf16 v[74:77], v[160:163], v[216:219], v[74:77]
	v_mfma_f32_16x16x32_bf16 v[78:81], v[168:171], v[216:219], v[78:81]
	v_mfma_f32_16x16x32_bf16 v[122:125], v[164:167], v[196:199], v[122:125]
	v_mfma_f32_16x16x32_bf16 v[126:129], v[172:175], v[196:199], v[126:129]
	v_mfma_f32_16x16x32_bf16 v[106:109], v[164:167], v[204:207], v[106:109]
	v_mfma_f32_16x16x32_bf16 v[110:113], v[172:175], v[204:207], v[110:113]
	v_mfma_f32_16x16x32_bf16 v[90:93], v[164:167], v[212:215], v[90:93]
	v_mfma_f32_16x16x32_bf16 v[94:97], v[172:175], v[212:215], v[94:97]
	v_mfma_f32_16x16x32_bf16 v[74:77], v[164:167], v[220:223], v[74:77]
	v_mfma_f32_16x16x32_bf16 v[78:81], v[172:175], v[220:223], v[78:81]
	v_mfma_f32_16x16x32_bf16 v[114:117], v[176:179], v[192:195], v[114:117]
	v_mfma_f32_16x16x32_bf16 v[118:121], v[184:187], v[192:195], v[118:121]
	v_mfma_f32_16x16x32_bf16 v[98:101], v[176:179], v[200:203], v[98:101]
	v_mfma_f32_16x16x32_bf16 v[102:105], v[184:187], v[200:203], v[102:105]
	v_mfma_f32_16x16x32_bf16 v[82:85], v[176:179], v[208:211], v[82:85]
	v_mfma_f32_16x16x32_bf16 v[86:89], v[184:187], v[208:211], v[86:89]
	v_mfma_f32_16x16x32_bf16 v[66:69], v[176:179], v[216:219], v[66:69]
	v_mfma_f32_16x16x32_bf16 v[70:73], v[184:187], v[216:219], v[70:73]
	v_mfma_f32_16x16x32_bf16 v[114:117], v[180:183], v[196:199], v[114:117]
	v_mfma_f32_16x16x32_bf16 v[118:121], v[188:191], v[196:199], v[118:121]
	v_mfma_f32_16x16x32_bf16 v[98:101], v[180:183], v[204:207], v[98:101]
	v_mfma_f32_16x16x32_bf16 v[102:105], v[188:191], v[204:207], v[102:105]
	v_mfma_f32_16x16x32_bf16 v[82:85], v[180:183], v[212:215], v[82:85]
	v_mfma_f32_16x16x32_bf16 v[86:89], v[188:191], v[212:215], v[86:89]
	v_mfma_f32_16x16x32_bf16 v[66:69], v[180:183], v[220:223], v[66:69]
	v_mfma_f32_16x16x32_bf16 v[70:73], v[188:191], v[220:223], v[70:73]
	s_setprio 0
	s_barrier
	s_add_i32 s68, s53, s45
	v_lshl_add_u64 v[224:225], s[40:41], 0, v[132:133]
	s_mov_b32 m0, s68
	ds_read_b128 v[192:195], v157 offset:16384
	ds_read_b128 v[196:199], v157 offset:17408
	ds_read_b128 v[200:203], v157 offset:18432
	ds_read_b128 v[204:207], v157 offset:19456
	ds_read_b128 v[208:211], v157 offset:20480
	ds_read_b128 v[212:215], v157 offset:21504
	ds_read_b128 v[216:219], v157 offset:22528
	ds_read_b128 v[220:223], v157 offset:23552
	global_load_lds_dwordx4 v[224:225], off
	s_add_i32 m0, s68, 0x2000
	s_add_u32 s68, s40, 0x80000
	v_lshl_add_u64 v[226:227], s[40:41], 0, v[130:131]
	s_addc_u32 s69, s41, 0
	s_add_i32 s70, s54, s45
	global_load_lds_dwordx4 v[226:227], off
	v_lshl_add_u64 v[228:229], s[68:69], 0, v[132:133]
	s_mov_b32 m0, s70
	v_mov_b32_e32 v151, v135
	global_load_lds_dwordx4 v[228:229], off
	v_lshl_add_u64 v[228:229], s[68:69], 0, v[130:131]
	s_add_i32 m0, s70, 0x2000
	s_nop 0
	global_load_lds_dwordx4 v[228:229], off
	s_mov_b32 m0, s35
	v_lshl_add_u64 v[228:229], s[42:43], 0, v[134:135]
	global_load_lds_dwordx4 v134, s[42:43]
	s_mov_b32 m0, s46
	s_nop 0
	global_load_lds_dwordx4 v150, s[42:43]
	s_waitcnt vmcnt(8)
	s_waitcnt lgkmcnt(0)
	v_lshl_add_u64 v[150:151], s[42:43], 0, v[150:151]
	s_barrier
; #define PG8_STAGE2(bufoff, gbase, v0, v1) do { \
;         __builtin_amdgcn_global_load_lds((const unsigned*)((const char*)(gbase) + (v0)), (LAS unsigned*)(lds + (bufoff) + ldsw), 16, 0, 0); \
;         __builtin_amdgcn_global_load_lds((const unsigned*)((const char*)(gbase) + (v1)), (LAS unsigned*)(lds + (bufoff) + ldsw + 8192), 16, 0, 0); } while (0)
; #define PG8_STAGE(bufoff, gbase, voff) PG8_STAGE2(bufoff, gbase, (voff)[0], (voff)[1])
; #define PG8_LDA(dst, b, h) do { _Pragma("unroll") for (int m = 0; m < 4; ++m) _Pragma("unroll") for (int k = 0; k < 2; ++k) dst[m][k] = *(const LAS bf16x8*)(lds + PG8_SA(b, h) + aoff + m * 2048 + k * 1024); } while (0)
; #define PG8_LDB(dst, b, h) do { _Pragma("unroll") for (int n = 0; n < 2; ++n) _Pragma("unroll") for (int k = 0; k < 2; ++k) dst[n][k] = *(const LAS bf16x8*)(lds + PG8_SB(b, h) + boff + n * 2048 + k * 1024); } while (0)
; #define PG8_WAIT_V(n) asm volatile("s_waitcnt vmcnt(" #n ")" ::: "memory")
; #define PG8_WAIT_L(n) asm volatile("s_waitcnt lgkmcnt(" #n ")" ::: "memory")
; #define PG8_BAR __builtin_amdgcn_s_barrier()
; #define PG8_SCHED __builtin_amdgcn_sched_barrier(0)
; template <class Epi, class Sched, bool ALIGN_EPI, bool SP2, bool GATHER>
; DI void gemm_phase(LAS unsigned char* lds, const Gemm g, const Sched& S, const Epi& E) {
;     ...
;             PG8_LDB(B0, 0, 0); PG8_LDB(B1, 0, 1); PG8_SCHED; PG8_LDA(At, 0, 0); PG8_STAGE2(PG8_SA(1, 1), a1 + hstepA, gC[1][0], gC[1][1]);
;             PG8_WAIT_V(8); PG8_WAIT_L(0); PG8_BAR; PG8_MMA(0, 0, At, B0); PG8_MMA(0, 1, At, B1); PG8_BAR; PG8_SCHED;
;             PG8_LDA(At, 0, 1); PG8_STAGE(PG8_SB(0, 0), b2, voffB); PG8_STAGE(PG8_SB(0, 1), b2 + hstep, voffB); PG8_STAGE2(PG8_SA(0, 0), a2, x00, x01);
;             PG8_WAIT_V(8); PG8_WAIT_L(0); PG8_BAR; PG8_MMA(1, 0, At, B0); PG8_MMA(1, 1, At, B1); PG8_BAR; PG8_SCHED;
;             PG8_LDB(B0, 1, 0); PG8_LDB(B1, 1, 1); PG8_SCHED; PG8_LDA(At, 1, 0); PG8_STAGE2(PG8_SA(0, 1), a2 + hstepA, x10, x11);
;             PG8_WAIT_V(8); PG8_WAIT_L(0); PG8_BAR; PG8_MMA(0, 0, At, B0); PG8_MMA(0, 1, At, B1); PG8_BAR; PG8_SCHED;
;             PG8_LDA(At, 1, 1); PG8_STAGE(PG8_SB(1, 0), b3, voffB); PG8_STAGE(PG8_SB(1, 1), b3 + hstep, voffB); PG8_STAGE2(PG8_SA(1, 0), a3, x00, x01);
;             PG8_WAIT_V(8); PG8_WAIT_L(0); PG8_BAR; PG8_MMA(1, 0, At, B0); PG8_MMA(1, 1, At, B1); PG8_BAR; PG8_SCHED;
	s_setprio 1
	s_waitcnt lgkmcnt(0)
	v_mfma_f32_16x16x32_bf16 v[58:61], v[160:163], v[192:195], v[58:61]
	v_mfma_f32_16x16x32_bf16 v[62:65], v[168:171], v[192:195], v[62:65]
	v_mfma_f32_16x16x32_bf16 v[42:45], v[160:163], v[200:203], v[42:45]
	v_mfma_f32_16x16x32_bf16 v[46:49], v[168:171], v[200:203], v[46:49]
	v_mfma_f32_16x16x32_bf16 v[26:29], v[160:163], v[208:211], v[26:29]
	v_mfma_f32_16x16x32_bf16 v[30:33], v[168:171], v[208:211], v[30:33]
	v_mfma_f32_16x16x32_bf16 v[10:13], v[160:163], v[216:219], v[10:13]
	v_mfma_f32_16x16x32_bf16 v[14:17], v[168:171], v[216:219], v[14:17]
	v_mfma_f32_16x16x32_bf16 v[58:61], v[164:167], v[196:199], v[58:61]
	v_mfma_f32_16x16x32_bf16 v[62:65], v[172:175], v[196:199], v[62:65]
	v_mfma_f32_16x16x32_bf16 v[42:45], v[164:167], v[204:207], v[42:45]
	v_mfma_f32_16x16x32_bf16 v[46:49], v[172:175], v[204:207], v[46:49]
	v_mfma_f32_16x16x32_bf16 v[26:29], v[164:167], v[212:215], v[26:29]
	v_mfma_f32_16x16x32_bf16 v[30:33], v[172:175], v[212:215], v[30:33]
	v_mfma_f32_16x16x32_bf16 v[10:13], v[164:167], v[220:223], v[10:13]
	v_mfma_f32_16x16x32_bf16 v[14:17], v[172:175], v[220:223], v[14:17]
	v_mfma_f32_16x16x32_bf16 v[50:53], v[176:179], v[192:195], v[50:53]
	v_mfma_f32_16x16x32_bf16 v[54:57], v[184:187], v[192:195], v[54:57]
	v_mfma_f32_16x16x32_bf16 v[34:37], v[176:179], v[200:203], v[34:37]
	v_mfma_f32_16x16x32_bf16 v[38:41], v[184:187], v[200:203], v[38:41]
	v_mfma_f32_16x16x32_bf16 v[18:21], v[176:179], v[208:211], v[18:21]
	v_mfma_f32_16x16x32_bf16 v[22:25], v[184:187], v[208:211], v[22:25]
	v_mfma_f32_16x16x32_bf16 v[2:5], v[176:179], v[216:219], v[2:5]
	v_mfma_f32_16x16x32_bf16 v[6:9], v[184:187], v[216:219], v[6:9]
	v_mfma_f32_16x16x32_bf16 v[50:53], v[180:183], v[196:199], v[50:53]
	v_mfma_f32_16x16x32_bf16 v[54:57], v[188:191], v[196:199], v[54:57]
	v_mfma_f32_16x16x32_bf16 v[34:37], v[180:183], v[204:207], v[34:37]
	v_mfma_f32_16x16x32_bf16 v[38:41], v[188:191], v[204:207], v[38:41]
	v_mfma_f32_16x16x32_bf16 v[18:21], v[180:183], v[212:215], v[18:21]
	v_mfma_f32_16x16x32_bf16 v[22:25], v[188:191], v[212:215], v[22:25]
	v_mfma_f32_16x16x32_bf16 v[2:5], v[180:183], v[220:223], v[2:5]
	v_mfma_f32_16x16x32_bf16 v[6:9], v[188:191], v[220:223], v[6:9]
	s_setprio 0
	s_barrier
	s_add_i32 s68, 0, 0x18000
	v_add_u32_e32 v134, s68, v155
	s_add_i32 s69, 0, 0x1c000
	ds_read_b128 v[160:163], v134
	ds_read_b128 v[164:167], v134 offset:1024
	ds_read_b128 v[168:171], v134 offset:2048
	ds_read_b128 v[172:175], v134 offset:3072
	v_add_u32_e32 v134, s69, v155
	ds_read_b128 v[176:179], v134
	ds_read_b128 v[180:183], v134 offset:1024
	ds_read_b128 v[184:187], v134 offset:2048
	ds_read_b128 v[188:191], v134 offset:3072
	s_mov_b32 m0, s47
	v_lshl_add_u64 v[148:149], s[42:43], 0, v[148:149]
	ds_read_b128 v[192:195], v157 offset:32768
	ds_read_b128 v[196:199], v157 offset:33792
	ds_read_b128 v[200:203], v157 offset:34816
	ds_read_b128 v[204:207], v157 offset:35840
	ds_read_b128 v[208:211], v157 offset:36864
	ds_read_b128 v[212:215], v157 offset:37888
	ds_read_b128 v[216:219], v157 offset:38912
	ds_read_b128 v[220:223], v157 offset:39936
	global_load_lds_dwordx4 v[148:149], off
	v_lshl_add_u64 v[146:147], s[42:43], 0, v[146:147]
	s_mov_b32 m0, s48
	s_nop 0
	global_load_lds_dwordx4 v[146:147], off
	s_waitcnt vmcnt(8)
	s_waitcnt lgkmcnt(0)
	s_barrier
	s_setprio 1
	s_waitcnt lgkmcnt(0)
	v_mfma_f32_16x16x32_bf16 v[122:125], v[160:163], v[192:195], v[122:125]
	v_mfma_f32_16x16x32_bf16 v[126:129], v[168:171], v[192:195], v[126:129]
	v_mfma_f32_16x16x32_bf16 v[106:109], v[160:163], v[200:203], v[106:109]
	v_mfma_f32_16x16x32_bf16 v[110:113], v[168:171], v[200:203], v[110:113]
	v_mfma_f32_16x16x32_bf16 v[90:93], v[160:163], v[208:211], v[90:93]
	v_mfma_f32_16x16x32_bf16 v[94:97], v[168:171], v[208:211], v[94:97]
	v_mfma_f32_16x16x32_bf16 v[74:77], v[160:163], v[216:219], v[74:77]
	v_mfma_f32_16x16x32_bf16 v[78:81], v[168:171], v[216:219], v[78:81]
	v_mfma_f32_16x16x32_bf16 v[122:125], v[164:167], v[196:199], v[122:125]
	v_mfma_f32_16x16x32_bf16 v[126:129], v[172:175], v[196:199], v[126:129]
	v_mfma_f32_16x16x32_bf16 v[106:109], v[164:167], v[204:207], v[106:109]
	v_mfma_f32_16x16x32_bf16 v[110:113], v[172:175], v[204:207], v[110:113]
	v_mfma_f32_16x16x32_bf16 v[90:93], v[164:167], v[212:215], v[90:93]
	v_mfma_f32_16x16x32_bf16 v[94:97], v[172:175], v[212:215], v[94:97]
	v_mfma_f32_16x16x32_bf16 v[74:77], v[164:167], v[220:223], v[74:77]
	v_mfma_f32_16x16x32_bf16 v[78:81], v[172:175], v[220:223], v[78:81]
	v_mfma_f32_16x16x32_bf16 v[114:117], v[176:179], v[192:195], v[114:117]
	v_mfma_f32_16x16x32_bf16 v[118:121], v[184:187], v[192:195], v[118:121]
	v_mfma_f32_16x16x32_bf16 v[98:101], v[176:179], v[200:203], v[98:101]
	v_mfma_f32_16x16x32_bf16 v[102:105], v[184:187], v[200:203], v[102:105]
	v_mfma_f32_16x16x32_bf16 v[82:85], v[176:179], v[208:211], v[82:85]
	v_mfma_f32_16x16x32_bf16 v[86:89], v[184:187], v[208:211], v[86:89]
	v_mfma_f32_16x16x32_bf16 v[66:69], v[176:179], v[216:219], v[66:69]
	v_mfma_f32_16x16x32_bf16 v[70:73], v[184:187], v[216:219], v[70:73]
	v_mfma_f32_16x16x32_bf16 v[114:117], v[180:183], v[196:199], v[114:117]
	v_mfma_f32_16x16x32_bf16 v[118:121], v[188:191], v[196:199], v[118:121]
	v_mfma_f32_16x16x32_bf16 v[98:101], v[180:183], v[204:207], v[98:101]
	v_mfma_f32_16x16x32_bf16 v[102:105], v[188:191], v[204:207], v[102:105]
	v_mfma_f32_16x16x32_bf16 v[82:85], v[180:183], v[212:215], v[82:85]
	v_mfma_f32_16x16x32_bf16 v[86:89], v[188:191], v[212:215], v[86:89]
	v_mfma_f32_16x16x32_bf16 v[66:69], v[180:183], v[220:223], v[66:69]
	v_mfma_f32_16x16x32_bf16 v[70:73], v[188:191], v[220:223], v[70:73]
	s_setprio 0
	s_barrier
; #define PG8_STAGE2(bufoff, gbase, v0, v1) do { \
;         __builtin_amdgcn_global_load_lds((const unsigned*)((const char*)(gbase) + (v0)), (LAS unsigned*)(lds + (bufoff) + ldsw), 16, 0, 0); \
;         __builtin_amdgcn_global_load_lds((const unsigned*)((const char*)(gbase) + (v1)), (LAS unsigned*)(lds + (bufoff) + ldsw + 8192), 16, 0, 0); } while (0)
; #define PG8_STAGE(bufoff, gbase, voff) PG8_STAGE2(bufoff, gbase, (voff)[0], (voff)[1])
; #define PG8_BAR __builtin_amdgcn_s_barrier()
; template <class Epi, class Sched, bool ALIGN_EPI, bool SP2, bool GATHER>
; DI void gemm_phase(LAS unsigned char* lds, const Gemm g, const Sched& S, const Epi& E) {
;     ...
;         for (int t = 0; t < nt; t += 2) {
;             if constexpr (Epi::MID_T >= 0) { if (t == Epi::MID_T) { E.mid(acc, cur, wr, wc, fr, fq); PG8_SCHED; } }
;             const bool last = (t == nt - 2);
;             const char* a1 = cA + (size_t)(t + 1) * kstep;
;             const char* a2 = last ? nA : cA + (size_t)(t + 2) * kstep; const char* b2 = last ? nB : cB + (size_t)(t + 2) * kstep;
;             const char* a3 = a2 + kstep; const char* b3 = b2 + kstep;
;             unsigned x00 = gC[0][0], x01 = gC[0][1], x10 = gC[1][0], x11 = gC[1][1];
;             if constexpr (GATHER) { if (last) { x00 = gN[0][0]; x01 = gN[0][1]; x10 = gN[1][0]; x11 = gN[1][1]; } }
;             PG8_LDB(B0, 0, 0); PG8_LDB(B1, 0, 1); PG8_SCHED; PG8_LDA(At, 0, 0); PG8_STAGE2(PG8_SA(1, 1), a1 + hstepA, gC[1][0], gC[1][1]);
;             PG8_WAIT_V(8); PG8_WAIT_L(0); PG8_BAR; PG8_MMA(0, 0, At, B0); PG8_MMA(0, 1, At, B1); PG8_BAR; PG8_SCHED;
;             PG8_LDA(At, 0, 1); PG8_STAGE(PG8_SB(0, 0), b2, voffB); PG8_STAGE(PG8_SB(0, 1), b2 + hstep, voffB); PG8_STAGE2(PG8_SA(0, 0), a2, x00, x01);
;             PG8_WAIT_V(8); PG8_WAIT_L(0); PG8_BAR; PG8_MMA(1, 0, At, B0); PG8_MMA(1, 1, At, B1); PG8_BAR; PG8_SCHED;
;             PG8_LDB(B0, 1, 0); PG8_LDB(B1, 1, 1); PG8_SCHED; PG8_LDA(At, 1, 0); PG8_STAGE2(PG8_SA(0, 1), a2 + hstepA, x10, x11);
;             PG8_WAIT_V(8); PG8_WAIT_L(0); PG8_BAR; PG8_MMA(0, 0, At, B0); PG8_MMA(0, 1, At, B1); PG8_BAR; PG8_SCHED;
;             PG8_LDA(At, 1, 1); PG8_STAGE(PG8_SB(1, 0), b3, voffB); PG8_STAGE(PG8_SB(1, 1), b3 + hstep, voffB); PG8_STAGE2(PG8_SA(1, 0), a3, x00, x01);
;             PG8_WAIT_V(8); PG8_WAIT_L(0); PG8_BAR; PG8_MMA(1, 0, At, B0); PG8_MMA(1, 1, At, B1); PG8_BAR; PG8_SCHED;
	s_add_i32 s42, s68, s45
	v_lshl_add_u64 v[220:221], v[224:225], 0, s[14:15]
	s_mov_b32 m0, s42
	ds_read_b128 v[146:149], v157 offset:49152
	ds_read_b128 v[192:195], v157 offset:50176
	ds_read_b128 v[196:199], v157 offset:51200
	ds_read_b128 v[200:203], v157 offset:52224
	ds_read_b128 v[204:207], v157 offset:53248
	ds_read_b128 v[208:211], v157 offset:54272
	ds_read_b128 v[212:215], v157 offset:55296
	ds_read_b128 v[216:219], v157 offset:56320
	global_load_lds_dwordx4 v[220:221], off
	s_add_i32 m0, s42, 0x2000
	s_add_u32 s40, s40, 0x80080
	v_lshl_add_u64 v[220:221], v[226:227], 0, s[14:15]
	s_addc_u32 s41, s41, 0
	s_add_i32 s42, s69, s45
	global_load_lds_dwordx4 v[220:221], off
	v_lshl_add_u64 v[220:221], s[40:41], 0, v[132:133]
	s_mov_b32 m0, s42
	v_lshl_add_u64 v[150:151], v[150:151], 0, s[14:15]
	global_load_lds_dwordx4 v[220:221], off
	v_lshl_add_u64 v[220:221], s[40:41], 0, v[130:131]
	s_add_i32 m0, s42, 0x2000
	s_nop 0
	global_load_lds_dwordx4 v[220:221], off
	v_lshl_add_u64 v[220:221], v[228:229], 0, s[14:15]
	s_mov_b32 m0, s50
	s_nop 0
	global_load_lds_dwordx4 v[220:221], off
	s_mov_b32 m0, s51
	s_nop 0
	global_load_lds_dwordx4 v[150:151], off
	s_waitcnt vmcnt(8)
	s_waitcnt lgkmcnt(0)
	s_barrier
	s_setprio 1
	s_waitcnt lgkmcnt(0)
	v_mfma_f32_16x16x32_bf16 v[58:61], v[160:163], v[146:149], v[58:61]
	v_mfma_f32_16x16x32_bf16 v[62:65], v[168:171], v[146:149], v[62:65]
	v_mfma_f32_16x16x32_bf16 v[42:45], v[160:163], v[196:199], v[42:45]
	v_mfma_f32_16x16x32_bf16 v[46:49], v[168:171], v[196:199], v[46:49]
	v_mfma_f32_16x16x32_bf16 v[26:29], v[160:163], v[204:207], v[26:29]
	v_mfma_f32_16x16x32_bf16 v[30:33], v[168:171], v[204:207], v[30:33]
	v_mfma_f32_16x16x32_bf16 v[10:13], v[160:163], v[212:215], v[10:13]
	v_mfma_f32_16x16x32_bf16 v[14:17], v[168:171], v[212:215], v[14:17]
	v_mfma_f32_16x16x32_bf16 v[58:61], v[164:167], v[192:195], v[58:61]
	v_mfma_f32_16x16x32_bf16 v[62:65], v[172:175], v[192:195], v[62:65]
	v_mfma_f32_16x16x32_bf16 v[42:45], v[164:167], v[200:203], v[42:45]
	v_mfma_f32_16x16x32_bf16 v[46:49], v[172:175], v[200:203], v[46:49]
	v_mfma_f32_16x16x32_bf16 v[26:29], v[164:167], v[208:211], v[26:29]
	v_mfma_f32_16x16x32_bf16 v[30:33], v[172:175], v[208:211], v[30:33]
	v_mfma_f32_16x16x32_bf16 v[10:13], v[164:167], v[216:219], v[10:13]
	v_mfma_f32_16x16x32_bf16 v[14:17], v[172:175], v[216:219], v[14:17]
	v_mfma_f32_16x16x32_bf16 v[50:53], v[176:179], v[146:149], v[50:53]
	v_mfma_f32_16x16x32_bf16 v[54:57], v[184:187], v[146:149], v[54:57]
	v_mfma_f32_16x16x32_bf16 v[34:37], v[176:179], v[196:199], v[34:37]
	v_mfma_f32_16x16x32_bf16 v[38:41], v[184:187], v[196:199], v[38:41]
	v_mfma_f32_16x16x32_bf16 v[18:21], v[176:179], v[204:207], v[18:21]
	v_mfma_f32_16x16x32_bf16 v[22:25], v[184:187], v[204:207], v[22:25]
	v_mfma_f32_16x16x32_bf16 v[2:5], v[176:179], v[212:215], v[2:5]
	v_mfma_f32_16x16x32_bf16 v[6:9], v[184:187], v[212:215], v[6:9]
	v_mfma_f32_16x16x32_bf16 v[50:53], v[180:183], v[192:195], v[50:53]
	v_mfma_f32_16x16x32_bf16 v[54:57], v[188:191], v[192:195], v[54:57]
	v_mfma_f32_16x16x32_bf16 v[34:37], v[180:183], v[200:203], v[34:37]
	v_mfma_f32_16x16x32_bf16 v[38:41], v[188:191], v[200:203], v[38:41]
	v_mfma_f32_16x16x32_bf16 v[18:21], v[180:183], v[208:211], v[18:21]
	v_mfma_f32_16x16x32_bf16 v[22:25], v[188:191], v[208:211], v[22:25]
	v_mfma_f32_16x16x32_bf16 v[2:5], v[180:183], v[216:219], v[2:5]
	v_mfma_f32_16x16x32_bf16 v[6:9], v[188:191], v[216:219], v[6:9]
	s_setprio 0
	s_barrier
	s_add_i32 s67, s67, 2
	s_add_u32 s36, s36, 0x100
	s_addc_u32 s37, s37, 0
	s_add_u32 s65, s65, 0x100
	s_addc_u32 s66, s66, 0
	s_cmp_gt_u32 s67, 29
	s_cbranch_scc1 .LBB0_908

; #define PG8_BAR __builtin_amdgcn_s_barrier()
; template <class Epi, class Sched, bool ALIGN_EPI, bool SP2, bool GATHER>
; DI void gemm_phase(LAS unsigned char* lds, const Gemm g, const Sched& S, const Epi& E) {
;     ...
;     for (;;) {
;         const bool has_next = S.next(ui + 1, nxt);
;         const char* nA = (has_next && !GATHER) ? (const char*)g.A + (size_t)nxt.pm * tstep : cA; const char* nB = has_next ? (const char*)g.Bt + (size_t)nxt.pn * tstep : cB;
;         if constexpr (GATHER) { if (has_next) { PG8_GATHER(nxt, gN); } else {
; #pragma unroll
;             for (int h = 0; h < 2; ++h) { gN[h][0] = gC[h][0]; gN[h][1] = gC[h][1]; } } }
;         for (int t = 0; t < nt; t += 2) {
;             if constexpr (Epi::MID_T >= 0) { if (t == Epi::MID_T) { E.mid(acc, cur, wr, wc, fr, fq); PG8_SCHED; } }
;             const bool last = (t == nt - 2);
;             const char* a1 = cA + (size_t)(t + 1) * kstep;
;             const char* a2 = last ? nA : cA + (size_t)(t + 2) * kstep; const char* b2 = last ? nB : cB + (size_t)(t + 2) * kstep;
;             const char* a3 = a2 + kstep; const char* b3 = b2 + kstep;
;             unsigned x00 = gC[0][0], x01 = gC[0][1], x10 = gC[1][0], x11 = gC[1][1];
;             if constexpr (GATHER) { if (last) { x00 = gN[0][0]; x01 = gN[0][1]; x10 = gN[1][0]; x11 = gN[1][1]; } }
;             PG8_LDB(B0, 0, 0); PG8_LDB(B1, 0, 1); PG8_SCHED; PG8_LDA(At, 0, 0); PG8_STAGE2(PG8_SA(1, 1), a1 + hstepA, gC[1][0], gC[1][1]);
;             PG8_WAIT_V(8); PG8_WAIT_L(0); PG8_BAR; PG8_MMA(0, 0, At, B0); PG8_MMA(0, 1, At, B1); PG8_BAR; PG8_SCHED;
;             PG8_LDA(At, 0, 1); PG8_STAGE(PG8_SB(0, 0), b2, voffB); PG8_STAGE(PG8_SB(0, 1), b2 + hstep, voffB); PG8_STAGE2(PG8_SA(0, 0), a2, x00, x01);
;             PG8_WAIT_V(8); PG8_WAIT_L(0); PG8_BAR; PG8_MMA(1, 0, At, B0); PG8_MMA(1, 1, At, B1); PG8_BAR; PG8_SCHED;
;             PG8_LDB(B0, 1, 0); PG8_LDB(B1, 1, 1); PG8_SCHED; PG8_LDA(At, 1, 0); PG8_STAGE2(PG8_SA(0, 1), a2 + hstepA, x10, x11);
;             PG8_WAIT_V(8); PG8_WAIT_L(0); PG8_BAR; PG8_MMA(0, 0, At, B0); PG8_MMA(0, 1, At, B1); PG8_BAR; PG8_SCHED;
;             PG8_LDA(At, 1, 1); PG8_STAGE(PG8_SB(1, 0), b3, voffB); PG8_STAGE(PG8_SB(1, 1), b3 + hstep, voffB); PG8_STAGE2(PG8_SA(1, 0), a3, x00, x01);
;             PG8_WAIT_V(8); PG8_WAIT_L(0); PG8_BAR; PG8_MMA(1, 0, At, B0); PG8_MMA(1, 1, At, B1); PG8_BAR; PG8_SCHED;
.LBB0_995:
	s_ashr_i32 s15, s14, 31
	s_lshl_b64 s[20:21], s[14:15], 18
	s_add_u32 s20, s37, s20
	s_addc_u32 s21, s38, s21
	s_and_b64 s[22:23], s[18:19], exec
	s_cselect_b32 s15, s21, s29
	s_cselect_b32 s25, s20, s28
	s_ashr_i32 s17, s16, 31
	s_lshl_b64 s[22:23], s[16:17], 18
	s_add_u32 s22, s39, s22
	s_addc_u32 s23, s40, s23
	s_and_b64 s[34:35], s[18:19], exec
	s_cselect_b32 s17, s23, s31
	s_cselect_b32 s50, s22, s30
	s_add_u32 s28, s28, 0x20080
	s_addc_u32 s29, s29, 0
	s_add_u32 s51, s30, 0x100
	s_addc_u32 s52, s31, 0
	s_mov_b32 s53, -2
	ds_read_b128 v[144:147], v154
	ds_read_b128 v[148:151], v154 offset:1024
	ds_read_b128 v[158:161], v154 offset:2048
	ds_read_b128 v[162:165], v154 offset:3072
	ds_read_b128 v[166:169], v155
	ds_read_b128 v[170:173], v155 offset:1024
	ds_read_b128 v[174:177], v155 offset:2048
	ds_read_b128 v[178:181], v155 offset:3072
	s_add_u32 s30, s28, 0xfffe0080
	s_addc_u32 s31, s29, -1
	s_cmp_eq_u32 s53, 4
	s_cselect_b32 s35, s15, s31
	s_cselect_b32 s34, s25, s30
	s_cselect_b32 s31, s17, s52
	s_cselect_b32 s30, s50, s51
	v_lshl_add_u64 v[214:215], s[28:29], 0, v[140:141]
	s_add_i32 m0, s27, 0xc000
	ds_read_b128 v[182:185], v156
	ds_read_b128 v[186:189], v156 offset:1024
	ds_read_b128 v[190:193], v156 offset:2048
	ds_read_b128 v[194:197], v156 offset:3072
	ds_read_b128 v[198:201], v156 offset:4096
	ds_read_b128 v[202:205], v156 offset:5120
	ds_read_b128 v[206:209], v156 offset:6144
	ds_read_b128 v[210:213], v156 offset:7168
	global_load_lds_dwordx4 v[214:215], off
	v_lshl_add_u64 v[214:215], s[28:29], 0, v[142:143]
	s_add_i32 m0, s27, 0xe000
	s_nop 0
	global_load_lds_dwordx4 v[214:215], off
	s_waitcnt vmcnt(8)
	s_waitcnt lgkmcnt(0)
	s_barrier
	s_setprio 1
	s_waitcnt lgkmcnt(0)
	v_mfma_f32_16x16x32_bf16 v[126:129], v[144:147], v[182:185], 0
	v_mfma_f32_16x16x32_bf16 v[122:125], v[158:161], v[182:185], 0
	v_mfma_f32_16x16x32_bf16 v[110:113], v[144:147], v[190:193], 0
	v_mfma_f32_16x16x32_bf16 v[106:109], v[158:161], v[190:193], 0
	v_mfma_f32_16x16x32_bf16 v[94:97], v[144:147], v[198:201], 0
	v_mfma_f32_16x16x32_bf16 v[90:93], v[158:161], v[198:201], 0
	v_mfma_f32_16x16x32_bf16 v[78:81], v[144:147], v[206:209], 0
	v_mfma_f32_16x16x32_bf16 v[74:77], v[158:161], v[206:209], 0
	v_mfma_f32_16x16x32_bf16 v[126:129], v[148:151], v[186:189], v[126:129]
	v_mfma_f32_16x16x32_bf16 v[122:125], v[162:165], v[186:189], v[122:125]
	v_mfma_f32_16x16x32_bf16 v[110:113], v[148:151], v[194:197], v[110:113]
	v_mfma_f32_16x16x32_bf16 v[106:109], v[162:165], v[194:197], v[106:109]
	v_mfma_f32_16x16x32_bf16 v[94:97], v[148:151], v[202:205], v[94:97]
	v_mfma_f32_16x16x32_bf16 v[90:93], v[162:165], v[202:205], v[90:93]
	v_mfma_f32_16x16x32_bf16 v[78:81], v[148:151], v[210:213], v[78:81]
	v_mfma_f32_16x16x32_bf16 v[74:77], v[162:165], v[210:213], v[74:77]
	v_mfma_f32_16x16x32_bf16 v[118:121], v[166:169], v[182:185], 0
	v_mfma_f32_16x16x32_bf16 v[114:117], v[174:177], v[182:185], 0
	v_mfma_f32_16x16x32_bf16 v[102:105], v[166:169], v[190:193], 0
	v_mfma_f32_16x16x32_bf16 v[98:101], v[174:177], v[190:193], 0
	v_mfma_f32_16x16x32_bf16 v[86:89], v[166:169], v[198:201], 0
	v_mfma_f32_16x16x32_bf16 v[82:85], v[174:177], v[198:201], 0
	v_mfma_f32_16x16x32_bf16 v[70:73], v[166:169], v[206:209], 0
	v_mfma_f32_16x16x32_bf16 v[66:69], v[174:177], v[206:209], 0
	v_mfma_f32_16x16x32_bf16 v[118:121], v[170:173], v[186:189], v[118:121]
	v_mfma_f32_16x16x32_bf16 v[114:117], v[178:181], v[186:189], v[114:117]
	v_mfma_f32_16x16x32_bf16 v[102:105], v[170:173], v[194:197], v[102:105]
	v_mfma_f32_16x16x32_bf16 v[98:101], v[178:181], v[194:197], v[98:101]
	v_mfma_f32_16x16x32_bf16 v[86:89], v[170:173], v[202:205], v[86:89]
	v_mfma_f32_16x16x32_bf16 v[82:85], v[178:181], v[202:205], v[82:85]
	v_mfma_f32_16x16x32_bf16 v[70:73], v[170:173], v[210:213], v[70:73]
	v_mfma_f32_16x16x32_bf16 v[66:69], v[178:181], v[210:213], v[66:69]
	s_setprio 0
	s_barrier
	s_add_i32 s54, s48, s41
	v_lshl_add_u64 v[214:215], s[30:31], 0, v[132:133]
	s_mov_b32 m0, s54
	ds_read_b128 v[182:185], v156 offset:16384
	ds_read_b128 v[186:189], v156 offset:17408
	ds_read_b128 v[190:193], v156 offset:18432
	ds_read_b128 v[194:197], v156 offset:19456
	ds_read_b128 v[198:201], v156 offset:20480
	ds_read_b128 v[202:205], v156 offset:21504
	ds_read_b128 v[206:209], v156 offset:22528
	ds_read_b128 v[210:213], v156 offset:23552
	global_load_lds_dwordx4 v[214:215], off
	s_add_i32 m0, s54, 0x2000
	s_add_u32 s54, s30, 0x20000
	v_lshl_add_u64 v[216:217], s[30:31], 0, v[136:137]
	s_addc_u32 s55, s31, 0
	s_add_i32 s56, s49, s41
	global_load_lds_dwordx4 v[216:217], off
	v_lshl_add_u64 v[218:219], s[54:55], 0, v[132:133]
	s_mov_b32 m0, s56
	v_lshl_add_u64 v[220:221], s[34:35], 0, v[134:135]
	global_load_lds_dwordx4 v[218:219], off
	v_lshl_add_u64 v[218:219], s[54:55], 0, v[136:137]
	s_add_i32 m0, s56, 0x2000
	s_nop 0
	global_load_lds_dwordx4 v[218:219], off
	v_lshl_add_u64 v[218:219], s[34:35], 0, v[130:131]
	s_mov_b32 m0, s27
	s_nop 0
	global_load_lds_dwordx4 v[218:219], off
	s_mov_b32 m0, s42
	s_nop 0
	global_load_lds_dwordx4 v[220:221], off
	s_waitcnt vmcnt(8)
	s_waitcnt lgkmcnt(0)
	s_barrier
; #define PG8_STAGE2(bufoff, gbase, v0, v1) do { \
;         __builtin_amdgcn_global_load_lds((const unsigned*)((const char*)(gbase) + (v0)), (LAS unsigned*)(lds + (bufoff) + ldsw), 16, 0, 0); \
;         __builtin_amdgcn_global_load_lds((const unsigned*)((const char*)(gbase) + (v1)), (LAS unsigned*)(lds + (bufoff) + ldsw + 8192), 16, 0, 0); } while (0)
; #define PG8_STAGE(bufoff, gbase, voff) PG8_STAGE2(bufoff, gbase, (voff)[0], (voff)[1])
; #define PG8_LDA(dst, b, h) do { _Pragma("unroll") for (int m = 0; m < 4; ++m) _Pragma("unroll") for (int k = 0; k < 2; ++k) dst[m][k] = *(const LAS bf16x8*)(lds + PG8_SA(b, h) + aoff + m * 2048 + k * 1024); } while (0)
; #define PG8_LDB(dst, b, h) do { _Pragma("unroll") for (int n = 0; n < 2; ++n) _Pragma("unroll") for (int k = 0; k < 2; ++k) dst[n][k] = *(const LAS bf16x8*)(lds + PG8_SB(b, h) + boff + n * 2048 + k * 1024); } while (0)
; #define PG8_WAIT_V(n) asm volatile("s_waitcnt vmcnt(" #n ")" ::: "memory")
; #define PG8_WAIT_L(n) asm volatile("s_waitcnt lgkmcnt(" #n ")" ::: "memory")
; #define PG8_BAR __builtin_amdgcn_s_barrier()
; #define PG8_SCHED __builtin_amdgcn_sched_barrier(0)
; template <class Epi, class Sched, bool ALIGN_EPI, bool SP2, bool GATHER>
; DI void gemm_phase(LAS unsigned char* lds, const Gemm g, const Sched& S, const Epi& E) {
;     ...
;             PG8_LDB(B0, 0, 0); PG8_LDB(B1, 0, 1); PG8_SCHED; PG8_LDA(At, 0, 0); PG8_STAGE2(PG8_SA(1, 1), a1 + hstepA, gC[1][0], gC[1][1]);
;             PG8_WAIT_V(8); PG8_WAIT_L(0); PG8_BAR; PG8_MMA(0, 0, At, B0); PG8_MMA(0, 1, At, B1); PG8_BAR; PG8_SCHED;
;             PG8_LDA(At, 0, 1); PG8_STAGE(PG8_SB(0, 0), b2, voffB); PG8_STAGE(PG8_SB(0, 1), b2 + hstep, voffB); PG8_STAGE2(PG8_SA(0, 0), a2, x00, x01);
;             PG8_WAIT_V(8); PG8_WAIT_L(0); PG8_BAR; PG8_MMA(1, 0, At, B0); PG8_MMA(1, 1, At, B1); PG8_BAR; PG8_SCHED;
;             PG8_LDB(B0, 1, 0); PG8_LDB(B1, 1, 1); PG8_SCHED; PG8_LDA(At, 1, 0); PG8_STAGE2(PG8_SA(0, 1), a2 + hstepA, x10, x11);
;             PG8_WAIT_V(8); PG8_WAIT_L(0); PG8_BAR; PG8_MMA(0, 0, At, B0); PG8_MMA(0, 1, At, B1); PG8_BAR; PG8_SCHED;
;             PG8_LDA(At, 1, 1); PG8_STAGE(PG8_SB(1, 0), b3, voffB); PG8_STAGE(PG8_SB(1, 1), b3 + hstep, voffB); PG8_STAGE2(PG8_SA(1, 0), a3, x00, x01);
;             PG8_WAIT_V(8); PG8_WAIT_L(0); PG8_BAR; PG8_MMA(1, 0, At, B0); PG8_MMA(1, 1, At, B1); PG8_BAR; PG8_SCHED;
	s_setprio 1
	s_waitcnt lgkmcnt(0)
	v_mfma_f32_16x16x32_bf16 v[62:65], v[144:147], v[182:185], 0
	v_mfma_f32_16x16x32_bf16 v[58:61], v[158:161], v[182:185], 0
	v_mfma_f32_16x16x32_bf16 v[46:49], v[144:147], v[190:193], 0
	v_mfma_f32_16x16x32_bf16 v[42:45], v[158:161], v[190:193], 0
	v_mfma_f32_16x16x32_bf16 v[14:17], v[144:147], v[198:201], 0
	v_mfma_f32_16x16x32_bf16 v[10:13], v[158:161], v[198:201], 0
	v_mfma_f32_16x16x32_bf16 v[6:9], v[144:147], v[206:209], 0
	v_mfma_f32_16x16x32_bf16 v[2:5], v[158:161], v[206:209], 0
	v_mfma_f32_16x16x32_bf16 v[62:65], v[148:151], v[186:189], v[62:65]
	v_mfma_f32_16x16x32_bf16 v[58:61], v[162:165], v[186:189], v[58:61]
	v_mfma_f32_16x16x32_bf16 v[46:49], v[148:151], v[194:197], v[46:49]
	v_mfma_f32_16x16x32_bf16 v[42:45], v[162:165], v[194:197], v[42:45]
	v_mfma_f32_16x16x32_bf16 v[14:17], v[148:151], v[202:205], v[14:17]
	v_mfma_f32_16x16x32_bf16 v[10:13], v[162:165], v[202:205], v[10:13]
	v_mfma_f32_16x16x32_bf16 v[6:9], v[148:151], v[210:213], v[6:9]
	v_mfma_f32_16x16x32_bf16 v[2:5], v[162:165], v[210:213], v[2:5]
	v_mfma_f32_16x16x32_bf16 v[54:57], v[166:169], v[182:185], 0
	v_mfma_f32_16x16x32_bf16 v[50:53], v[174:177], v[182:185], 0
	v_mfma_f32_16x16x32_bf16 v[30:33], v[166:169], v[190:193], 0
	v_mfma_f32_16x16x32_bf16 v[26:29], v[174:177], v[190:193], 0
	v_mfma_f32_16x16x32_bf16 v[34:37], v[166:169], v[198:201], 0
	v_mfma_f32_16x16x32_bf16 v[38:41], v[174:177], v[198:201], 0
	v_mfma_f32_16x16x32_bf16 v[18:21], v[166:169], v[206:209], 0
	v_mfma_f32_16x16x32_bf16 v[22:25], v[174:177], v[206:209], 0
	v_mfma_f32_16x16x32_bf16 v[54:57], v[170:173], v[186:189], v[54:57]
	v_mfma_f32_16x16x32_bf16 v[50:53], v[178:181], v[186:189], v[50:53]
	v_mfma_f32_16x16x32_bf16 v[30:33], v[170:173], v[194:197], v[30:33]
	v_mfma_f32_16x16x32_bf16 v[26:29], v[178:181], v[194:197], v[26:29]
	v_mfma_f32_16x16x32_bf16 v[34:37], v[170:173], v[202:205], v[34:37]
	v_mfma_f32_16x16x32_bf16 v[38:41], v[178:181], v[202:205], v[38:41]
	v_mfma_f32_16x16x32_bf16 v[18:21], v[170:173], v[210:213], v[18:21]
	v_mfma_f32_16x16x32_bf16 v[22:25], v[178:181], v[210:213], v[22:25]
	s_setprio 0
	s_barrier
	s_add_i32 s54, 0, 0x18000
	v_add_u32_e32 v138, s54, v152
	s_add_i32 s55, 0, 0x1c000
	ds_read_b128 v[144:147], v138
	ds_read_b128 v[148:151], v138 offset:1024
	ds_read_b128 v[158:161], v138 offset:2048
	ds_read_b128 v[162:165], v138 offset:3072
	v_add_u32_e32 v138, s55, v152
	ds_read_b128 v[166:169], v138
	ds_read_b128 v[170:173], v138 offset:1024
	ds_read_b128 v[174:177], v138 offset:2048
	ds_read_b128 v[178:181], v138 offset:3072
	s_add_u32 s34, s34, 0x20000
	s_addc_u32 s35, s35, 0
	s_mov_b32 m0, s43
	v_lshl_add_u64 v[222:223], s[34:35], 0, v[130:131]
	ds_read_b128 v[182:185], v156 offset:32768
	ds_read_b128 v[186:189], v156 offset:33792
	ds_read_b128 v[190:193], v156 offset:34816
	ds_read_b128 v[194:197], v156 offset:35840
	ds_read_b128 v[198:201], v156 offset:36864
	ds_read_b128 v[202:205], v156 offset:37888
	ds_read_b128 v[206:209], v156 offset:38912
	ds_read_b128 v[210:213], v156 offset:39936
	global_load_lds_dwordx4 v[222:223], off
	v_lshl_add_u64 v[222:223], s[34:35], 0, v[134:135]
	s_mov_b32 m0, s44
	s_nop 0
	global_load_lds_dwordx4 v[222:223], off
	s_waitcnt vmcnt(8)
	s_waitcnt lgkmcnt(0)
	s_barrier
	s_setprio 1
	s_waitcnt lgkmcnt(0)
	v_mfma_f32_16x16x32_bf16 v[126:129], v[144:147], v[182:185], v[126:129]
	v_mfma_f32_16x16x32_bf16 v[122:125], v[158:161], v[182:185], v[122:125]
	v_mfma_f32_16x16x32_bf16 v[110:113], v[144:147], v[190:193], v[110:113]
	v_mfma_f32_16x16x32_bf16 v[106:109], v[158:161], v[190:193], v[106:109]
	v_mfma_f32_16x16x32_bf16 v[94:97], v[144:147], v[198:201], v[94:97]
	v_mfma_f32_16x16x32_bf16 v[90:93], v[158:161], v[198:201], v[90:93]
	v_mfma_f32_16x16x32_bf16 v[78:81], v[144:147], v[206:209], v[78:81]
	v_mfma_f32_16x16x32_bf16 v[74:77], v[158:161], v[206:209], v[74:77]
	v_mfma_f32_16x16x32_bf16 v[126:129], v[148:151], v[186:189], v[126:129]
	v_mfma_f32_16x16x32_bf16 v[122:125], v[162:165], v[186:189], v[122:125]
	v_mfma_f32_16x16x32_bf16 v[110:113], v[148:151], v[194:197], v[110:113]
	v_mfma_f32_16x16x32_bf16 v[106:109], v[162:165], v[194:197], v[106:109]
	v_mfma_f32_16x16x32_bf16 v[94:97], v[148:151], v[202:205], v[94:97]
	v_mfma_f32_16x16x32_bf16 v[90:93], v[162:165], v[202:205], v[90:93]
	v_mfma_f32_16x16x32_bf16 v[78:81], v[148:151], v[210:213], v[78:81]
	v_mfma_f32_16x16x32_bf16 v[74:77], v[162:165], v[210:213], v[74:77]
	v_mfma_f32_16x16x32_bf16 v[118:121], v[166:169], v[182:185], v[118:121]
	v_mfma_f32_16x16x32_bf16 v[114:117], v[174:177], v[182:185], v[114:117]
	v_mfma_f32_16x16x32_bf16 v[102:105], v[166:169], v[190:193], v[102:105]
	v_mfma_f32_16x16x32_bf16 v[98:101], v[174:177], v[190:193], v[98:101]
	v_mfma_f32_16x16x32_bf16 v[86:89], v[166:169], v[198:201], v[86:89]
	v_mfma_f32_16x16x32_bf16 v[82:85], v[174:177], v[198:201], v[82:85]
	v_mfma_f32_16x16x32_bf16 v[70:73], v[166:169], v[206:209], v[70:73]
	v_mfma_f32_16x16x32_bf16 v[66:69], v[174:177], v[206:209], v[66:69]
	v_mfma_f32_16x16x32_bf16 v[118:121], v[170:173], v[186:189], v[118:121]
	v_mfma_f32_16x16x32_bf16 v[114:117], v[178:181], v[186:189], v[114:117]
	v_mfma_f32_16x16x32_bf16 v[102:105], v[170:173], v[194:197], v[102:105]
	v_mfma_f32_16x16x32_bf16 v[98:101], v[178:181], v[194:197], v[98:101]
	v_mfma_f32_16x16x32_bf16 v[86:89], v[170:173], v[202:205], v[86:89]
	v_mfma_f32_16x16x32_bf16 v[82:85], v[178:181], v[202:205], v[82:85]
	v_mfma_f32_16x16x32_bf16 v[70:73], v[170:173], v[210:213], v[70:73]
	v_mfma_f32_16x16x32_bf16 v[66:69], v[178:181], v[210:213], v[66:69]
	s_setprio 0
	s_barrier
; #define PG8_STAGE2(bufoff, gbase, v0, v1) do { \
;         __builtin_amdgcn_global_load_lds((const unsigned*)((const char*)(gbase) + (v0)), (LAS unsigned*)(lds + (bufoff) + ldsw), 16, 0, 0); \
;         __builtin_amdgcn_global_load_lds((const unsigned*)((const char*)(gbase) + (v1)), (LAS unsigned*)(lds + (bufoff) + ldsw + 8192), 16, 0, 0); } while (0)
; #define PG8_STAGE(bufoff, gbase, voff) PG8_STAGE2(bufoff, gbase, (voff)[0], (voff)[1])
; #define PG8_BAR __builtin_amdgcn_s_barrier()
; template <class Epi, class Sched, bool ALIGN_EPI, bool SP2, bool GATHER>
; DI void gemm_phase(LAS unsigned char* lds, const Gemm g, const Sched& S, const Epi& E) {
;     ...
;         for (int t = 0; t < nt; t += 2) {
;             if constexpr (Epi::MID_T >= 0) { if (t == Epi::MID_T) { E.mid(acc, cur, wr, wc, fr, fq); PG8_SCHED; } }
;             const bool last = (t == nt - 2);
;             const char* a1 = cA + (size_t)(t + 1) * kstep;
;             const char* a2 = last ? nA : cA + (size_t)(t + 2) * kstep; const char* b2 = last ? nB : cB + (size_t)(t + 2) * kstep;
;             const char* a3 = a2 + kstep; const char* b3 = b2 + kstep;
;             unsigned x00 = gC[0][0], x01 = gC[0][1], x10 = gC[1][0], x11 = gC[1][1];
;             if constexpr (GATHER) { if (last) { x00 = gN[0][0]; x01 = gN[0][1]; x10 = gN[1][0]; x11 = gN[1][1]; } }
;             PG8_LDB(B0, 0, 0); PG8_LDB(B1, 0, 1); PG8_SCHED; PG8_LDA(At, 0, 0); PG8_STAGE2(PG8_SA(1, 1), a1 + hstepA, gC[1][0], gC[1][1]);
;             PG8_WAIT_V(8); PG8_WAIT_L(0); PG8_BAR; PG8_MMA(0, 0, At, B0); PG8_MMA(0, 1, At, B1); PG8_BAR; PG8_SCHED;
;             PG8_LDA(At, 0, 1); PG8_STAGE(PG8_SB(0, 0), b2, voffB); PG8_STAGE(PG8_SB(0, 1), b2 + hstep, voffB); PG8_STAGE2(PG8_SA(0, 0), a2, x00, x01);
;             PG8_WAIT_V(8); PG8_WAIT_L(0); PG8_BAR; PG8_MMA(1, 0, At, B0); PG8_MMA(1, 1, At, B1); PG8_BAR; PG8_SCHED;
;             PG8_LDB(B0, 1, 0); PG8_LDB(B1, 1, 1); PG8_SCHED; PG8_LDA(At, 1, 0); PG8_STAGE2(PG8_SA(0, 1), a2 + hstepA, x10, x11);
;             PG8_WAIT_V(8); PG8_WAIT_L(0); PG8_BAR; PG8_MMA(0, 0, At, B0); PG8_MMA(0, 1, At, B1); PG8_BAR; PG8_SCHED;
;             PG8_LDA(At, 1, 1); PG8_STAGE(PG8_SB(1, 0), b3, voffB); PG8_STAGE(PG8_SB(1, 1), b3 + hstep, voffB); PG8_STAGE2(PG8_SA(1, 0), a3, x00, x01);
;             PG8_WAIT_V(8); PG8_WAIT_L(0); PG8_BAR; PG8_MMA(1, 0, At, B0); PG8_MMA(1, 1, At, B1); PG8_BAR; PG8_SCHED;
	s_add_i32 s34, s54, s41
	v_lshl_add_u64 v[214:215], v[214:215], 0, s[10:11]
	s_mov_b32 m0, s34
	ds_read_b128 v[182:185], v156 offset:49152
	ds_read_b128 v[186:189], v156 offset:50176
	ds_read_b128 v[190:193], v156 offset:51200
	ds_read_b128 v[194:197], v156 offset:52224
	ds_read_b128 v[198:201], v156 offset:53248
	ds_read_b128 v[202:205], v156 offset:54272
	ds_read_b128 v[206:209], v156 offset:55296
	ds_read_b128 v[210:213], v156 offset:56320
	global_load_lds_dwordx4 v[214:215], off
	s_add_i32 m0, s34, 0x2000
	s_add_u32 s30, s30, 0x20080
	v_lshl_add_u64 v[214:215], v[216:217], 0, s[10:11]
	s_addc_u32 s31, s31, 0
	s_add_i32 s34, s55, s41
	global_load_lds_dwordx4 v[214:215], off
	v_lshl_add_u64 v[214:215], s[30:31], 0, v[132:133]
	s_mov_b32 m0, s34
	s_nop 0
	global_load_lds_dwordx4 v[214:215], off
	v_lshl_add_u64 v[214:215], s[30:31], 0, v[136:137]
	s_add_i32 m0, s34, 0x2000
	s_nop 0
	global_load_lds_dwordx4 v[214:215], off
	v_lshl_add_u64 v[214:215], v[218:219], 0, s[10:11]
	s_mov_b32 m0, s46
	s_nop 0
	global_load_lds_dwordx4 v[214:215], off
	v_lshl_add_u64 v[214:215], v[220:221], 0, s[10:11]
	s_mov_b32 m0, s47
	s_nop 0
	global_load_lds_dwordx4 v[214:215], off
	s_waitcnt vmcnt(8)
	s_waitcnt lgkmcnt(0)
	s_barrier
	s_setprio 1
	s_waitcnt lgkmcnt(0)
	v_mfma_f32_16x16x32_bf16 v[62:65], v[144:147], v[182:185], v[62:65]
	v_mfma_f32_16x16x32_bf16 v[58:61], v[158:161], v[182:185], v[58:61]
	v_mfma_f32_16x16x32_bf16 v[46:49], v[144:147], v[190:193], v[46:49]
	v_mfma_f32_16x16x32_bf16 v[42:45], v[158:161], v[190:193], v[42:45]
	v_mfma_f32_16x16x32_bf16 v[14:17], v[144:147], v[198:201], v[14:17]
	v_mfma_f32_16x16x32_bf16 v[10:13], v[158:161], v[198:201], v[10:13]
	v_mfma_f32_16x16x32_bf16 v[6:9], v[144:147], v[206:209], v[6:9]
	v_mfma_f32_16x16x32_bf16 v[2:5], v[158:161], v[206:209], v[2:5]
	v_mfma_f32_16x16x32_bf16 v[62:65], v[148:151], v[186:189], v[62:65]
	v_mfma_f32_16x16x32_bf16 v[58:61], v[162:165], v[186:189], v[58:61]
	v_mfma_f32_16x16x32_bf16 v[46:49], v[148:151], v[194:197], v[46:49]
	v_mfma_f32_16x16x32_bf16 v[42:45], v[162:165], v[194:197], v[42:45]
	v_mfma_f32_16x16x32_bf16 v[14:17], v[148:151], v[202:205], v[14:17]
	v_mfma_f32_16x16x32_bf16 v[10:13], v[162:165], v[202:205], v[10:13]
	v_mfma_f32_16x16x32_bf16 v[6:9], v[148:151], v[210:213], v[6:9]
	v_mfma_f32_16x16x32_bf16 v[2:5], v[162:165], v[210:213], v[2:5]
	v_mfma_f32_16x16x32_bf16 v[54:57], v[166:169], v[182:185], v[54:57]
	v_mfma_f32_16x16x32_bf16 v[50:53], v[174:177], v[182:185], v[50:53]
	v_mfma_f32_16x16x32_bf16 v[30:33], v[166:169], v[190:193], v[30:33]
	v_mfma_f32_16x16x32_bf16 v[26:29], v[174:177], v[190:193], v[26:29]
	v_mfma_f32_16x16x32_bf16 v[34:37], v[166:169], v[198:201], v[34:37]
	v_mfma_f32_16x16x32_bf16 v[38:41], v[174:177], v[198:201], v[38:41]
	v_mfma_f32_16x16x32_bf16 v[18:21], v[166:169], v[206:209], v[18:21]
	v_mfma_f32_16x16x32_bf16 v[22:25], v[174:177], v[206:209], v[22:25]
	v_mfma_f32_16x16x32_bf16 v[54:57], v[170:173], v[186:189], v[54:57]
	v_mfma_f32_16x16x32_bf16 v[50:53], v[178:181], v[186:189], v[50:53]
	v_mfma_f32_16x16x32_bf16 v[30:33], v[170:173], v[194:197], v[30:33]
	v_mfma_f32_16x16x32_bf16 v[26:29], v[178:181], v[194:197], v[26:29]
	v_mfma_f32_16x16x32_bf16 v[34:37], v[170:173], v[202:205], v[34:37]
	v_mfma_f32_16x16x32_bf16 v[38:41], v[178:181], v[202:205], v[38:41]
	v_mfma_f32_16x16x32_bf16 v[18:21], v[170:173], v[210:213], v[18:21]
	v_mfma_f32_16x16x32_bf16 v[22:25], v[178:181], v[210:213], v[22:25]
	s_setprio 0
	s_barrier
	s_add_i32 s53, s53, 2
	s_add_u32 s28, s28, 0x100
	s_addc_u32 s29, s29, 0
	s_add_u32 s51, s51, 0x100
	s_addc_u32 s52, s52, 0
	s_cmp_gt_u32 s53, 5
	s_cbranch_scc1 .Lpeel_exit_p10
.LBB0_996:
	ds_read_b128 v[144:147], v154
	ds_read_b128 v[148:151], v154 offset:1024
	ds_read_b128 v[158:161], v154 offset:2048
	ds_read_b128 v[162:165], v154 offset:3072
	ds_read_b128 v[166:169], v155
	ds_read_b128 v[170:173], v155 offset:1024
	ds_read_b128 v[174:177], v155 offset:2048
	ds_read_b128 v[178:181], v155 offset:3072
	s_add_u32 s30, s28, 0xfffe0080
	s_addc_u32 s31, s29, -1
	s_cmp_eq_u32 s53, 4
	s_cselect_b32 s35, s15, s31
	s_cselect_b32 s34, s25, s30
	s_cselect_b32 s31, s17, s52
	s_cselect_b32 s30, s50, s51
	v_lshl_add_u64 v[214:215], s[28:29], 0, v[140:141]
	s_add_i32 m0, s27, 0xc000
	ds_read_b128 v[182:185], v156
	ds_read_b128 v[186:189], v156 offset:1024
	ds_read_b128 v[190:193], v156 offset:2048
	ds_read_b128 v[194:197], v156 offset:3072
	ds_read_b128 v[198:201], v156 offset:4096
	ds_read_b128 v[202:205], v156 offset:5120
	ds_read_b128 v[206:209], v156 offset:6144
	ds_read_b128 v[210:213], v156 offset:7168
	global_load_lds_dwordx4 v[214:215], off
	v_lshl_add_u64 v[214:215], s[28:29], 0, v[142:143]
	s_add_i32 m0, s27, 0xe000
	s_nop 0
	global_load_lds_dwordx4 v[214:215], off
	s_waitcnt vmcnt(8)
	s_waitcnt lgkmcnt(0)
	s_barrier
; #define PG8_STAGE2(bufoff, gbase, v0, v1) do { \
;         __builtin_amdgcn_global_load_lds((const unsigned*)((const char*)(gbase) + (v0)), (LAS unsigned*)(lds + (bufoff) + ldsw), 16, 0, 0); \
;         __builtin_amdgcn_global_load_lds((const unsigned*)((const char*)(gbase) + (v1)), (LAS unsigned*)(lds + (bufoff) + ldsw + 8192), 16, 0, 0); } while (0)
; #define PG8_STAGE(bufoff, gbase, voff) PG8_STAGE2(bufoff, gbase, (voff)[0], (voff)[1])
; #define PG8_LDA(dst, b, h) do { _Pragma("unroll") for (int m = 0; m < 4; ++m) _Pragma("unroll") for (int k = 0; k < 2; ++k) dst[m][k] = *(const LAS bf16x8*)(lds + PG8_SA(b, h) + aoff + m * 2048 + k * 1024); } while (0)
; #define PG8_LDB(dst, b, h) do { _Pragma("unroll") for (int n = 0; n < 2; ++n) _Pragma("unroll") for (int k = 0; k < 2; ++k) dst[n][k] = *(const LAS bf16x8*)(lds + PG8_SB(b, h) + boff + n * 2048 + k * 1024); } while (0)
; #define PG8_WAIT_V(n) asm volatile("s_waitcnt vmcnt(" #n ")" ::: "memory")
; #define PG8_WAIT_L(n) asm volatile("s_waitcnt lgkmcnt(" #n ")" ::: "memory")
; #define PG8_BAR __builtin_amdgcn_s_barrier()
; #define PG8_SCHED __builtin_amdgcn_sched_barrier(0)
; template <class Epi, class Sched, bool ALIGN_EPI, bool SP2, bool GATHER>
; DI void gemm_phase(LAS unsigned char* lds, const Gemm g, const Sched& S, const Epi& E) {
;     ...
;             PG8_LDB(B0, 0, 0); PG8_LDB(B1, 0, 1); PG8_SCHED; PG8_LDA(At, 0, 0); PG8_STAGE2(PG8_SA(1, 1), a1 + hstepA, gC[1][0], gC[1][1]);
;             PG8_WAIT_V(8); PG8_WAIT_L(0); PG8_BAR; PG8_MMA(0, 0, At, B0); PG8_MMA(0, 1, At, B1); PG8_BAR; PG8_SCHED;
;             PG8_LDA(At, 0, 1); PG8_STAGE(PG8_SB(0, 0), b2, voffB); PG8_STAGE(PG8_SB(0, 1), b2 + hstep, voffB); PG8_STAGE2(PG8_SA(0, 0), a2, x00, x01);
;             PG8_WAIT_V(8); PG8_WAIT_L(0); PG8_BAR; PG8_MMA(1, 0, At, B0); PG8_MMA(1, 1, At, B1); PG8_BAR; PG8_SCHED;
;             PG8_LDB(B0, 1, 0); PG8_LDB(B1, 1, 1); PG8_SCHED; PG8_LDA(At, 1, 0); PG8_STAGE2(PG8_SA(0, 1), a2 + hstepA, x10, x11);
;             PG8_WAIT_V(8); PG8_WAIT_L(0); PG8_BAR; PG8_MMA(0, 0, At, B0); PG8_MMA(0, 1, At, B1); PG8_BAR; PG8_SCHED;
;             PG8_LDA(At, 1, 1); PG8_STAGE(PG8_SB(1, 0), b3, voffB); PG8_STAGE(PG8_SB(1, 1), b3 + hstep, voffB); PG8_STAGE2(PG8_SA(1, 0), a3, x00, x01);
;             PG8_WAIT_V(8); PG8_WAIT_L(0); PG8_BAR; PG8_MMA(1, 0, At, B0); PG8_MMA(1, 1, At, B1); PG8_BAR; PG8_SCHED;
	s_setprio 1
	s_waitcnt lgkmcnt(0)
	v_mfma_f32_16x16x32_bf16 v[126:129], v[144:147], v[182:185], v[126:129]
	v_mfma_f32_16x16x32_bf16 v[122:125], v[158:161], v[182:185], v[122:125]
	v_mfma_f32_16x16x32_bf16 v[110:113], v[144:147], v[190:193], v[110:113]
	v_mfma_f32_16x16x32_bf16 v[106:109], v[158:161], v[190:193], v[106:109]
	v_mfma_f32_16x16x32_bf16 v[94:97], v[144:147], v[198:201], v[94:97]
	v_mfma_f32_16x16x32_bf16 v[90:93], v[158:161], v[198:201], v[90:93]
	v_mfma_f32_16x16x32_bf16 v[78:81], v[144:147], v[206:209], v[78:81]
	v_mfma_f32_16x16x32_bf16 v[74:77], v[158:161], v[206:209], v[74:77]
	v_mfma_f32_16x16x32_bf16 v[126:129], v[148:151], v[186:189], v[126:129]
	v_mfma_f32_16x16x32_bf16 v[122:125], v[162:165], v[186:189], v[122:125]
	v_mfma_f32_16x16x32_bf16 v[110:113], v[148:151], v[194:197], v[110:113]
	v_mfma_f32_16x16x32_bf16 v[106:109], v[162:165], v[194:197], v[106:109]
	v_mfma_f32_16x16x32_bf16 v[94:97], v[148:151], v[202:205], v[94:97]
	v_mfma_f32_16x16x32_bf16 v[90:93], v[162:165], v[202:205], v[90:93]
	v_mfma_f32_16x16x32_bf16 v[78:81], v[148:151], v[210:213], v[78:81]
	v_mfma_f32_16x16x32_bf16 v[74:77], v[162:165], v[210:213], v[74:77]
	v_mfma_f32_16x16x32_bf16 v[118:121], v[166:169], v[182:185], v[118:121]
	v_mfma_f32_16x16x32_bf16 v[114:117], v[174:177], v[182:185], v[114:117]
	v_mfma_f32_16x16x32_bf16 v[102:105], v[166:169], v[190:193], v[102:105]
	v_mfma_f32_16x16x32_bf16 v[98:101], v[174:177], v[190:193], v[98:101]
	v_mfma_f32_16x16x32_bf16 v[86:89], v[166:169], v[198:201], v[86:89]
	v_mfma_f32_16x16x32_bf16 v[82:85], v[174:177], v[198:201], v[82:85]
	v_mfma_f32_16x16x32_bf16 v[70:73], v[166:169], v[206:209], v[70:73]
	v_mfma_f32_16x16x32_bf16 v[66:69], v[174:177], v[206:209], v[66:69]
	v_mfma_f32_16x16x32_bf16 v[118:121], v[170:173], v[186:189], v[118:121]
	v_mfma_f32_16x16x32_bf16 v[114:117], v[178:181], v[186:189], v[114:117]
	v_mfma_f32_16x16x32_bf16 v[102:105], v[170:173], v[194:197], v[102:105]
	v_mfma_f32_16x16x32_bf16 v[98:101], v[178:181], v[194:197], v[98:101]
	v_mfma_f32_16x16x32_bf16 v[86:89], v[170:173], v[202:205], v[86:89]
	v_mfma_f32_16x16x32_bf16 v[82:85], v[178:181], v[202:205], v[82:85]
	v_mfma_f32_16x16x32_bf16 v[70:73], v[170:173], v[210:213], v[70:73]
	v_mfma_f32_16x16x32_bf16 v[66:69], v[178:181], v[210:213], v[66:69]
	s_setprio 0
	s_barrier
	s_add_i32 s54, s48, s41
	v_lshl_add_u64 v[214:215], s[30:31], 0, v[132:133]
	s_mov_b32 m0, s54
	ds_read_b128 v[182:185], v156 offset:16384
	ds_read_b128 v[186:189], v156 offset:17408
	ds_read_b128 v[190:193], v156 offset:18432
	ds_read_b128 v[194:197], v156 offset:19456
	ds_read_b128 v[198:201], v156 offset:20480
	ds_read_b128 v[202:205], v156 offset:21504
	ds_read_b128 v[206:209], v156 offset:22528
	ds_read_b128 v[210:213], v156 offset:23552
	global_load_lds_dwordx4 v[214:215], off
	s_add_i32 m0, s54, 0x2000
	s_add_u32 s54, s30, 0x20000
	v_lshl_add_u64 v[216:217], s[30:31], 0, v[136:137]
	s_addc_u32 s55, s31, 0
	s_add_i32 s56, s49, s41
	global_load_lds_dwordx4 v[216:217], off
	v_lshl_add_u64 v[218:219], s[54:55], 0, v[132:133]
	s_mov_b32 m0, s56
	v_lshl_add_u64 v[220:221], s[34:35], 0, v[134:135]
	global_load_lds_dwordx4 v[218:219], off
	v_lshl_add_u64 v[218:219], s[54:55], 0, v[136:137]
	s_add_i32 m0, s56, 0x2000
	s_nop 0
	global_load_lds_dwordx4 v[218:219], off
	v_lshl_add_u64 v[218:219], s[34:35], 0, v[130:131]
	s_mov_b32 m0, s27
	s_nop 0
	global_load_lds_dwordx4 v[218:219], off
	s_mov_b32 m0, s42
	s_nop 0
	global_load_lds_dwordx4 v[220:221], off
	s_waitcnt vmcnt(8)
	s_waitcnt lgkmcnt(0)
	s_barrier
	s_setprio 1
	s_waitcnt lgkmcnt(0)
	v_mfma_f32_16x16x32_bf16 v[62:65], v[144:147], v[182:185], v[62:65]
	v_mfma_f32_16x16x32_bf16 v[58:61], v[158:161], v[182:185], v[58:61]
	v_mfma_f32_16x16x32_bf16 v[46:49], v[144:147], v[190:193], v[46:49]
	v_mfma_f32_16x16x32_bf16 v[42:45], v[158:161], v[190:193], v[42:45]
	v_mfma_f32_16x16x32_bf16 v[14:17], v[144:147], v[198:201], v[14:17]
	v_mfma_f32_16x16x32_bf16 v[10:13], v[158:161], v[198:201], v[10:13]
	v_mfma_f32_16x16x32_bf16 v[6:9], v[144:147], v[206:209], v[6:9]
	v_mfma_f32_16x16x32_bf16 v[2:5], v[158:161], v[206:209], v[2:5]
	v_mfma_f32_16x16x32_bf16 v[62:65], v[148:151], v[186:189], v[62:65]
	v_mfma_f32_16x16x32_bf16 v[58:61], v[162:165], v[186:189], v[58:61]
	v_mfma_f32_16x16x32_bf16 v[46:49], v[148:151], v[194:197], v[46:49]
	v_mfma_f32_16x16x32_bf16 v[42:45], v[162:165], v[194:197], v[42:45]
	v_mfma_f32_16x16x32_bf16 v[14:17], v[148:151], v[202:205], v[14:17]
	v_mfma_f32_16x16x32_bf16 v[10:13], v[162:165], v[202:205], v[10:13]
	v_mfma_f32_16x16x32_bf16 v[6:9], v[148:151], v[210:213], v[6:9]
	v_mfma_f32_16x16x32_bf16 v[2:5], v[162:165], v[210:213], v[2:5]
	v_mfma_f32_16x16x32_bf16 v[54:57], v[166:169], v[182:185], v[54:57]
	v_mfma_f32_16x16x32_bf16 v[50:53], v[174:177], v[182:185], v[50:53]
	v_mfma_f32_16x16x32_bf16 v[30:33], v[166:169], v[190:193], v[30:33]
	v_mfma_f32_16x16x32_bf16 v[26:29], v[174:177], v[190:193], v[26:29]
	v_mfma_f32_16x16x32_bf16 v[34:37], v[166:169], v[198:201], v[34:37]
	v_mfma_f32_16x16x32_bf16 v[38:41], v[174:177], v[198:201], v[38:41]
	v_mfma_f32_16x16x32_bf16 v[18:21], v[166:169], v[206:209], v[18:21]
	v_mfma_f32_16x16x32_bf16 v[22:25], v[174:177], v[206:209], v[22:25]
	v_mfma_f32_16x16x32_bf16 v[54:57], v[170:173], v[186:189], v[54:57]
	v_mfma_f32_16x16x32_bf16 v[50:53], v[178:181], v[186:189], v[50:53]
	v_mfma_f32_16x16x32_bf16 v[30:33], v[170:173], v[194:197], v[30:33]
	v_mfma_f32_16x16x32_bf16 v[26:29], v[178:181], v[194:197], v[26:29]
	v_mfma_f32_16x16x32_bf16 v[34:37], v[170:173], v[202:205], v[34:37]
	v_mfma_f32_16x16x32_bf16 v[38:41], v[178:181], v[202:205], v[38:41]
	v_mfma_f32_16x16x32_bf16 v[18:21], v[170:173], v[210:213], v[18:21]
	v_mfma_f32_16x16x32_bf16 v[22:25], v[178:181], v[210:213], v[22:25]
	s_setprio 0
	s_barrier
; #define PG8_STAGE2(bufoff, gbase, v0, v1) do { \
;         __builtin_amdgcn_global_load_lds((const unsigned*)((const char*)(gbase) + (v0)), (LAS unsigned*)(lds + (bufoff) + ldsw), 16, 0, 0); \
;         __builtin_amdgcn_global_load_lds((const unsigned*)((const char*)(gbase) + (v1)), (LAS unsigned*)(lds + (bufoff) + ldsw + 8192), 16, 0, 0); } while (0)
; #define PG8_STAGE(bufoff, gbase, voff) PG8_STAGE2(bufoff, gbase, (voff)[0], (voff)[1])
; #define PG8_LDA(dst, b, h) do { _Pragma("unroll") for (int m = 0; m < 4; ++m) _Pragma("unroll") for (int k = 0; k < 2; ++k) dst[m][k] = *(const LAS bf16x8*)(lds + PG8_SA(b, h) + aoff + m * 2048 + k * 1024); } while (0)
; #define PG8_LDB(dst, b, h) do { _Pragma("unroll") for (int n = 0; n < 2; ++n) _Pragma("unroll") for (int k = 0; k < 2; ++k) dst[n][k] = *(const LAS bf16x8*)(lds + PG8_SB(b, h) + boff + n * 2048 + k * 1024); } while (0)
; #define PG8_WAIT_V(n) asm volatile("s_waitcnt vmcnt(" #n ")" ::: "memory")
; #define PG8_WAIT_L(n) asm volatile("s_waitcnt lgkmcnt(" #n ")" ::: "memory")
; #define PG8_BAR __builtin_amdgcn_s_barrier()
; #define PG8_SCHED __builtin_amdgcn_sched_barrier(0)
; template <class Epi, class Sched, bool ALIGN_EPI, bool SP2, bool GATHER>
; DI void gemm_phase(LAS unsigned char* lds, const Gemm g, const Sched& S, const Epi& E) {
;     ...
;             PG8_LDB(B0, 0, 0); PG8_LDB(B1, 0, 1); PG8_SCHED; PG8_LDA(At, 0, 0); PG8_STAGE2(PG8_SA(1, 1), a1 + hstepA, gC[1][0], gC[1][1]);
;             PG8_WAIT_V(8); PG8_WAIT_L(0); PG8_BAR; PG8_MMA(0, 0, At, B0); PG8_MMA(0, 1, At, B1); PG8_BAR; PG8_SCHED;
;             PG8_LDA(At, 0, 1); PG8_STAGE(PG8_SB(0, 0), b2, voffB); PG8_STAGE(PG8_SB(0, 1), b2 + hstep, voffB); PG8_STAGE2(PG8_SA(0, 0), a2, x00, x01);
;             PG8_WAIT_V(8); PG8_WAIT_L(0); PG8_BAR; PG8_MMA(1, 0, At, B0); PG8_MMA(1, 1, At, B1); PG8_BAR; PG8_SCHED;
;             PG8_LDB(B0, 1, 0); PG8_LDB(B1, 1, 1); PG8_SCHED; PG8_LDA(At, 1, 0); PG8_STAGE2(PG8_SA(0, 1), a2 + hstepA, x10, x11);
;             PG8_WAIT_V(8); PG8_WAIT_L(0); PG8_BAR; PG8_MMA(0, 0, At, B0); PG8_MMA(0, 1, At, B1); PG8_BAR; PG8_SCHED;
;             PG8_LDA(At, 1, 1); PG8_STAGE(PG8_SB(1, 0), b3, voffB); PG8_STAGE(PG8_SB(1, 1), b3 + hstep, voffB); PG8_STAGE2(PG8_SA(1, 0), a3, x00, x01);
;             PG8_WAIT_V(8); PG8_WAIT_L(0); PG8_BAR; PG8_MMA(1, 0, At, B0); PG8_MMA(1, 1, At, B1); PG8_BAR; PG8_SCHED;
	s_add_i32 s54, 0, 0x18000
	v_add_u32_e32 v138, s54, v152
	s_add_i32 s55, 0, 0x1c000
	ds_read_b128 v[144:147], v138
	ds_read_b128 v[148:151], v138 offset:1024
	ds_read_b128 v[158:161], v138 offset:2048
	ds_read_b128 v[162:165], v138 offset:3072
	v_add_u32_e32 v138, s55, v152
	ds_read_b128 v[166:169], v138
	ds_read_b128 v[170:173], v138 offset:1024
	ds_read_b128 v[174:177], v138 offset:2048
	ds_read_b128 v[178:181], v138 offset:3072
	s_add_u32 s34, s34, 0x20000
	s_addc_u32 s35, s35, 0
	s_mov_b32 m0, s43
	v_lshl_add_u64 v[222:223], s[34:35], 0, v[130:131]
	ds_read_b128 v[182:185], v156 offset:32768
	ds_read_b128 v[186:189], v156 offset:33792
	ds_read_b128 v[190:193], v156 offset:34816
	ds_read_b128 v[194:197], v156 offset:35840
	ds_read_b128 v[198:201], v156 offset:36864
	ds_read_b128 v[202:205], v156 offset:37888
	ds_read_b128 v[206:209], v156 offset:38912
	ds_read_b128 v[210:213], v156 offset:39936
	global_load_lds_dwordx4 v[222:223], off
	v_lshl_add_u64 v[222:223], s[34:35], 0, v[134:135]
	s_mov_b32 m0, s44
	s_nop 0
	global_load_lds_dwordx4 v[222:223], off
	s_waitcnt vmcnt(8)
	s_waitcnt lgkmcnt(0)
	s_barrier
	s_setprio 1
	s_waitcnt lgkmcnt(0)
	v_mfma_f32_16x16x32_bf16 v[126:129], v[144:147], v[182:185], v[126:129]
	v_mfma_f32_16x16x32_bf16 v[122:125], v[158:161], v[182:185], v[122:125]
	v_mfma_f32_16x16x32_bf16 v[110:113], v[144:147], v[190:193], v[110:113]
	v_mfma_f32_16x16x32_bf16 v[106:109], v[158:161], v[190:193], v[106:109]
	v_mfma_f32_16x16x32_bf16 v[94:97], v[144:147], v[198:201], v[94:97]
	v_mfma_f32_16x16x32_bf16 v[90:93], v[158:161], v[198:201], v[90:93]
	v_mfma_f32_16x16x32_bf16 v[78:81], v[144:147], v[206:209], v[78:81]
	v_mfma_f32_16x16x32_bf16 v[74:77], v[158:161], v[206:209], v[74:77]
	v_mfma_f32_16x16x32_bf16 v[126:129], v[148:151], v[186:189], v[126:129]
	v_mfma_f32_16x16x32_bf16 v[122:125], v[162:165], v[186:189], v[122:125]
	v_mfma_f32_16x16x32_bf16 v[110:113], v[148:151], v[194:197], v[110:113]
	v_mfma_f32_16x16x32_bf16 v[106:109], v[162:165], v[194:197], v[106:109]
	v_mfma_f32_16x16x32_bf16 v[94:97], v[148:151], v[202:205], v[94:97]
	v_mfma_f32_16x16x32_bf16 v[90:93], v[162:165], v[202:205], v[90:93]
	v_mfma_f32_16x16x32_bf16 v[78:81], v[148:151], v[210:213], v[78:81]
	v_mfma_f32_16x16x32_bf16 v[74:77], v[162:165], v[210:213], v[74:77]
	v_mfma_f32_16x16x32_bf16 v[118:121], v[166:169], v[182:185], v[118:121]
	v_mfma_f32_16x16x32_bf16 v[114:117], v[174:177], v[182:185], v[114:117]
	v_mfma_f32_16x16x32_bf16 v[102:105], v[166:169], v[190:193], v[102:105]
	v_mfma_f32_16x16x32_bf16 v[98:101], v[174:177], v[190:193], v[98:101]
	v_mfma_f32_16x16x32_bf16 v[86:89], v[166:169], v[198:201], v[86:89]
	v_mfma_f32_16x16x32_bf16 v[82:85], v[174:177], v[198:201], v[82:85]
	v_mfma_f32_16x16x32_bf16 v[70:73], v[166:169], v[206:209], v[70:73]
	v_mfma_f32_16x16x32_bf16 v[66:69], v[174:177], v[206:209], v[66:69]
	v_mfma_f32_16x16x32_bf16 v[118:121], v[170:173], v[186:189], v[118:121]
	v_mfma_f32_16x16x32_bf16 v[114:117], v[178:181], v[186:189], v[114:117]
	v_mfma_f32_16x16x32_bf16 v[102:105], v[170:173], v[194:197], v[102:105]
	v_mfma_f32_16x16x32_bf16 v[98:101], v[178:181], v[194:197], v[98:101]
	v_mfma_f32_16x16x32_bf16 v[86:89], v[170:173], v[202:205], v[86:89]
	v_mfma_f32_16x16x32_bf16 v[82:85], v[178:181], v[202:205], v[82:85]
	v_mfma_f32_16x16x32_bf16 v[70:73], v[170:173], v[210:213], v[70:73]
	v_mfma_f32_16x16x32_bf16 v[66:69], v[178:181], v[210:213], v[66:69]
	s_setprio 0
	s_barrier
; #define PG8_STAGE2(bufoff, gbase, v0, v1) do { \
;         __builtin_amdgcn_global_load_lds((const unsigned*)((const char*)(gbase) + (v0)), (LAS unsigned*)(lds + (bufoff) + ldsw), 16, 0, 0); \
;         __builtin_amdgcn_global_load_lds((const unsigned*)((const char*)(gbase) + (v1)), (LAS unsigned*)(lds + (bufoff) + ldsw + 8192), 16, 0, 0); } while (0)
; #define PG8_STAGE(bufoff, gbase, voff) PG8_STAGE2(bufoff, gbase, (voff)[0], (voff)[1])
; #define PG8_BAR __builtin_amdgcn_s_barrier()
; template <class Epi, class Sched, bool ALIGN_EPI, bool SP2, bool GATHER>
; DI void gemm_phase(LAS unsigned char* lds, const Gemm g, const Sched& S, const Epi& E) {
;     ...
;         for (int t = 0; t < nt; t += 2) {
;             if constexpr (Epi::MID_T >= 0) { if (t == Epi::MID_T) { E.mid(acc, cur, wr, wc, fr, fq); PG8_SCHED; } }
;             const bool last = (t == nt - 2);
;             const char* a1 = cA + (size_t)(t + 1) * kstep;
;             const char* a2 = last ? nA : cA + (size_t)(t + 2) * kstep; const char* b2 = last ? nB : cB + (size_t)(t + 2) * kstep;
;             const char* a3 = a2 + kstep; const char* b3 = b2 + kstep;
;             unsigned x00 = gC[0][0], x01 = gC[0][1], x10 = gC[1][0], x11 = gC[1][1];
;             if constexpr (GATHER) { if (last) { x00 = gN[0][0]; x01 = gN[0][1]; x10 = gN[1][0]; x11 = gN[1][1]; } }
;             PG8_LDB(B0, 0, 0); PG8_LDB(B1, 0, 1); PG8_SCHED; PG8_LDA(At, 0, 0); PG8_STAGE2(PG8_SA(1, 1), a1 + hstepA, gC[1][0], gC[1][1]);
;             PG8_WAIT_V(8); PG8_WAIT_L(0); PG8_BAR; PG8_MMA(0, 0, At, B0); PG8_MMA(0, 1, At, B1); PG8_BAR; PG8_SCHED;
;             PG8_LDA(At, 0, 1); PG8_STAGE(PG8_SB(0, 0), b2, voffB); PG8_STAGE(PG8_SB(0, 1), b2 + hstep, voffB); PG8_STAGE2(PG8_SA(0, 0), a2, x00, x01);
;             PG8_WAIT_V(8); PG8_WAIT_L(0); PG8_BAR; PG8_MMA(1, 0, At, B0); PG8_MMA(1, 1, At, B1); PG8_BAR; PG8_SCHED;
;             PG8_LDB(B0, 1, 0); PG8_LDB(B1, 1, 1); PG8_SCHED; PG8_LDA(At, 1, 0); PG8_STAGE2(PG8_SA(0, 1), a2 + hstepA, x10, x11);
;             PG8_WAIT_V(8); PG8_WAIT_L(0); PG8_BAR; PG8_MMA(0, 0, At, B0); PG8_MMA(0, 1, At, B1); PG8_BAR; PG8_SCHED;
;             PG8_LDA(At, 1, 1); PG8_STAGE(PG8_SB(1, 0), b3, voffB); PG8_STAGE(PG8_SB(1, 1), b3 + hstep, voffB); PG8_STAGE2(PG8_SA(1, 0), a3, x00, x01);
;             PG8_WAIT_V(8); PG8_WAIT_L(0); PG8_BAR; PG8_MMA(1, 0, At, B0); PG8_MMA(1, 1, At, B1); PG8_BAR; PG8_SCHED;
	s_add_i32 s34, s54, s41
	v_lshl_add_u64 v[214:215], v[214:215], 0, s[10:11]
	s_mov_b32 m0, s34
	ds_read_b128 v[182:185], v156 offset:49152
	ds_read_b128 v[186:189], v156 offset:50176
	ds_read_b128 v[190:193], v156 offset:51200
	ds_read_b128 v[194:197], v156 offset:52224
	ds_read_b128 v[198:201], v156 offset:53248
	ds_read_b128 v[202:205], v156 offset:54272
	ds_read_b128 v[206:209], v156 offset:55296
	ds_read_b128 v[210:213], v156 offset:56320
	global_load_lds_dwordx4 v[214:215], off
	s_add_i32 m0, s34, 0x2000
	s_add_u32 s30, s30, 0x20080
	v_lshl_add_u64 v[214:215], v[216:217], 0, s[10:11]
	s_addc_u32 s31, s31, 0
	s_add_i32 s34, s55, s41
	global_load_lds_dwordx4 v[214:215], off
	v_lshl_add_u64 v[214:215], s[30:31], 0, v[132:133]
	s_mov_b32 m0, s34
	s_nop 0
	global_load_lds_dwordx4 v[214:215], off
	v_lshl_add_u64 v[214:215], s[30:31], 0, v[136:137]
	s_add_i32 m0, s34, 0x2000
	s_nop 0
	global_load_lds_dwordx4 v[214:215], off
	v_lshl_add_u64 v[214:215], v[218:219], 0, s[10:11]
	s_mov_b32 m0, s46
	s_nop 0
	global_load_lds_dwordx4 v[214:215], off
	v_lshl_add_u64 v[214:215], v[220:221], 0, s[10:11]
	s_mov_b32 m0, s47
	s_nop 0
	global_load_lds_dwordx4 v[214:215], off
	s_waitcnt vmcnt(8)
	s_waitcnt lgkmcnt(0)
	s_barrier
	s_setprio 1
	s_waitcnt lgkmcnt(0)
	v_mfma_f32_16x16x32_bf16 v[62:65], v[144:147], v[182:185], v[62:65]
	v_mfma_f32_16x16x32_bf16 v[58:61], v[158:161], v[182:185], v[58:61]
	v_mfma_f32_16x16x32_bf16 v[46:49], v[144:147], v[190:193], v[46:49]
	v_mfma_f32_16x16x32_bf16 v[42:45], v[158:161], v[190:193], v[42:45]
	v_mfma_f32_16x16x32_bf16 v[14:17], v[144:147], v[198:201], v[14:17]
	v_mfma_f32_16x16x32_bf16 v[10:13], v[158:161], v[198:201], v[10:13]
	v_mfma_f32_16x16x32_bf16 v[6:9], v[144:147], v[206:209], v[6:9]
	v_mfma_f32_16x16x32_bf16 v[2:5], v[158:161], v[206:209], v[2:5]
	v_mfma_f32_16x16x32_bf16 v[62:65], v[148:151], v[186:189], v[62:65]
	v_mfma_f32_16x16x32_bf16 v[58:61], v[162:165], v[186:189], v[58:61]
	v_mfma_f32_16x16x32_bf16 v[46:49], v[148:151], v[194:197], v[46:49]
	v_mfma_f32_16x16x32_bf16 v[42:45], v[162:165], v[194:197], v[42:45]
	v_mfma_f32_16x16x32_bf16 v[14:17], v[148:151], v[202:205], v[14:17]
	v_mfma_f32_16x16x32_bf16 v[10:13], v[162:165], v[202:205], v[10:13]
	v_mfma_f32_16x16x32_bf16 v[6:9], v[148:151], v[210:213], v[6:9]
	v_mfma_f32_16x16x32_bf16 v[2:5], v[162:165], v[210:213], v[2:5]
	v_mfma_f32_16x16x32_bf16 v[54:57], v[166:169], v[182:185], v[54:57]
	v_mfma_f32_16x16x32_bf16 v[50:53], v[174:177], v[182:185], v[50:53]
	v_mfma_f32_16x16x32_bf16 v[30:33], v[166:169], v[190:193], v[30:33]
	v_mfma_f32_16x16x32_bf16 v[26:29], v[174:177], v[190:193], v[26:29]
	v_mfma_f32_16x16x32_bf16 v[34:37], v[166:169], v[198:201], v[34:37]
	v_mfma_f32_16x16x32_bf16 v[38:41], v[174:177], v[198:201], v[38:41]
	v_mfma_f32_16x16x32_bf16 v[18:21], v[166:169], v[206:209], v[18:21]
	v_mfma_f32_16x16x32_bf16 v[22:25], v[174:177], v[206:209], v[22:25]
	v_mfma_f32_16x16x32_bf16 v[54:57], v[170:173], v[186:189], v[54:57]
	v_mfma_f32_16x16x32_bf16 v[50:53], v[178:181], v[186:189], v[50:53]
	v_mfma_f32_16x16x32_bf16 v[30:33], v[170:173], v[194:197], v[30:33]
	v_mfma_f32_16x16x32_bf16 v[26:29], v[178:181], v[194:197], v[26:29]
	v_mfma_f32_16x16x32_bf16 v[34:37], v[170:173], v[202:205], v[34:37]
	v_mfma_f32_16x16x32_bf16 v[38:41], v[178:181], v[202:205], v[38:41]
	v_mfma_f32_16x16x32_bf16 v[18:21], v[170:173], v[210:213], v[18:21]
	v_mfma_f32_16x16x32_bf16 v[22:25], v[178:181], v[210:213], v[22:25]
	s_setprio 0
	s_barrier
	s_add_i32 s53, s53, 2
	s_add_u32 s28, s28, 0x100
	s_addc_u32 s29, s29, 0
	s_add_u32 s51, s51, 0x100
	s_addc_u32 s52, s52, 0
	s_cmp_gt_u32 s53, 5
	s_cbranch_scc0 .LBB0_996
